# speedup vs baseline: 1.0127x; 1.0063x over previous
.LBB1_26:
	s_waitcnt vmcnt(35)
	v_and_b32_e32 v113, 3, v0
	s_and_b32 s18, s2, 15
	v_cmp_eq_u32_e32 vcc, 0, v113
	v_cmp_gt_u32_e64 s[4:5], 12, v92
	s_and_b64 s[12:13], vcc, s[4:5]
	s_lshl_b32 s4, s3, 12
	s_lshl_b32 s5, s18, 8
	s_or_b32 s4, s4, s5
	s_mul_hi_i32 s5, s4, 0x6000
	s_mulk_i32 s4, 0x6000
	s_lshl_b32 s3, s3, 8
	s_add_u32 s16, s24, s4
	s_addc_u32 s17, s25, s5
	s_ashr_i32 s4, s21, 31
	s_lshr_b32 s4, s4, 29
	s_add_i32 s4, s21, s4
	s_ashr_i32 s19, s4, 3
	v_and_b32_e32 v101, 1, v74
	v_lshl_or_b32 v74, v91, 1, v95
	s_min_i32 s4, s19, 0xff
	v_mul_u32_u24_e32 v74, 0x60, v74
	v_lshlrev_b32_e32 v75, 1, v92
	s_mul_hi_i32 s5, s4, 0x6000
	s_mulk_i32 s4, 0x6000
	v_or3_b32 v88, v74, v75, v101
	s_add_u32 s4, s16, s4
	s_addc_u32 s5, s17, s5
	v_lshlrev_b64 v[102:103], 4, v[88:89]
	v_lshl_add_u64 v[104:105], s[4:5], 0, v[102:103]
	global_load_dwordx4 v[82:85], v[104:105], off
	global_load_dwordx4 v[74:77], v[104:105], off offset:512
	global_load_dwordx4 v[78:81], v[104:105], off offset:1024
	s_waitcnt vmcnt(5)
	v_mul_f32_e32 v88, 0xbfb8aa3b, v97
	v_mul_f32_e32 v99, 0x3c91a2b4, v88
	s_waitcnt vmcnt(4)
	v_mul_f32_e32 v88, 0x4038aa3b, v96
	v_mul_f32_e32 v104, 0x3c91a2b4, v88
	v_lshrrev_b32_e32 v88, 2, v92
	v_and_b32_e32 v92, 4, v92
	v_cmp_lt_u32_e64 s[4:5], 1, v93
	v_mov_b32_e32 v93, 0xd0
	v_cmp_ne_u32_e32 vcc, 0, v92
	v_lshlrev_b32_e32 v107, 3, v88
	v_sub_u32_e32 v88, 0, v107
	v_cndmask_b32_e32 v92, 0, v93, vcc
	v_add_u32_e32 v106, v92, v86
	v_and_b32_e32 v92, 12, v0
	v_mul_u32_u24_e32 v86, 0xd0, v101
	v_mad_u32_u24 v91, v91, 24, v92
	v_mul_u32_u24_e32 v93, 12, v95
	v_lshlrev_b32_e32 v92, 20, v101
	v_add3_u32 v112, v91, v86, v93
	v_lshl_or_b32 v86, s18, 21, v90
	v_add3_u32 v86, v86, s3, v92
	v_mul_f32_e32 v1, 0xbfb8aa3b, v1
	v_and_b32_e32 v114, 24, v88
	v_or_b32_e32 v88, v86, v94
	s_min_i32 s3, s19, 0xfe
	v_mul_f32_e32 v1, 0x3c91a2b4, v1
	s_waitcnt vmcnt(3)
	v_mul_f32_e32 v105, 0x4038aa3b, v100
	v_add_u32_e32 v108, 16, v106
	v_add_u32_e32 v109, 0x70, v106
	v_add_u32_e32 v110, 0x1b0, v106
	v_add_u32_e32 v111, 0x210, v106
	v_mul_u32_u24_e32 v113, 6, v113
	s_add_i32 s19, s3, 1
	v_lshl_add_u64 v[100:101], s[16:17], 0, v[102:103]
	v_lshl_add_u64 v[102:103], v[88:89], 1, s[14:15]
	s_sub_i32 s3, 0x7ff, s21
	v_mov_b32_e32 v115, 0x7f7f7f7f
	s_mov_b32 s16, 0x42700000
	s_mov_b32 s17, 0x41f00000
	s_mov_b32 s18, 0x41700000
	v_mov_b32_e32 v116, 0x6000
	v_mov_b32_e32 v117, 0x4b400000
	v_mov_b32_e32 v118, 0x4b400008
	v_mov_b32_e32 v119, 0x4b400010
	v_mbcnt_lo_u32_b32 v200, -1, 0
	v_mbcnt_hi_u32_b32 v200, -1, v200
	v_and_b32_e32 v201, 3, v200
	v_and_b32_e32 v202, 15, v200
	v_cmp_gt_u32_e32 vcc, 8, v202
	s_nop 1
	v_cndmask_b32_e64 v178, 0, v115, vcc
	v_cndmask_b32_e64 v179, v115, 0, vcc
	v_lshlrev_b32_e32 v181, 1, v201
	v_sub_u32_e32 v202, 6, v181
	v_lshlrev_b32_e64 v180, v202, 1
	v_lshrrev_b32_e32 v202, 3, v107
	v_sub_u32_e32 v184, v112, v202
	v_add_u32_e32 v184, v184, v201
	v_add_u32_e32 v202, 0xc0, v202
	v_cmp_eq_u32_e32 vcc, 3, v201
	s_nop 1
	v_cndmask_b32_e32 v184, v184, v202, vcc
	v_subrev_u32_e32 v185, s14, v102
	s_mov_b32 s44, s21
	s_mov_b32 s45, s22
	s_lshr_b32 s46, s44, 3
	s_add_i32 s46, s46, 1
	s_mul_i32 s46, s46, 0x6000
	s_mov_b32 s47, 0
	v_lshl_add_u64 v[196:197], v[100:101], 0, s[46:47]
	s_mov_b32 s42, 0x6000
	s_mov_b32 s43, 0
	s_sub_i32 s46, s44, 1
	s_sub_i32 s47, 0x800, s44
	s_and_b64 s[40:41], s[6:7], exec
	s_cselect_b32 s46, s46, s47
	s_cselect_b32 s41, 0, -1
	s_xor_b32 s40, s41, 0x400
	s_sub_i32 s40, s40, s41
	s_ashr_i32 s47, s46, 31
	s_lshl_b64 s[46:47], s[46:47], 10
	s_add_u32 s48, s14, s46
	s_addc_u32 s49, s15, s47
	v_readfirstlane_b32 s51, v112
	s_waitcnt vmcnt(0) lgkmcnt(0)
	v_mov_b32_e32 v176, v87
	v_rcp_f32_e32 v186, v104
	s_nop 1
	v_mul_f32_e32 v188, v105, v186
	v_mov_b32_e32 v189, 0
	v_mov_b32_e32 v190, 0
	v_mov_b32_e32 v191, 0
	s_nop 1
	s_cmp_lt_i32 s44, s45
	s_cbranch_scc0 .Lscan_exit_st
	ds_read_b64 v[122:123], v106 offset:0
	ds_read_b64 v[124:125], v106 offset:8
	ds_read_b64 v[126:127], v106 offset:16
	s_waitcnt lgkmcnt(0)
	s_cmp_lt_u32 s51, 96
	s_cbranch_scc0 .Lscan_loop_b_st
.Lscan_loop_a_st:
	ds_read_b64 v[128:129], v106 offset:96
	ds_read_b64 v[130:131], v106 offset:104
	ds_read_b64 v[132:133], v106 offset:112
	s_waitcnt vmcnt(8)
	global_load_dwordx4 v[146:149], v[196:197], off
	global_load_dwordx4 v[150:153], v[196:197], off offset:512
	global_load_dwordx4 v[154:157], v[196:197], off offset:1024
	v_lshl_add_u64 v[196:197], v[196:197], 0, s[42:43]
	s_waitcnt lgkmcnt(3)
	v_mfma_scale_f32_16x16x128_f8f6f4 v[134:137], v[122:127], v[2:7], 0, v178, v115 op_sel_hi:[0,0,0] cbsz:2 blgp:2
	v_mfma_scale_f32_16x16x128_f8f6f4 v[138:141], v[122:127], v[14:19], 0, v178, v115 op_sel_hi:[0,0,0] cbsz:2 blgp:2
	v_mfma_scale_f32_16x16x128_f8f6f4 v[142:145], v[122:127], v[26:31], v[188:191], v178, v115 op_sel_hi:[0,0,0] cbsz:2 blgp:2
	v_mfma_scale_f32_16x16x128_f8f6f4 v[134:137], v[122:127], v[38:43], v[134:137], v179, v115 op_sel_hi:[0,0,0] cbsz:2 blgp:2
	v_mfma_scale_f32_16x16x128_f8f6f4 v[138:141], v[122:127], v[50:55], v[138:141], v179, v115 op_sel_hi:[0,0,0] cbsz:2 blgp:2
	v_mfma_scale_f32_16x16x128_f8f6f4 v[142:145], v[122:127], v[62:67], v[142:145], v179, v115 op_sel_hi:[0,0,0] cbsz:2 blgp:2
	s_waitcnt lgkmcnt(0)
	v_mfma_scale_f32_16x16x128_f8f6f4 v[134:137], v[128:133], v[8:13], v[134:137], v178, v115 op_sel_hi:[0,0,0] cbsz:2 blgp:2
	v_mfma_scale_f32_16x16x128_f8f6f4 v[134:137], v[128:133], v[44:49], v[134:137], v179, v115 op_sel_hi:[0,0,0] cbsz:2 blgp:2
	v_mfma_scale_f32_16x16x128_f8f6f4 v[138:141], v[128:133], v[20:25], v[138:141], v178, v115 op_sel_hi:[0,0,0] cbsz:2 blgp:2
	v_mfma_scale_f32_16x16x128_f8f6f4 v[138:141], v[128:133], v[56:61], v[138:141], v179, v115 op_sel_hi:[0,0,0] cbsz:2 blgp:2
	v_mfma_scale_f32_16x16x128_f8f6f4 v[142:145], v[128:133], v[32:37], v[142:145], v178, v115 op_sel_hi:[0,0,0] cbsz:2 blgp:2
	v_mfma_scale_f32_16x16x128_f8f6f4 v[142:145], v[128:133], v[68:73], v[142:145], v179, v115 op_sel_hi:[0,0,0] cbsz:2 blgp:2
	v_fma_mix_f32 v158, v134, v1, v82 op_sel_hi:[0,0,1]
	v_exp_f32_e32 v158, v158
	v_fma_mix_f32 v159, v138, v99, v74 op_sel_hi:[0,0,1]
	v_exp_f32_e32 v159, v159
	v_fma_f32 v158, v158, v186, v186
	v_rcp_f32_e32 v158, v158
	v_add_f32_e32 v159, 1.0, v159
	v_rcp_f32_e32 v159, v159
	s_nop 0
	v_fma_mix_f32 v161, v158, v142, v78 op_sel_hi:[0,0,1]
	v_exp_f32_e32 v161, v161
	s_add_u32 s48, s48, s40
	v_add_f32_e32 v161, 1.0, v161
	v_rcp_f32_e32 v161, v161
	s_addc_u32 s49, s49, s41
	v_fma_f32 v162, v161, -2.0, 1.0
	v_sub_f32_e32 v163, v176, v162
	v_fma_f32 v176, v159, v163, v162
	v_fma_f32 v164, |v176|, s16, v117
	v_fma_f32 v165, |v176|, s17, v118
	v_fma_f32 v166, |v176|, s18, v119
	v_lshrrev_b32_e32 v167, 26, v176
	v_min3_u32 v164, v164, v165, v166
	v_bfi_b32 v168, 31, v164, v167
	v_lshrrev_b32_e32 v169, v181, v168
	global_store_short_d16_hi v185, v176, s[48:49]
	v_mul_u32_u24_dpp v170, v168, v180 quad_perm:[1,2,3,3] row_mask:0xf bank_mask:0xf bound_ctrl:1
	v_or_b32_e32 v171, v169, v170
	ds_write_b8 v184, v171 offset:416
	s_waitcnt lgkmcnt(0)
	s_barrier
	ds_read_b64 v[122:123], v106 offset:416
	ds_read_b64 v[124:125], v106 offset:424
	ds_read_b64 v[126:127], v106 offset:432
	s_barrier
	ds_read_b64 v[128:129], v106 offset:512
	ds_read_b64 v[130:131], v106 offset:520
	ds_read_b64 v[132:133], v106 offset:528
	s_waitcnt lgkmcnt(3)
	v_mfma_scale_f32_16x16x128_f8f6f4 v[134:137], v[122:127], v[2:7], 0, v178, v115 op_sel_hi:[0,0,0] cbsz:2 blgp:2
	v_mfma_scale_f32_16x16x128_f8f6f4 v[138:141], v[122:127], v[14:19], 0, v178, v115 op_sel_hi:[0,0,0] cbsz:2 blgp:2
	v_mfma_scale_f32_16x16x128_f8f6f4 v[142:145], v[122:127], v[26:31], v[188:191], v178, v115 op_sel_hi:[0,0,0] cbsz:2 blgp:2
	v_mfma_scale_f32_16x16x128_f8f6f4 v[134:137], v[122:127], v[38:43], v[134:137], v179, v115 op_sel_hi:[0,0,0] cbsz:2 blgp:2
	v_mfma_scale_f32_16x16x128_f8f6f4 v[138:141], v[122:127], v[50:55], v[138:141], v179, v115 op_sel_hi:[0,0,0] cbsz:2 blgp:2
	v_mfma_scale_f32_16x16x128_f8f6f4 v[142:145], v[122:127], v[62:67], v[142:145], v179, v115 op_sel_hi:[0,0,0] cbsz:2 blgp:2
	s_waitcnt lgkmcnt(0)
	v_mfma_scale_f32_16x16x128_f8f6f4 v[134:137], v[128:133], v[8:13], v[134:137], v178, v115 op_sel_hi:[0,0,0] cbsz:2 blgp:2
	v_mfma_scale_f32_16x16x128_f8f6f4 v[134:137], v[128:133], v[44:49], v[134:137], v179, v115 op_sel_hi:[0,0,0] cbsz:2 blgp:2
	v_mfma_scale_f32_16x16x128_f8f6f4 v[138:141], v[128:133], v[20:25], v[138:141], v178, v115 op_sel_hi:[0,0,0] cbsz:2 blgp:2
	v_mfma_scale_f32_16x16x128_f8f6f4 v[138:141], v[128:133], v[56:61], v[138:141], v179, v115 op_sel_hi:[0,0,0] cbsz:2 blgp:2
	v_mfma_scale_f32_16x16x128_f8f6f4 v[142:145], v[128:133], v[32:37], v[142:145], v178, v115 op_sel_hi:[0,0,0] cbsz:2 blgp:2
	v_mfma_scale_f32_16x16x128_f8f6f4 v[142:145], v[128:133], v[68:73], v[142:145], v179, v115 op_sel_hi:[0,0,0] cbsz:2 blgp:2
	v_fma_mix_f32 v158, v134, v1, v82 op_sel:[0,0,1] op_sel_hi:[0,0,1]
	v_exp_f32_e32 v158, v158
	v_fma_mix_f32 v159, v138, v99, v74 op_sel:[0,0,1] op_sel_hi:[0,0,1]
	v_exp_f32_e32 v159, v159
	v_fma_f32 v158, v158, v186, v186
	v_rcp_f32_e32 v158, v158
	v_add_f32_e32 v159, 1.0, v159
	v_rcp_f32_e32 v159, v159
	s_nop 0
	v_fma_mix_f32 v161, v158, v142, v78 op_sel:[0,0,1] op_sel_hi:[0,0,1]
	v_exp_f32_e32 v161, v161
	s_add_u32 s48, s48, s40
	v_add_f32_e32 v161, 1.0, v161
	v_rcp_f32_e32 v161, v161
	s_addc_u32 s49, s49, s41
	v_fma_f32 v162, v161, -2.0, 1.0
	v_sub_f32_e32 v163, v176, v162
	v_fma_f32 v176, v159, v163, v162
	v_fma_f32 v164, |v176|, s16, v117
	v_fma_f32 v165, |v176|, s17, v118
	v_fma_f32 v166, |v176|, s18, v119
	v_lshrrev_b32_e32 v167, 26, v176
	v_min3_u32 v164, v164, v165, v166
	v_bfi_b32 v168, 31, v164, v167
	v_lshrrev_b32_e32 v169, v181, v168
	global_store_short_d16_hi v185, v176, s[48:49]
	v_mul_u32_u24_dpp v170, v168, v180 quad_perm:[1,2,3,3] row_mask:0xf bank_mask:0xf bound_ctrl:1
	v_or_b32_e32 v171, v169, v170
	ds_write_b8 v184, v171
	s_waitcnt lgkmcnt(0)
	s_barrier
	ds_read_b64 v[122:123], v106 offset:0
	ds_read_b64 v[124:125], v106 offset:8
	ds_read_b64 v[126:127], v106 offset:16
	s_barrier
	ds_read_b64 v[128:129], v106 offset:96
	ds_read_b64 v[130:131], v106 offset:104
	ds_read_b64 v[132:133], v106 offset:112
	s_waitcnt lgkmcnt(3)
	v_mfma_scale_f32_16x16x128_f8f6f4 v[134:137], v[122:127], v[2:7], 0, v178, v115 op_sel_hi:[0,0,0] cbsz:2 blgp:2
	v_mfma_scale_f32_16x16x128_f8f6f4 v[138:141], v[122:127], v[14:19], 0, v178, v115 op_sel_hi:[0,0,0] cbsz:2 blgp:2
	v_mfma_scale_f32_16x16x128_f8f6f4 v[142:145], v[122:127], v[26:31], v[188:191], v178, v115 op_sel_hi:[0,0,0] cbsz:2 blgp:2
	v_mfma_scale_f32_16x16x128_f8f6f4 v[134:137], v[122:127], v[38:43], v[134:137], v179, v115 op_sel_hi:[0,0,0] cbsz:2 blgp:2
	v_mfma_scale_f32_16x16x128_f8f6f4 v[138:141], v[122:127], v[50:55], v[138:141], v179, v115 op_sel_hi:[0,0,0] cbsz:2 blgp:2
	v_mfma_scale_f32_16x16x128_f8f6f4 v[142:145], v[122:127], v[62:67], v[142:145], v179, v115 op_sel_hi:[0,0,0] cbsz:2 blgp:2
	s_waitcnt lgkmcnt(0)
	v_mfma_scale_f32_16x16x128_f8f6f4 v[134:137], v[128:133], v[8:13], v[134:137], v178, v115 op_sel_hi:[0,0,0] cbsz:2 blgp:2
	v_mfma_scale_f32_16x16x128_f8f6f4 v[134:137], v[128:133], v[44:49], v[134:137], v179, v115 op_sel_hi:[0,0,0] cbsz:2 blgp:2
	v_mfma_scale_f32_16x16x128_f8f6f4 v[138:141], v[128:133], v[20:25], v[138:141], v178, v115 op_sel_hi:[0,0,0] cbsz:2 blgp:2
	v_mfma_scale_f32_16x16x128_f8f6f4 v[138:141], v[128:133], v[56:61], v[138:141], v179, v115 op_sel_hi:[0,0,0] cbsz:2 blgp:2
	v_mfma_scale_f32_16x16x128_f8f6f4 v[142:145], v[128:133], v[32:37], v[142:145], v178, v115 op_sel_hi:[0,0,0] cbsz:2 blgp:2
	v_mfma_scale_f32_16x16x128_f8f6f4 v[142:145], v[128:133], v[68:73], v[142:145], v179, v115 op_sel_hi:[0,0,0] cbsz:2 blgp:2
	v_fma_mix_f32 v158, v134, v1, v83 op_sel_hi:[0,0,1]
	v_exp_f32_e32 v158, v158
	v_fma_mix_f32 v159, v138, v99, v75 op_sel_hi:[0,0,1]
	v_exp_f32_e32 v159, v159
	v_fma_f32 v158, v158, v186, v186
	v_rcp_f32_e32 v158, v158
	v_add_f32_e32 v159, 1.0, v159
	v_rcp_f32_e32 v159, v159
	s_nop 0
	v_fma_mix_f32 v161, v158, v142, v79 op_sel_hi:[0,0,1]
	v_exp_f32_e32 v161, v161
	s_add_u32 s48, s48, s40
	v_add_f32_e32 v161, 1.0, v161
	v_rcp_f32_e32 v161, v161
	s_addc_u32 s49, s49, s41
	v_fma_f32 v162, v161, -2.0, 1.0
	v_sub_f32_e32 v163, v176, v162
	v_fma_f32 v176, v159, v163, v162
	v_fma_f32 v164, |v176|, s16, v117
	v_fma_f32 v165, |v176|, s17, v118
	v_fma_f32 v166, |v176|, s18, v119
	v_lshrrev_b32_e32 v167, 26, v176
	v_min3_u32 v164, v164, v165, v166
	v_bfi_b32 v168, 31, v164, v167
	v_lshrrev_b32_e32 v169, v181, v168
	global_store_short_d16_hi v185, v176, s[48:49]
	v_mul_u32_u24_dpp v170, v168, v180 quad_perm:[1,2,3,3] row_mask:0xf bank_mask:0xf bound_ctrl:1
	v_or_b32_e32 v171, v169, v170
	ds_write_b8 v184, v171 offset:416
	s_waitcnt lgkmcnt(0)
	s_barrier
	ds_read_b64 v[122:123], v106 offset:416
	ds_read_b64 v[124:125], v106 offset:424
	ds_read_b64 v[126:127], v106 offset:432
	s_barrier
	ds_read_b64 v[128:129], v106 offset:512
	ds_read_b64 v[130:131], v106 offset:520
	ds_read_b64 v[132:133], v106 offset:528
	s_waitcnt lgkmcnt(3)
	v_mfma_scale_f32_16x16x128_f8f6f4 v[134:137], v[122:127], v[2:7], 0, v178, v115 op_sel_hi:[0,0,0] cbsz:2 blgp:2
	v_mfma_scale_f32_16x16x128_f8f6f4 v[138:141], v[122:127], v[14:19], 0, v178, v115 op_sel_hi:[0,0,0] cbsz:2 blgp:2
	v_mfma_scale_f32_16x16x128_f8f6f4 v[142:145], v[122:127], v[26:31], v[188:191], v178, v115 op_sel_hi:[0,0,0] cbsz:2 blgp:2
	v_mfma_scale_f32_16x16x128_f8f6f4 v[134:137], v[122:127], v[38:43], v[134:137], v179, v115 op_sel_hi:[0,0,0] cbsz:2 blgp:2
	v_mfma_scale_f32_16x16x128_f8f6f4 v[138:141], v[122:127], v[50:55], v[138:141], v179, v115 op_sel_hi:[0,0,0] cbsz:2 blgp:2
	v_mfma_scale_f32_16x16x128_f8f6f4 v[142:145], v[122:127], v[62:67], v[142:145], v179, v115 op_sel_hi:[0,0,0] cbsz:2 blgp:2
	s_waitcnt lgkmcnt(0)
	v_mfma_scale_f32_16x16x128_f8f6f4 v[134:137], v[128:133], v[8:13], v[134:137], v178, v115 op_sel_hi:[0,0,0] cbsz:2 blgp:2
	v_mfma_scale_f32_16x16x128_f8f6f4 v[134:137], v[128:133], v[44:49], v[134:137], v179, v115 op_sel_hi:[0,0,0] cbsz:2 blgp:2
	v_mfma_scale_f32_16x16x128_f8f6f4 v[138:141], v[128:133], v[20:25], v[138:141], v178, v115 op_sel_hi:[0,0,0] cbsz:2 blgp:2
	v_mfma_scale_f32_16x16x128_f8f6f4 v[138:141], v[128:133], v[56:61], v[138:141], v179, v115 op_sel_hi:[0,0,0] cbsz:2 blgp:2
	v_mfma_scale_f32_16x16x128_f8f6f4 v[142:145], v[128:133], v[32:37], v[142:145], v178, v115 op_sel_hi:[0,0,0] cbsz:2 blgp:2
	v_mfma_scale_f32_16x16x128_f8f6f4 v[142:145], v[128:133], v[68:73], v[142:145], v179, v115 op_sel_hi:[0,0,0] cbsz:2 blgp:2
	v_fma_mix_f32 v158, v134, v1, v83 op_sel:[0,0,1] op_sel_hi:[0,0,1]
	v_exp_f32_e32 v158, v158
	v_fma_mix_f32 v159, v138, v99, v75 op_sel:[0,0,1] op_sel_hi:[0,0,1]
	v_exp_f32_e32 v159, v159
	v_fma_f32 v158, v158, v186, v186
	v_rcp_f32_e32 v158, v158
	v_add_f32_e32 v159, 1.0, v159
	v_rcp_f32_e32 v159, v159
	s_nop 0
	v_fma_mix_f32 v161, v158, v142, v79 op_sel:[0,0,1] op_sel_hi:[0,0,1]
	v_exp_f32_e32 v161, v161
	s_add_u32 s48, s48, s40
	v_add_f32_e32 v161, 1.0, v161
	v_rcp_f32_e32 v161, v161
	s_addc_u32 s49, s49, s41
	v_fma_f32 v162, v161, -2.0, 1.0
	v_sub_f32_e32 v163, v176, v162
	v_fma_f32 v176, v159, v163, v162
	v_fma_f32 v164, |v176|, s16, v117
	v_fma_f32 v165, |v176|, s17, v118
	v_fma_f32 v166, |v176|, s18, v119
	v_lshrrev_b32_e32 v167, 26, v176
	v_min3_u32 v164, v164, v165, v166
	v_bfi_b32 v168, 31, v164, v167
	v_lshrrev_b32_e32 v169, v181, v168
	global_store_short_d16_hi v185, v176, s[48:49]
	v_mul_u32_u24_dpp v170, v168, v180 quad_perm:[1,2,3,3] row_mask:0xf bank_mask:0xf bound_ctrl:1
	v_or_b32_e32 v171, v169, v170
	ds_write_b8 v184, v171
	s_waitcnt lgkmcnt(0)
	s_barrier
	ds_read_b64 v[122:123], v106 offset:0
	ds_read_b64 v[124:125], v106 offset:8
	ds_read_b64 v[126:127], v106 offset:16
	s_barrier
	ds_read_b64 v[128:129], v106 offset:96
	ds_read_b64 v[130:131], v106 offset:104
	ds_read_b64 v[132:133], v106 offset:112
	s_waitcnt lgkmcnt(3)
	v_mfma_scale_f32_16x16x128_f8f6f4 v[134:137], v[122:127], v[2:7], 0, v178, v115 op_sel_hi:[0,0,0] cbsz:2 blgp:2
	v_mfma_scale_f32_16x16x128_f8f6f4 v[138:141], v[122:127], v[14:19], 0, v178, v115 op_sel_hi:[0,0,0] cbsz:2 blgp:2
	v_mfma_scale_f32_16x16x128_f8f6f4 v[142:145], v[122:127], v[26:31], v[188:191], v178, v115 op_sel_hi:[0,0,0] cbsz:2 blgp:2
	v_mfma_scale_f32_16x16x128_f8f6f4 v[134:137], v[122:127], v[38:43], v[134:137], v179, v115 op_sel_hi:[0,0,0] cbsz:2 blgp:2
	v_mfma_scale_f32_16x16x128_f8f6f4 v[138:141], v[122:127], v[50:55], v[138:141], v179, v115 op_sel_hi:[0,0,0] cbsz:2 blgp:2
	v_mfma_scale_f32_16x16x128_f8f6f4 v[142:145], v[122:127], v[62:67], v[142:145], v179, v115 op_sel_hi:[0,0,0] cbsz:2 blgp:2
	s_waitcnt lgkmcnt(0)
	v_mfma_scale_f32_16x16x128_f8f6f4 v[134:137], v[128:133], v[8:13], v[134:137], v178, v115 op_sel_hi:[0,0,0] cbsz:2 blgp:2
	v_mfma_scale_f32_16x16x128_f8f6f4 v[134:137], v[128:133], v[44:49], v[134:137], v179, v115 op_sel_hi:[0,0,0] cbsz:2 blgp:2
	v_mfma_scale_f32_16x16x128_f8f6f4 v[138:141], v[128:133], v[20:25], v[138:141], v178, v115 op_sel_hi:[0,0,0] cbsz:2 blgp:2
	v_mfma_scale_f32_16x16x128_f8f6f4 v[138:141], v[128:133], v[56:61], v[138:141], v179, v115 op_sel_hi:[0,0,0] cbsz:2 blgp:2
	v_mfma_scale_f32_16x16x128_f8f6f4 v[142:145], v[128:133], v[32:37], v[142:145], v178, v115 op_sel_hi:[0,0,0] cbsz:2 blgp:2
	v_mfma_scale_f32_16x16x128_f8f6f4 v[142:145], v[128:133], v[68:73], v[142:145], v179, v115 op_sel_hi:[0,0,0] cbsz:2 blgp:2
	v_fma_mix_f32 v158, v134, v1, v84 op_sel_hi:[0,0,1]
	v_exp_f32_e32 v158, v158
	v_fma_mix_f32 v159, v138, v99, v76 op_sel_hi:[0,0,1]
	v_exp_f32_e32 v159, v159
	v_fma_f32 v158, v158, v186, v186
	v_rcp_f32_e32 v158, v158
	v_add_f32_e32 v159, 1.0, v159
	v_rcp_f32_e32 v159, v159
	s_nop 0
	v_fma_mix_f32 v161, v158, v142, v80 op_sel_hi:[0,0,1]
	v_exp_f32_e32 v161, v161
	s_add_u32 s48, s48, s40
	v_add_f32_e32 v161, 1.0, v161
	v_rcp_f32_e32 v161, v161
	s_addc_u32 s49, s49, s41
	v_fma_f32 v162, v161, -2.0, 1.0
	v_sub_f32_e32 v163, v176, v162
	v_fma_f32 v176, v159, v163, v162
	v_fma_f32 v164, |v176|, s16, v117
	v_fma_f32 v165, |v176|, s17, v118
	v_fma_f32 v166, |v176|, s18, v119
	v_lshrrev_b32_e32 v167, 26, v176
	v_min3_u32 v164, v164, v165, v166
	v_bfi_b32 v168, 31, v164, v167
	v_lshrrev_b32_e32 v169, v181, v168
	global_store_short_d16_hi v185, v176, s[48:49]
	v_mul_u32_u24_dpp v170, v168, v180 quad_perm:[1,2,3,3] row_mask:0xf bank_mask:0xf bound_ctrl:1
	v_or_b32_e32 v171, v169, v170
	ds_write_b8 v184, v171 offset:416
	s_waitcnt lgkmcnt(0)
	s_barrier
	ds_read_b64 v[122:123], v106 offset:416
	ds_read_b64 v[124:125], v106 offset:424
	ds_read_b64 v[126:127], v106 offset:432
	s_barrier
	ds_read_b64 v[128:129], v106 offset:512
	ds_read_b64 v[130:131], v106 offset:520
	ds_read_b64 v[132:133], v106 offset:528
	s_waitcnt lgkmcnt(3)
	v_mfma_scale_f32_16x16x128_f8f6f4 v[134:137], v[122:127], v[2:7], 0, v178, v115 op_sel_hi:[0,0,0] cbsz:2 blgp:2
	v_mfma_scale_f32_16x16x128_f8f6f4 v[138:141], v[122:127], v[14:19], 0, v178, v115 op_sel_hi:[0,0,0] cbsz:2 blgp:2
	v_mfma_scale_f32_16x16x128_f8f6f4 v[142:145], v[122:127], v[26:31], v[188:191], v178, v115 op_sel_hi:[0,0,0] cbsz:2 blgp:2
	v_mfma_scale_f32_16x16x128_f8f6f4 v[134:137], v[122:127], v[38:43], v[134:137], v179, v115 op_sel_hi:[0,0,0] cbsz:2 blgp:2
	v_mfma_scale_f32_16x16x128_f8f6f4 v[138:141], v[122:127], v[50:55], v[138:141], v179, v115 op_sel_hi:[0,0,0] cbsz:2 blgp:2
	v_mfma_scale_f32_16x16x128_f8f6f4 v[142:145], v[122:127], v[62:67], v[142:145], v179, v115 op_sel_hi:[0,0,0] cbsz:2 blgp:2
	s_waitcnt lgkmcnt(0)
	v_mfma_scale_f32_16x16x128_f8f6f4 v[134:137], v[128:133], v[8:13], v[134:137], v178, v115 op_sel_hi:[0,0,0] cbsz:2 blgp:2
	v_mfma_scale_f32_16x16x128_f8f6f4 v[134:137], v[128:133], v[44:49], v[134:137], v179, v115 op_sel_hi:[0,0,0] cbsz:2 blgp:2
	v_mfma_scale_f32_16x16x128_f8f6f4 v[138:141], v[128:133], v[20:25], v[138:141], v178, v115 op_sel_hi:[0,0,0] cbsz:2 blgp:2
	v_mfma_scale_f32_16x16x128_f8f6f4 v[138:141], v[128:133], v[56:61], v[138:141], v179, v115 op_sel_hi:[0,0,0] cbsz:2 blgp:2
	v_mfma_scale_f32_16x16x128_f8f6f4 v[142:145], v[128:133], v[32:37], v[142:145], v178, v115 op_sel_hi:[0,0,0] cbsz:2 blgp:2
	v_mfma_scale_f32_16x16x128_f8f6f4 v[142:145], v[128:133], v[68:73], v[142:145], v179, v115 op_sel_hi:[0,0,0] cbsz:2 blgp:2
	v_fma_mix_f32 v158, v134, v1, v84 op_sel:[0,0,1] op_sel_hi:[0,0,1]
	v_exp_f32_e32 v158, v158
	v_fma_mix_f32 v159, v138, v99, v76 op_sel:[0,0,1] op_sel_hi:[0,0,1]
	v_exp_f32_e32 v159, v159
	v_fma_f32 v158, v158, v186, v186
	v_rcp_f32_e32 v158, v158
	v_add_f32_e32 v159, 1.0, v159
	v_rcp_f32_e32 v159, v159
	s_nop 0
	v_fma_mix_f32 v161, v158, v142, v80 op_sel:[0,0,1] op_sel_hi:[0,0,1]
	v_exp_f32_e32 v161, v161
	s_add_u32 s48, s48, s40
	v_add_f32_e32 v161, 1.0, v161
	v_rcp_f32_e32 v161, v161
	s_addc_u32 s49, s49, s41
	v_fma_f32 v162, v161, -2.0, 1.0
	v_sub_f32_e32 v163, v176, v162
	v_fma_f32 v176, v159, v163, v162
	v_fma_f32 v164, |v176|, s16, v117
	v_fma_f32 v165, |v176|, s17, v118
	v_fma_f32 v166, |v176|, s18, v119
	v_lshrrev_b32_e32 v167, 26, v176
	v_min3_u32 v164, v164, v165, v166
	v_bfi_b32 v168, 31, v164, v167
	v_lshrrev_b32_e32 v169, v181, v168
	global_store_short_d16_hi v185, v176, s[48:49]
	v_mul_u32_u24_dpp v170, v168, v180 quad_perm:[1,2,3,3] row_mask:0xf bank_mask:0xf bound_ctrl:1
	v_or_b32_e32 v171, v169, v170
	ds_write_b8 v184, v171
	s_waitcnt lgkmcnt(0)
	s_barrier
	ds_read_b64 v[122:123], v106 offset:0
	ds_read_b64 v[124:125], v106 offset:8
	ds_read_b64 v[126:127], v106 offset:16
	s_barrier
	ds_read_b64 v[128:129], v106 offset:96
	ds_read_b64 v[130:131], v106 offset:104
	ds_read_b64 v[132:133], v106 offset:112
	s_waitcnt lgkmcnt(3)
	v_mfma_scale_f32_16x16x128_f8f6f4 v[134:137], v[122:127], v[2:7], 0, v178, v115 op_sel_hi:[0,0,0] cbsz:2 blgp:2
	v_mfma_scale_f32_16x16x128_f8f6f4 v[138:141], v[122:127], v[14:19], 0, v178, v115 op_sel_hi:[0,0,0] cbsz:2 blgp:2
	v_mfma_scale_f32_16x16x128_f8f6f4 v[142:145], v[122:127], v[26:31], v[188:191], v178, v115 op_sel_hi:[0,0,0] cbsz:2 blgp:2
	v_mfma_scale_f32_16x16x128_f8f6f4 v[134:137], v[122:127], v[38:43], v[134:137], v179, v115 op_sel_hi:[0,0,0] cbsz:2 blgp:2
	v_mfma_scale_f32_16x16x128_f8f6f4 v[138:141], v[122:127], v[50:55], v[138:141], v179, v115 op_sel_hi:[0,0,0] cbsz:2 blgp:2
	v_mfma_scale_f32_16x16x128_f8f6f4 v[142:145], v[122:127], v[62:67], v[142:145], v179, v115 op_sel_hi:[0,0,0] cbsz:2 blgp:2
	s_waitcnt lgkmcnt(0)
	v_mfma_scale_f32_16x16x128_f8f6f4 v[134:137], v[128:133], v[8:13], v[134:137], v178, v115 op_sel_hi:[0,0,0] cbsz:2 blgp:2
	v_mfma_scale_f32_16x16x128_f8f6f4 v[134:137], v[128:133], v[44:49], v[134:137], v179, v115 op_sel_hi:[0,0,0] cbsz:2 blgp:2
	v_mfma_scale_f32_16x16x128_f8f6f4 v[138:141], v[128:133], v[20:25], v[138:141], v178, v115 op_sel_hi:[0,0,0] cbsz:2 blgp:2
	v_mfma_scale_f32_16x16x128_f8f6f4 v[138:141], v[128:133], v[56:61], v[138:141], v179, v115 op_sel_hi:[0,0,0] cbsz:2 blgp:2
	v_mfma_scale_f32_16x16x128_f8f6f4 v[142:145], v[128:133], v[32:37], v[142:145], v178, v115 op_sel_hi:[0,0,0] cbsz:2 blgp:2
	v_mfma_scale_f32_16x16x128_f8f6f4 v[142:145], v[128:133], v[68:73], v[142:145], v179, v115 op_sel_hi:[0,0,0] cbsz:2 blgp:2
	v_fma_mix_f32 v158, v134, v1, v85 op_sel_hi:[0,0,1]
	v_exp_f32_e32 v158, v158
	v_fma_mix_f32 v159, v138, v99, v77 op_sel_hi:[0,0,1]
	v_exp_f32_e32 v159, v159
	v_fma_f32 v158, v158, v186, v186
	v_rcp_f32_e32 v158, v158
	v_add_f32_e32 v159, 1.0, v159
	v_rcp_f32_e32 v159, v159
	s_nop 0
	v_fma_mix_f32 v161, v158, v142, v81 op_sel_hi:[0,0,1]
	v_exp_f32_e32 v161, v161
	s_add_u32 s48, s48, s40
	v_add_f32_e32 v161, 1.0, v161
	v_rcp_f32_e32 v161, v161
	s_addc_u32 s49, s49, s41
	v_fma_f32 v162, v161, -2.0, 1.0
	v_sub_f32_e32 v163, v176, v162
	v_fma_f32 v176, v159, v163, v162
	v_fma_f32 v164, |v176|, s16, v117
	v_fma_f32 v165, |v176|, s17, v118
	v_fma_f32 v166, |v176|, s18, v119
	v_lshrrev_b32_e32 v167, 26, v176
	v_min3_u32 v164, v164, v165, v166
	v_bfi_b32 v168, 31, v164, v167
	v_lshrrev_b32_e32 v169, v181, v168
	global_store_short_d16_hi v185, v176, s[48:49]
	v_mul_u32_u24_dpp v170, v168, v180 quad_perm:[1,2,3,3] row_mask:0xf bank_mask:0xf bound_ctrl:1
	v_or_b32_e32 v171, v169, v170
	ds_write_b8 v184, v171 offset:416
	s_waitcnt lgkmcnt(0)
	s_barrier
	ds_read_b64 v[122:123], v106 offset:416
	ds_read_b64 v[124:125], v106 offset:424
	ds_read_b64 v[126:127], v106 offset:432
	s_barrier
	ds_read_b64 v[128:129], v106 offset:512
	ds_read_b64 v[130:131], v106 offset:520
	ds_read_b64 v[132:133], v106 offset:528
	s_waitcnt lgkmcnt(3)
	v_mfma_scale_f32_16x16x128_f8f6f4 v[134:137], v[122:127], v[2:7], 0, v178, v115 op_sel_hi:[0,0,0] cbsz:2 blgp:2
	v_mfma_scale_f32_16x16x128_f8f6f4 v[138:141], v[122:127], v[14:19], 0, v178, v115 op_sel_hi:[0,0,0] cbsz:2 blgp:2
	v_mfma_scale_f32_16x16x128_f8f6f4 v[142:145], v[122:127], v[26:31], v[188:191], v178, v115 op_sel_hi:[0,0,0] cbsz:2 blgp:2
	v_mfma_scale_f32_16x16x128_f8f6f4 v[134:137], v[122:127], v[38:43], v[134:137], v179, v115 op_sel_hi:[0,0,0] cbsz:2 blgp:2
	v_mfma_scale_f32_16x16x128_f8f6f4 v[138:141], v[122:127], v[50:55], v[138:141], v179, v115 op_sel_hi:[0,0,0] cbsz:2 blgp:2
	v_mfma_scale_f32_16x16x128_f8f6f4 v[142:145], v[122:127], v[62:67], v[142:145], v179, v115 op_sel_hi:[0,0,0] cbsz:2 blgp:2
	s_waitcnt lgkmcnt(0)
	v_mfma_scale_f32_16x16x128_f8f6f4 v[134:137], v[128:133], v[8:13], v[134:137], v178, v115 op_sel_hi:[0,0,0] cbsz:2 blgp:2
	v_mfma_scale_f32_16x16x128_f8f6f4 v[134:137], v[128:133], v[44:49], v[134:137], v179, v115 op_sel_hi:[0,0,0] cbsz:2 blgp:2
	v_mfma_scale_f32_16x16x128_f8f6f4 v[138:141], v[128:133], v[20:25], v[138:141], v178, v115 op_sel_hi:[0,0,0] cbsz:2 blgp:2
	v_mfma_scale_f32_16x16x128_f8f6f4 v[138:141], v[128:133], v[56:61], v[138:141], v179, v115 op_sel_hi:[0,0,0] cbsz:2 blgp:2
	v_mfma_scale_f32_16x16x128_f8f6f4 v[142:145], v[128:133], v[32:37], v[142:145], v178, v115 op_sel_hi:[0,0,0] cbsz:2 blgp:2
	v_mfma_scale_f32_16x16x128_f8f6f4 v[142:145], v[128:133], v[68:73], v[142:145], v179, v115 op_sel_hi:[0,0,0] cbsz:2 blgp:2
	v_fma_mix_f32 v158, v134, v1, v85 op_sel:[0,0,1] op_sel_hi:[0,0,1]
	v_exp_f32_e32 v158, v158
	v_fma_mix_f32 v159, v138, v99, v77 op_sel:[0,0,1] op_sel_hi:[0,0,1]
	v_exp_f32_e32 v159, v159
	v_fma_f32 v158, v158, v186, v186
	v_rcp_f32_e32 v158, v158
	v_add_f32_e32 v159, 1.0, v159
	v_rcp_f32_e32 v159, v159
	s_nop 0
	v_fma_mix_f32 v161, v158, v142, v81 op_sel:[0,0,1] op_sel_hi:[0,0,1]
	v_exp_f32_e32 v161, v161
	s_add_u32 s48, s48, s40
	v_add_f32_e32 v161, 1.0, v161
	v_rcp_f32_e32 v161, v161
	s_addc_u32 s49, s49, s41
	v_fma_f32 v162, v161, -2.0, 1.0
	v_sub_f32_e32 v163, v176, v162
	v_fma_f32 v176, v159, v163, v162
	v_fma_f32 v164, |v176|, s16, v117
	v_fma_f32 v165, |v176|, s17, v118
	v_fma_f32 v166, |v176|, s18, v119
	v_lshrrev_b32_e32 v167, 26, v176
	v_min3_u32 v164, v164, v165, v166
	v_bfi_b32 v168, 31, v164, v167
	v_lshrrev_b32_e32 v169, v181, v168
	global_store_short_d16_hi v185, v176, s[48:49]
	v_mul_u32_u24_dpp v170, v168, v180 quad_perm:[1,2,3,3] row_mask:0xf bank_mask:0xf bound_ctrl:1
	v_or_b32_e32 v171, v169, v170
	ds_write_b8 v184, v171
	s_waitcnt lgkmcnt(0)
	s_barrier
	ds_read_b64 v[122:123], v106 offset:0
	ds_read_b64 v[124:125], v106 offset:8
	ds_read_b64 v[126:127], v106 offset:16
	s_barrier
	ds_read_b64 v[128:129], v106 offset:96
	ds_read_b64 v[130:131], v106 offset:104
	ds_read_b64 v[132:133], v106 offset:112
	s_waitcnt vmcnt(8)
	global_load_dwordx4 v[82:85], v[196:197], off
	global_load_dwordx4 v[74:77], v[196:197], off offset:512
	global_load_dwordx4 v[78:81], v[196:197], off offset:1024
	v_lshl_add_u64 v[196:197], v[196:197], 0, s[42:43]
	s_waitcnt lgkmcnt(3)
	v_mfma_scale_f32_16x16x128_f8f6f4 v[134:137], v[122:127], v[2:7], 0, v178, v115 op_sel_hi:[0,0,0] cbsz:2 blgp:2
	v_mfma_scale_f32_16x16x128_f8f6f4 v[138:141], v[122:127], v[14:19], 0, v178, v115 op_sel_hi:[0,0,0] cbsz:2 blgp:2
	v_mfma_scale_f32_16x16x128_f8f6f4 v[142:145], v[122:127], v[26:31], v[188:191], v178, v115 op_sel_hi:[0,0,0] cbsz:2 blgp:2
	v_mfma_scale_f32_16x16x128_f8f6f4 v[134:137], v[122:127], v[38:43], v[134:137], v179, v115 op_sel_hi:[0,0,0] cbsz:2 blgp:2
	v_mfma_scale_f32_16x16x128_f8f6f4 v[138:141], v[122:127], v[50:55], v[138:141], v179, v115 op_sel_hi:[0,0,0] cbsz:2 blgp:2
	v_mfma_scale_f32_16x16x128_f8f6f4 v[142:145], v[122:127], v[62:67], v[142:145], v179, v115 op_sel_hi:[0,0,0] cbsz:2 blgp:2
	s_waitcnt lgkmcnt(0)
	v_mfma_scale_f32_16x16x128_f8f6f4 v[134:137], v[128:133], v[8:13], v[134:137], v178, v115 op_sel_hi:[0,0,0] cbsz:2 blgp:2
	v_mfma_scale_f32_16x16x128_f8f6f4 v[134:137], v[128:133], v[44:49], v[134:137], v179, v115 op_sel_hi:[0,0,0] cbsz:2 blgp:2
	v_mfma_scale_f32_16x16x128_f8f6f4 v[138:141], v[128:133], v[20:25], v[138:141], v178, v115 op_sel_hi:[0,0,0] cbsz:2 blgp:2
	v_mfma_scale_f32_16x16x128_f8f6f4 v[138:141], v[128:133], v[56:61], v[138:141], v179, v115 op_sel_hi:[0,0,0] cbsz:2 blgp:2
	v_mfma_scale_f32_16x16x128_f8f6f4 v[142:145], v[128:133], v[32:37], v[142:145], v178, v115 op_sel_hi:[0,0,0] cbsz:2 blgp:2
	v_mfma_scale_f32_16x16x128_f8f6f4 v[142:145], v[128:133], v[68:73], v[142:145], v179, v115 op_sel_hi:[0,0,0] cbsz:2 blgp:2
	v_fma_mix_f32 v158, v134, v1, v146 op_sel_hi:[0,0,1]
	v_exp_f32_e32 v158, v158
	v_fma_mix_f32 v159, v138, v99, v150 op_sel_hi:[0,0,1]
	v_exp_f32_e32 v159, v159
	v_fma_f32 v158, v158, v186, v186
	v_rcp_f32_e32 v158, v158
	v_add_f32_e32 v159, 1.0, v159
	v_rcp_f32_e32 v159, v159
	s_nop 0
	v_fma_mix_f32 v161, v158, v142, v154 op_sel_hi:[0,0,1]
	v_exp_f32_e32 v161, v161
	s_add_u32 s48, s48, s40
	v_add_f32_e32 v161, 1.0, v161
	v_rcp_f32_e32 v161, v161
	s_addc_u32 s49, s49, s41
	v_fma_f32 v162, v161, -2.0, 1.0
	v_sub_f32_e32 v163, v176, v162
	v_fma_f32 v176, v159, v163, v162
	v_fma_f32 v164, |v176|, s16, v117
	v_fma_f32 v165, |v176|, s17, v118
	v_fma_f32 v166, |v176|, s18, v119
	v_lshrrev_b32_e32 v167, 26, v176
	v_min3_u32 v164, v164, v165, v166
	v_bfi_b32 v168, 31, v164, v167
	v_lshrrev_b32_e32 v169, v181, v168
	global_store_short_d16_hi v185, v176, s[48:49]
	v_mul_u32_u24_dpp v170, v168, v180 quad_perm:[1,2,3,3] row_mask:0xf bank_mask:0xf bound_ctrl:1
	v_or_b32_e32 v171, v169, v170
	ds_write_b8 v184, v171 offset:416
	s_waitcnt lgkmcnt(0)
	s_barrier
	ds_read_b64 v[122:123], v106 offset:416
	ds_read_b64 v[124:125], v106 offset:424
	ds_read_b64 v[126:127], v106 offset:432
	s_barrier
	ds_read_b64 v[128:129], v106 offset:512
	ds_read_b64 v[130:131], v106 offset:520
	ds_read_b64 v[132:133], v106 offset:528
	s_waitcnt lgkmcnt(3)
	v_mfma_scale_f32_16x16x128_f8f6f4 v[134:137], v[122:127], v[2:7], 0, v178, v115 op_sel_hi:[0,0,0] cbsz:2 blgp:2
	v_mfma_scale_f32_16x16x128_f8f6f4 v[138:141], v[122:127], v[14:19], 0, v178, v115 op_sel_hi:[0,0,0] cbsz:2 blgp:2
	v_mfma_scale_f32_16x16x128_f8f6f4 v[142:145], v[122:127], v[26:31], v[188:191], v178, v115 op_sel_hi:[0,0,0] cbsz:2 blgp:2
	v_mfma_scale_f32_16x16x128_f8f6f4 v[134:137], v[122:127], v[38:43], v[134:137], v179, v115 op_sel_hi:[0,0,0] cbsz:2 blgp:2
	v_mfma_scale_f32_16x16x128_f8f6f4 v[138:141], v[122:127], v[50:55], v[138:141], v179, v115 op_sel_hi:[0,0,0] cbsz:2 blgp:2
	v_mfma_scale_f32_16x16x128_f8f6f4 v[142:145], v[122:127], v[62:67], v[142:145], v179, v115 op_sel_hi:[0,0,0] cbsz:2 blgp:2
	s_waitcnt lgkmcnt(0)
	v_mfma_scale_f32_16x16x128_f8f6f4 v[134:137], v[128:133], v[8:13], v[134:137], v178, v115 op_sel_hi:[0,0,0] cbsz:2 blgp:2
	v_mfma_scale_f32_16x16x128_f8f6f4 v[134:137], v[128:133], v[44:49], v[134:137], v179, v115 op_sel_hi:[0,0,0] cbsz:2 blgp:2
	v_mfma_scale_f32_16x16x128_f8f6f4 v[138:141], v[128:133], v[20:25], v[138:141], v178, v115 op_sel_hi:[0,0,0] cbsz:2 blgp:2
	v_mfma_scale_f32_16x16x128_f8f6f4 v[138:141], v[128:133], v[56:61], v[138:141], v179, v115 op_sel_hi:[0,0,0] cbsz:2 blgp:2
	v_mfma_scale_f32_16x16x128_f8f6f4 v[142:145], v[128:133], v[32:37], v[142:145], v178, v115 op_sel_hi:[0,0,0] cbsz:2 blgp:2
	v_mfma_scale_f32_16x16x128_f8f6f4 v[142:145], v[128:133], v[68:73], v[142:145], v179, v115 op_sel_hi:[0,0,0] cbsz:2 blgp:2
	v_fma_mix_f32 v158, v134, v1, v146 op_sel:[0,0,1] op_sel_hi:[0,0,1]
	v_exp_f32_e32 v158, v158
	v_fma_mix_f32 v159, v138, v99, v150 op_sel:[0,0,1] op_sel_hi:[0,0,1]
	v_exp_f32_e32 v159, v159
	v_fma_f32 v158, v158, v186, v186
	v_rcp_f32_e32 v158, v158
	v_add_f32_e32 v159, 1.0, v159
	v_rcp_f32_e32 v159, v159
	s_nop 0
	v_fma_mix_f32 v161, v158, v142, v154 op_sel:[0,0,1] op_sel_hi:[0,0,1]
	v_exp_f32_e32 v161, v161
	s_add_u32 s48, s48, s40
	v_add_f32_e32 v161, 1.0, v161
	v_rcp_f32_e32 v161, v161
	s_addc_u32 s49, s49, s41
	v_fma_f32 v162, v161, -2.0, 1.0
	v_sub_f32_e32 v163, v176, v162
	v_fma_f32 v176, v159, v163, v162
	v_fma_f32 v164, |v176|, s16, v117
	v_fma_f32 v165, |v176|, s17, v118
	v_fma_f32 v166, |v176|, s18, v119
	v_lshrrev_b32_e32 v167, 26, v176
	v_min3_u32 v164, v164, v165, v166
	v_bfi_b32 v168, 31, v164, v167
	v_lshrrev_b32_e32 v169, v181, v168
	global_store_short_d16_hi v185, v176, s[48:49]
	v_mul_u32_u24_dpp v170, v168, v180 quad_perm:[1,2,3,3] row_mask:0xf bank_mask:0xf bound_ctrl:1
	v_or_b32_e32 v171, v169, v170
	ds_write_b8 v184, v171
	s_waitcnt lgkmcnt(0)
	s_barrier
	ds_read_b64 v[122:123], v106 offset:0
	ds_read_b64 v[124:125], v106 offset:8
	ds_read_b64 v[126:127], v106 offset:16
	s_barrier
	ds_read_b64 v[128:129], v106 offset:96
	ds_read_b64 v[130:131], v106 offset:104
	ds_read_b64 v[132:133], v106 offset:112
	s_waitcnt lgkmcnt(3)
	v_mfma_scale_f32_16x16x128_f8f6f4 v[134:137], v[122:127], v[2:7], 0, v178, v115 op_sel_hi:[0,0,0] cbsz:2 blgp:2
	v_mfma_scale_f32_16x16x128_f8f6f4 v[138:141], v[122:127], v[14:19], 0, v178, v115 op_sel_hi:[0,0,0] cbsz:2 blgp:2
	v_mfma_scale_f32_16x16x128_f8f6f4 v[142:145], v[122:127], v[26:31], v[188:191], v178, v115 op_sel_hi:[0,0,0] cbsz:2 blgp:2
	v_mfma_scale_f32_16x16x128_f8f6f4 v[134:137], v[122:127], v[38:43], v[134:137], v179, v115 op_sel_hi:[0,0,0] cbsz:2 blgp:2
	v_mfma_scale_f32_16x16x128_f8f6f4 v[138:141], v[122:127], v[50:55], v[138:141], v179, v115 op_sel_hi:[0,0,0] cbsz:2 blgp:2
	v_mfma_scale_f32_16x16x128_f8f6f4 v[142:145], v[122:127], v[62:67], v[142:145], v179, v115 op_sel_hi:[0,0,0] cbsz:2 blgp:2
	s_waitcnt lgkmcnt(0)
	v_mfma_scale_f32_16x16x128_f8f6f4 v[134:137], v[128:133], v[8:13], v[134:137], v178, v115 op_sel_hi:[0,0,0] cbsz:2 blgp:2
	v_mfma_scale_f32_16x16x128_f8f6f4 v[134:137], v[128:133], v[44:49], v[134:137], v179, v115 op_sel_hi:[0,0,0] cbsz:2 blgp:2
	v_mfma_scale_f32_16x16x128_f8f6f4 v[138:141], v[128:133], v[20:25], v[138:141], v178, v115 op_sel_hi:[0,0,0] cbsz:2 blgp:2
	v_mfma_scale_f32_16x16x128_f8f6f4 v[138:141], v[128:133], v[56:61], v[138:141], v179, v115 op_sel_hi:[0,0,0] cbsz:2 blgp:2
	v_mfma_scale_f32_16x16x128_f8f6f4 v[142:145], v[128:133], v[32:37], v[142:145], v178, v115 op_sel_hi:[0,0,0] cbsz:2 blgp:2
	v_mfma_scale_f32_16x16x128_f8f6f4 v[142:145], v[128:133], v[68:73], v[142:145], v179, v115 op_sel_hi:[0,0,0] cbsz:2 blgp:2
	v_fma_mix_f32 v158, v134, v1, v147 op_sel_hi:[0,0,1]
	v_exp_f32_e32 v158, v158
	v_fma_mix_f32 v159, v138, v99, v151 op_sel_hi:[0,0,1]
	v_exp_f32_e32 v159, v159
	v_fma_f32 v158, v158, v186, v186
	v_rcp_f32_e32 v158, v158
	v_add_f32_e32 v159, 1.0, v159
	v_rcp_f32_e32 v159, v159
	s_nop 0
	v_fma_mix_f32 v161, v158, v142, v155 op_sel_hi:[0,0,1]
	v_exp_f32_e32 v161, v161
	s_add_u32 s48, s48, s40
	v_add_f32_e32 v161, 1.0, v161
	v_rcp_f32_e32 v161, v161
	s_addc_u32 s49, s49, s41
	v_fma_f32 v162, v161, -2.0, 1.0
	v_sub_f32_e32 v163, v176, v162
	v_fma_f32 v176, v159, v163, v162
	v_fma_f32 v164, |v176|, s16, v117
	v_fma_f32 v165, |v176|, s17, v118
	v_fma_f32 v166, |v176|, s18, v119
	v_lshrrev_b32_e32 v167, 26, v176
	v_min3_u32 v164, v164, v165, v166
	v_bfi_b32 v168, 31, v164, v167
	v_lshrrev_b32_e32 v169, v181, v168
	global_store_short_d16_hi v185, v176, s[48:49]
	v_mul_u32_u24_dpp v170, v168, v180 quad_perm:[1,2,3,3] row_mask:0xf bank_mask:0xf bound_ctrl:1
	v_or_b32_e32 v171, v169, v170
	ds_write_b8 v184, v171 offset:416
	s_waitcnt lgkmcnt(0)
	s_barrier
	ds_read_b64 v[122:123], v106 offset:416
	ds_read_b64 v[124:125], v106 offset:424
	ds_read_b64 v[126:127], v106 offset:432
	s_barrier
	ds_read_b64 v[128:129], v106 offset:512
	ds_read_b64 v[130:131], v106 offset:520
	ds_read_b64 v[132:133], v106 offset:528
	s_waitcnt lgkmcnt(3)
	v_mfma_scale_f32_16x16x128_f8f6f4 v[134:137], v[122:127], v[2:7], 0, v178, v115 op_sel_hi:[0,0,0] cbsz:2 blgp:2
	v_mfma_scale_f32_16x16x128_f8f6f4 v[138:141], v[122:127], v[14:19], 0, v178, v115 op_sel_hi:[0,0,0] cbsz:2 blgp:2
	v_mfma_scale_f32_16x16x128_f8f6f4 v[142:145], v[122:127], v[26:31], v[188:191], v178, v115 op_sel_hi:[0,0,0] cbsz:2 blgp:2
	v_mfma_scale_f32_16x16x128_f8f6f4 v[134:137], v[122:127], v[38:43], v[134:137], v179, v115 op_sel_hi:[0,0,0] cbsz:2 blgp:2
	v_mfma_scale_f32_16x16x128_f8f6f4 v[138:141], v[122:127], v[50:55], v[138:141], v179, v115 op_sel_hi:[0,0,0] cbsz:2 blgp:2
	v_mfma_scale_f32_16x16x128_f8f6f4 v[142:145], v[122:127], v[62:67], v[142:145], v179, v115 op_sel_hi:[0,0,0] cbsz:2 blgp:2
	s_waitcnt lgkmcnt(0)
	v_mfma_scale_f32_16x16x128_f8f6f4 v[134:137], v[128:133], v[8:13], v[134:137], v178, v115 op_sel_hi:[0,0,0] cbsz:2 blgp:2
	v_mfma_scale_f32_16x16x128_f8f6f4 v[134:137], v[128:133], v[44:49], v[134:137], v179, v115 op_sel_hi:[0,0,0] cbsz:2 blgp:2
	v_mfma_scale_f32_16x16x128_f8f6f4 v[138:141], v[128:133], v[20:25], v[138:141], v178, v115 op_sel_hi:[0,0,0] cbsz:2 blgp:2
	v_mfma_scale_f32_16x16x128_f8f6f4 v[138:141], v[128:133], v[56:61], v[138:141], v179, v115 op_sel_hi:[0,0,0] cbsz:2 blgp:2
	v_mfma_scale_f32_16x16x128_f8f6f4 v[142:145], v[128:133], v[32:37], v[142:145], v178, v115 op_sel_hi:[0,0,0] cbsz:2 blgp:2
	v_mfma_scale_f32_16x16x128_f8f6f4 v[142:145], v[128:133], v[68:73], v[142:145], v179, v115 op_sel_hi:[0,0,0] cbsz:2 blgp:2
	v_fma_mix_f32 v158, v134, v1, v147 op_sel:[0,0,1] op_sel_hi:[0,0,1]
	v_exp_f32_e32 v158, v158
	v_fma_mix_f32 v159, v138, v99, v151 op_sel:[0,0,1] op_sel_hi:[0,0,1]
	v_exp_f32_e32 v159, v159
	v_fma_f32 v158, v158, v186, v186
	v_rcp_f32_e32 v158, v158
	v_add_f32_e32 v159, 1.0, v159
	v_rcp_f32_e32 v159, v159
	s_nop 0
	v_fma_mix_f32 v161, v158, v142, v155 op_sel:[0,0,1] op_sel_hi:[0,0,1]
	v_exp_f32_e32 v161, v161
	s_add_u32 s48, s48, s40
	v_add_f32_e32 v161, 1.0, v161
	v_rcp_f32_e32 v161, v161
	s_addc_u32 s49, s49, s41
	v_fma_f32 v162, v161, -2.0, 1.0
	v_sub_f32_e32 v163, v176, v162
	v_fma_f32 v176, v159, v163, v162
	v_fma_f32 v164, |v176|, s16, v117
	v_fma_f32 v165, |v176|, s17, v118
	v_fma_f32 v166, |v176|, s18, v119
	v_lshrrev_b32_e32 v167, 26, v176
	v_min3_u32 v164, v164, v165, v166
	v_bfi_b32 v168, 31, v164, v167
	v_lshrrev_b32_e32 v169, v181, v168
	global_store_short_d16_hi v185, v176, s[48:49]
	v_mul_u32_u24_dpp v170, v168, v180 quad_perm:[1,2,3,3] row_mask:0xf bank_mask:0xf bound_ctrl:1
	v_or_b32_e32 v171, v169, v170
	ds_write_b8 v184, v171
	s_waitcnt lgkmcnt(0)
	s_barrier
	ds_read_b64 v[122:123], v106 offset:0
	ds_read_b64 v[124:125], v106 offset:8
	ds_read_b64 v[126:127], v106 offset:16
	s_barrier
	ds_read_b64 v[128:129], v106 offset:96
	ds_read_b64 v[130:131], v106 offset:104
	ds_read_b64 v[132:133], v106 offset:112
	s_waitcnt lgkmcnt(3)
	v_mfma_scale_f32_16x16x128_f8f6f4 v[134:137], v[122:127], v[2:7], 0, v178, v115 op_sel_hi:[0,0,0] cbsz:2 blgp:2
	v_mfma_scale_f32_16x16x128_f8f6f4 v[138:141], v[122:127], v[14:19], 0, v178, v115 op_sel_hi:[0,0,0] cbsz:2 blgp:2
	v_mfma_scale_f32_16x16x128_f8f6f4 v[142:145], v[122:127], v[26:31], v[188:191], v178, v115 op_sel_hi:[0,0,0] cbsz:2 blgp:2
	v_mfma_scale_f32_16x16x128_f8f6f4 v[134:137], v[122:127], v[38:43], v[134:137], v179, v115 op_sel_hi:[0,0,0] cbsz:2 blgp:2
	v_mfma_scale_f32_16x16x128_f8f6f4 v[138:141], v[122:127], v[50:55], v[138:141], v179, v115 op_sel_hi:[0,0,0] cbsz:2 blgp:2
	v_mfma_scale_f32_16x16x128_f8f6f4 v[142:145], v[122:127], v[62:67], v[142:145], v179, v115 op_sel_hi:[0,0,0] cbsz:2 blgp:2
	s_waitcnt lgkmcnt(0)
	v_mfma_scale_f32_16x16x128_f8f6f4 v[134:137], v[128:133], v[8:13], v[134:137], v178, v115 op_sel_hi:[0,0,0] cbsz:2 blgp:2
	v_mfma_scale_f32_16x16x128_f8f6f4 v[134:137], v[128:133], v[44:49], v[134:137], v179, v115 op_sel_hi:[0,0,0] cbsz:2 blgp:2
	v_mfma_scale_f32_16x16x128_f8f6f4 v[138:141], v[128:133], v[20:25], v[138:141], v178, v115 op_sel_hi:[0,0,0] cbsz:2 blgp:2
	v_mfma_scale_f32_16x16x128_f8f6f4 v[138:141], v[128:133], v[56:61], v[138:141], v179, v115 op_sel_hi:[0,0,0] cbsz:2 blgp:2
	v_mfma_scale_f32_16x16x128_f8f6f4 v[142:145], v[128:133], v[32:37], v[142:145], v178, v115 op_sel_hi:[0,0,0] cbsz:2 blgp:2
	v_mfma_scale_f32_16x16x128_f8f6f4 v[142:145], v[128:133], v[68:73], v[142:145], v179, v115 op_sel_hi:[0,0,0] cbsz:2 blgp:2
	v_fma_mix_f32 v158, v134, v1, v148 op_sel_hi:[0,0,1]
	v_exp_f32_e32 v158, v158
	v_fma_mix_f32 v159, v138, v99, v152 op_sel_hi:[0,0,1]
	v_exp_f32_e32 v159, v159
	v_fma_f32 v158, v158, v186, v186
	v_rcp_f32_e32 v158, v158
	v_add_f32_e32 v159, 1.0, v159
	v_rcp_f32_e32 v159, v159
	s_nop 0
	v_fma_mix_f32 v161, v158, v142, v156 op_sel_hi:[0,0,1]
	v_exp_f32_e32 v161, v161
	s_add_u32 s48, s48, s40
	v_add_f32_e32 v161, 1.0, v161
	v_rcp_f32_e32 v161, v161
	s_addc_u32 s49, s49, s41
	v_fma_f32 v162, v161, -2.0, 1.0
	v_sub_f32_e32 v163, v176, v162
	v_fma_f32 v176, v159, v163, v162
	v_fma_f32 v164, |v176|, s16, v117
	v_fma_f32 v165, |v176|, s17, v118
	v_fma_f32 v166, |v176|, s18, v119
	v_lshrrev_b32_e32 v167, 26, v176
	v_min3_u32 v164, v164, v165, v166
	v_bfi_b32 v168, 31, v164, v167
	v_lshrrev_b32_e32 v169, v181, v168
	global_store_short_d16_hi v185, v176, s[48:49]
	v_mul_u32_u24_dpp v170, v168, v180 quad_perm:[1,2,3,3] row_mask:0xf bank_mask:0xf bound_ctrl:1
	v_or_b32_e32 v171, v169, v170
	ds_write_b8 v184, v171 offset:416
	s_waitcnt lgkmcnt(0)
	s_barrier
	ds_read_b64 v[122:123], v106 offset:416
	ds_read_b64 v[124:125], v106 offset:424
	ds_read_b64 v[126:127], v106 offset:432
	s_barrier
	ds_read_b64 v[128:129], v106 offset:512
	ds_read_b64 v[130:131], v106 offset:520
	ds_read_b64 v[132:133], v106 offset:528
	s_waitcnt lgkmcnt(3)
	v_mfma_scale_f32_16x16x128_f8f6f4 v[134:137], v[122:127], v[2:7], 0, v178, v115 op_sel_hi:[0,0,0] cbsz:2 blgp:2
	v_mfma_scale_f32_16x16x128_f8f6f4 v[138:141], v[122:127], v[14:19], 0, v178, v115 op_sel_hi:[0,0,0] cbsz:2 blgp:2
	v_mfma_scale_f32_16x16x128_f8f6f4 v[142:145], v[122:127], v[26:31], v[188:191], v178, v115 op_sel_hi:[0,0,0] cbsz:2 blgp:2
	v_mfma_scale_f32_16x16x128_f8f6f4 v[134:137], v[122:127], v[38:43], v[134:137], v179, v115 op_sel_hi:[0,0,0] cbsz:2 blgp:2
	v_mfma_scale_f32_16x16x128_f8f6f4 v[138:141], v[122:127], v[50:55], v[138:141], v179, v115 op_sel_hi:[0,0,0] cbsz:2 blgp:2
	v_mfma_scale_f32_16x16x128_f8f6f4 v[142:145], v[122:127], v[62:67], v[142:145], v179, v115 op_sel_hi:[0,0,0] cbsz:2 blgp:2
	s_waitcnt lgkmcnt(0)
	v_mfma_scale_f32_16x16x128_f8f6f4 v[134:137], v[128:133], v[8:13], v[134:137], v178, v115 op_sel_hi:[0,0,0] cbsz:2 blgp:2
	v_mfma_scale_f32_16x16x128_f8f6f4 v[134:137], v[128:133], v[44:49], v[134:137], v179, v115 op_sel_hi:[0,0,0] cbsz:2 blgp:2
	v_mfma_scale_f32_16x16x128_f8f6f4 v[138:141], v[128:133], v[20:25], v[138:141], v178, v115 op_sel_hi:[0,0,0] cbsz:2 blgp:2
	v_mfma_scale_f32_16x16x128_f8f6f4 v[138:141], v[128:133], v[56:61], v[138:141], v179, v115 op_sel_hi:[0,0,0] cbsz:2 blgp:2
	v_mfma_scale_f32_16x16x128_f8f6f4 v[142:145], v[128:133], v[32:37], v[142:145], v178, v115 op_sel_hi:[0,0,0] cbsz:2 blgp:2
	v_mfma_scale_f32_16x16x128_f8f6f4 v[142:145], v[128:133], v[68:73], v[142:145], v179, v115 op_sel_hi:[0,0,0] cbsz:2 blgp:2
	v_fma_mix_f32 v158, v134, v1, v148 op_sel:[0,0,1] op_sel_hi:[0,0,1]
	v_exp_f32_e32 v158, v158
	v_fma_mix_f32 v159, v138, v99, v152 op_sel:[0,0,1] op_sel_hi:[0,0,1]
	v_exp_f32_e32 v159, v159
	v_fma_f32 v158, v158, v186, v186
	v_rcp_f32_e32 v158, v158
	v_add_f32_e32 v159, 1.0, v159
	v_rcp_f32_e32 v159, v159
	s_nop 0
	v_fma_mix_f32 v161, v158, v142, v156 op_sel:[0,0,1] op_sel_hi:[0,0,1]
	v_exp_f32_e32 v161, v161
	s_add_u32 s48, s48, s40
	v_add_f32_e32 v161, 1.0, v161
	v_rcp_f32_e32 v161, v161
	s_addc_u32 s49, s49, s41
	v_fma_f32 v162, v161, -2.0, 1.0
	v_sub_f32_e32 v163, v176, v162
	v_fma_f32 v176, v159, v163, v162
	v_fma_f32 v164, |v176|, s16, v117
	v_fma_f32 v165, |v176|, s17, v118
	v_fma_f32 v166, |v176|, s18, v119
	v_lshrrev_b32_e32 v167, 26, v176
	v_min3_u32 v164, v164, v165, v166
	v_bfi_b32 v168, 31, v164, v167
	v_lshrrev_b32_e32 v169, v181, v168
	global_store_short_d16_hi v185, v176, s[48:49]
	v_mul_u32_u24_dpp v170, v168, v180 quad_perm:[1,2,3,3] row_mask:0xf bank_mask:0xf bound_ctrl:1
	v_or_b32_e32 v171, v169, v170
	ds_write_b8 v184, v171
	s_waitcnt lgkmcnt(0)
	s_barrier
	ds_read_b64 v[122:123], v106 offset:0
	ds_read_b64 v[124:125], v106 offset:8
	ds_read_b64 v[126:127], v106 offset:16
	s_barrier
	ds_read_b64 v[128:129], v106 offset:96
	ds_read_b64 v[130:131], v106 offset:104
	ds_read_b64 v[132:133], v106 offset:112
	s_waitcnt lgkmcnt(3)
	v_mfma_scale_f32_16x16x128_f8f6f4 v[134:137], v[122:127], v[2:7], 0, v178, v115 op_sel_hi:[0,0,0] cbsz:2 blgp:2
	v_mfma_scale_f32_16x16x128_f8f6f4 v[138:141], v[122:127], v[14:19], 0, v178, v115 op_sel_hi:[0,0,0] cbsz:2 blgp:2
	v_mfma_scale_f32_16x16x128_f8f6f4 v[142:145], v[122:127], v[26:31], v[188:191], v178, v115 op_sel_hi:[0,0,0] cbsz:2 blgp:2
	v_mfma_scale_f32_16x16x128_f8f6f4 v[134:137], v[122:127], v[38:43], v[134:137], v179, v115 op_sel_hi:[0,0,0] cbsz:2 blgp:2
	v_mfma_scale_f32_16x16x128_f8f6f4 v[138:141], v[122:127], v[50:55], v[138:141], v179, v115 op_sel_hi:[0,0,0] cbsz:2 blgp:2
	v_mfma_scale_f32_16x16x128_f8f6f4 v[142:145], v[122:127], v[62:67], v[142:145], v179, v115 op_sel_hi:[0,0,0] cbsz:2 blgp:2
	s_waitcnt lgkmcnt(0)
	v_mfma_scale_f32_16x16x128_f8f6f4 v[134:137], v[128:133], v[8:13], v[134:137], v178, v115 op_sel_hi:[0,0,0] cbsz:2 blgp:2
	v_mfma_scale_f32_16x16x128_f8f6f4 v[134:137], v[128:133], v[44:49], v[134:137], v179, v115 op_sel_hi:[0,0,0] cbsz:2 blgp:2
	v_mfma_scale_f32_16x16x128_f8f6f4 v[138:141], v[128:133], v[20:25], v[138:141], v178, v115 op_sel_hi:[0,0,0] cbsz:2 blgp:2
	v_mfma_scale_f32_16x16x128_f8f6f4 v[138:141], v[128:133], v[56:61], v[138:141], v179, v115 op_sel_hi:[0,0,0] cbsz:2 blgp:2
	v_mfma_scale_f32_16x16x128_f8f6f4 v[142:145], v[128:133], v[32:37], v[142:145], v178, v115 op_sel_hi:[0,0,0] cbsz:2 blgp:2
	v_mfma_scale_f32_16x16x128_f8f6f4 v[142:145], v[128:133], v[68:73], v[142:145], v179, v115 op_sel_hi:[0,0,0] cbsz:2 blgp:2
	v_fma_mix_f32 v158, v134, v1, v149 op_sel_hi:[0,0,1]
	v_exp_f32_e32 v158, v158
	v_fma_mix_f32 v159, v138, v99, v153 op_sel_hi:[0,0,1]
	v_exp_f32_e32 v159, v159
	v_fma_f32 v158, v158, v186, v186
	v_rcp_f32_e32 v158, v158
	v_add_f32_e32 v159, 1.0, v159
	v_rcp_f32_e32 v159, v159
	s_nop 0
	v_fma_mix_f32 v161, v158, v142, v157 op_sel_hi:[0,0,1]
	v_exp_f32_e32 v161, v161
	s_add_u32 s48, s48, s40
	v_add_f32_e32 v161, 1.0, v161
	v_rcp_f32_e32 v161, v161
	s_addc_u32 s49, s49, s41
	v_fma_f32 v162, v161, -2.0, 1.0
	v_sub_f32_e32 v163, v176, v162
	v_fma_f32 v176, v159, v163, v162
	v_fma_f32 v164, |v176|, s16, v117
	v_fma_f32 v165, |v176|, s17, v118
	v_fma_f32 v166, |v176|, s18, v119
	v_lshrrev_b32_e32 v167, 26, v176
	v_min3_u32 v164, v164, v165, v166
	v_bfi_b32 v168, 31, v164, v167
	v_lshrrev_b32_e32 v169, v181, v168
	global_store_short_d16_hi v185, v176, s[48:49]
	v_mul_u32_u24_dpp v170, v168, v180 quad_perm:[1,2,3,3] row_mask:0xf bank_mask:0xf bound_ctrl:1
	v_or_b32_e32 v171, v169, v170
	ds_write_b8 v184, v171 offset:416
	s_waitcnt lgkmcnt(0)
	s_barrier
	ds_read_b64 v[122:123], v106 offset:416
	ds_read_b64 v[124:125], v106 offset:424
	ds_read_b64 v[126:127], v106 offset:432
	s_barrier
	ds_read_b64 v[128:129], v106 offset:512
	ds_read_b64 v[130:131], v106 offset:520
	ds_read_b64 v[132:133], v106 offset:528
	s_add_i32 s44, s44, 16
	s_waitcnt lgkmcnt(3)
	v_mfma_scale_f32_16x16x128_f8f6f4 v[134:137], v[122:127], v[2:7], 0, v178, v115 op_sel_hi:[0,0,0] cbsz:2 blgp:2
	v_mfma_scale_f32_16x16x128_f8f6f4 v[138:141], v[122:127], v[14:19], 0, v178, v115 op_sel_hi:[0,0,0] cbsz:2 blgp:2
	v_mfma_scale_f32_16x16x128_f8f6f4 v[142:145], v[122:127], v[26:31], v[188:191], v178, v115 op_sel_hi:[0,0,0] cbsz:2 blgp:2
	v_mfma_scale_f32_16x16x128_f8f6f4 v[134:137], v[122:127], v[38:43], v[134:137], v179, v115 op_sel_hi:[0,0,0] cbsz:2 blgp:2
	v_mfma_scale_f32_16x16x128_f8f6f4 v[138:141], v[122:127], v[50:55], v[138:141], v179, v115 op_sel_hi:[0,0,0] cbsz:2 blgp:2
	v_mfma_scale_f32_16x16x128_f8f6f4 v[142:145], v[122:127], v[62:67], v[142:145], v179, v115 op_sel_hi:[0,0,0] cbsz:2 blgp:2
	s_waitcnt lgkmcnt(0)
	v_mfma_scale_f32_16x16x128_f8f6f4 v[134:137], v[128:133], v[8:13], v[134:137], v178, v115 op_sel_hi:[0,0,0] cbsz:2 blgp:2
	v_mfma_scale_f32_16x16x128_f8f6f4 v[134:137], v[128:133], v[44:49], v[134:137], v179, v115 op_sel_hi:[0,0,0] cbsz:2 blgp:2
	v_mfma_scale_f32_16x16x128_f8f6f4 v[138:141], v[128:133], v[20:25], v[138:141], v178, v115 op_sel_hi:[0,0,0] cbsz:2 blgp:2
	v_mfma_scale_f32_16x16x128_f8f6f4 v[138:141], v[128:133], v[56:61], v[138:141], v179, v115 op_sel_hi:[0,0,0] cbsz:2 blgp:2
	v_mfma_scale_f32_16x16x128_f8f6f4 v[142:145], v[128:133], v[32:37], v[142:145], v178, v115 op_sel_hi:[0,0,0] cbsz:2 blgp:2
	v_mfma_scale_f32_16x16x128_f8f6f4 v[142:145], v[128:133], v[68:73], v[142:145], v179, v115 op_sel_hi:[0,0,0] cbsz:2 blgp:2
	v_fma_mix_f32 v158, v134, v1, v149 op_sel:[0,0,1] op_sel_hi:[0,0,1]
	v_exp_f32_e32 v158, v158
	v_fma_mix_f32 v159, v138, v99, v153 op_sel:[0,0,1] op_sel_hi:[0,0,1]
	v_exp_f32_e32 v159, v159
	v_fma_f32 v158, v158, v186, v186
	v_rcp_f32_e32 v158, v158
	v_add_f32_e32 v159, 1.0, v159
	v_rcp_f32_e32 v159, v159
	s_nop 0
	v_fma_mix_f32 v161, v158, v142, v157 op_sel:[0,0,1] op_sel_hi:[0,0,1]
	v_exp_f32_e32 v161, v161
	s_add_u32 s48, s48, s40
	v_add_f32_e32 v161, 1.0, v161
	v_rcp_f32_e32 v161, v161
	s_addc_u32 s49, s49, s41
	v_fma_f32 v162, v161, -2.0, 1.0
	v_sub_f32_e32 v163, v176, v162
	v_fma_f32 v176, v159, v163, v162
	v_fma_f32 v164, |v176|, s16, v117
	v_fma_f32 v165, |v176|, s17, v118
	v_fma_f32 v166, |v176|, s18, v119
	v_lshrrev_b32_e32 v167, 26, v176
	v_min3_u32 v164, v164, v165, v166
	v_bfi_b32 v168, 31, v164, v167
	v_lshrrev_b32_e32 v169, v181, v168
	global_store_short_d16_hi v185, v176, s[48:49]
	v_mul_u32_u24_dpp v170, v168, v180 quad_perm:[1,2,3,3] row_mask:0xf bank_mask:0xf bound_ctrl:1
	v_or_b32_e32 v171, v169, v170
	ds_write_b8 v184, v171
	s_waitcnt lgkmcnt(0)
	s_barrier
	ds_read_b64 v[122:123], v106 offset:0
	ds_read_b64 v[124:125], v106 offset:8
	ds_read_b64 v[126:127], v106 offset:16
	s_cmp_lt_i32 s44, s45
	s_barrier
	s_cbranch_scc1 .Lscan_loop_a_st
	s_branch .Lscan_exit_st
.Lscan_loop_b_st:
	ds_read_b64 v[128:129], v106 offset:96
	ds_read_b64 v[130:131], v106 offset:104
	ds_read_b64 v[132:133], v106 offset:112
	s_waitcnt vmcnt(8)
	global_load_dwordx4 v[146:149], v[196:197], off
	global_load_dwordx4 v[150:153], v[196:197], off offset:512
	global_load_dwordx4 v[154:157], v[196:197], off offset:1024
	v_lshl_add_u64 v[196:197], v[196:197], 0, s[42:43]
	s_waitcnt lgkmcnt(3)
	v_mfma_scale_f32_16x16x128_f8f6f4 v[134:137], v[122:127], v[2:7], 0, v178, v115 op_sel_hi:[0,0,0] cbsz:2 blgp:2
	v_mfma_scale_f32_16x16x128_f8f6f4 v[138:141], v[122:127], v[14:19], 0, v178, v115 op_sel_hi:[0,0,0] cbsz:2 blgp:2
	v_mfma_scale_f32_16x16x128_f8f6f4 v[142:145], v[122:127], v[26:31], v[188:191], v178, v115 op_sel_hi:[0,0,0] cbsz:2 blgp:2
	v_mfma_scale_f32_16x16x128_f8f6f4 v[134:137], v[122:127], v[38:43], v[134:137], v179, v115 op_sel_hi:[0,0,0] cbsz:2 blgp:2
	v_mfma_scale_f32_16x16x128_f8f6f4 v[138:141], v[122:127], v[50:55], v[138:141], v179, v115 op_sel_hi:[0,0,0] cbsz:2 blgp:2
	v_mfma_scale_f32_16x16x128_f8f6f4 v[142:145], v[122:127], v[62:67], v[142:145], v179, v115 op_sel_hi:[0,0,0] cbsz:2 blgp:2
	s_waitcnt lgkmcnt(0)
	v_mfma_scale_f32_16x16x128_f8f6f4 v[134:137], v[128:133], v[8:13], v[134:137], v178, v115 op_sel_hi:[0,0,0] cbsz:2 blgp:2
	v_mfma_scale_f32_16x16x128_f8f6f4 v[134:137], v[128:133], v[44:49], v[134:137], v179, v115 op_sel_hi:[0,0,0] cbsz:2 blgp:2
	v_mfma_scale_f32_16x16x128_f8f6f4 v[138:141], v[128:133], v[20:25], v[138:141], v178, v115 op_sel_hi:[0,0,0] cbsz:2 blgp:2
	v_mfma_scale_f32_16x16x128_f8f6f4 v[138:141], v[128:133], v[56:61], v[138:141], v179, v115 op_sel_hi:[0,0,0] cbsz:2 blgp:2
	v_mfma_scale_f32_16x16x128_f8f6f4 v[142:145], v[128:133], v[32:37], v[142:145], v178, v115 op_sel_hi:[0,0,0] cbsz:2 blgp:2
	v_mfma_scale_f32_16x16x128_f8f6f4 v[142:145], v[128:133], v[68:73], v[142:145], v179, v115 op_sel_hi:[0,0,0] cbsz:2 blgp:2
	v_fma_mix_f32 v158, v134, v1, v82 op_sel_hi:[0,0,1]
	v_exp_f32_e32 v158, v158
	v_fma_mix_f32 v159, v138, v99, v74 op_sel_hi:[0,0,1]
	v_exp_f32_e32 v159, v159
	v_fma_f32 v158, v158, v186, v186
	v_rcp_f32_e32 v158, v158
	v_add_f32_e32 v159, 1.0, v159
	v_rcp_f32_e32 v159, v159
	s_nop 0
	v_fma_mix_f32 v161, v158, v142, v78 op_sel_hi:[0,0,1]
	v_exp_f32_e32 v161, v161
	s_add_u32 s48, s48, s40
	v_add_f32_e32 v161, 1.0, v161
	v_rcp_f32_e32 v161, v161
	s_addc_u32 s49, s49, s41
	v_fma_f32 v162, v161, -2.0, 1.0
	v_sub_f32_e32 v163, v176, v162
	v_fma_f32 v176, v159, v163, v162
	v_fma_f32 v164, |v176|, s16, v117
	v_fma_f32 v165, |v176|, s17, v118
	v_fma_f32 v166, |v176|, s18, v119
	v_lshrrev_b32_e32 v167, 26, v176
	v_min3_u32 v164, v164, v165, v166
	v_bfi_b32 v168, 31, v164, v167
	v_lshrrev_b32_e32 v169, v181, v168
	global_store_short_d16_hi v185, v176, s[48:49]
	v_mul_u32_u24_dpp v170, v168, v180 quad_perm:[1,2,3,3] row_mask:0xf bank_mask:0xf bound_ctrl:1
	v_or_b32_e32 v171, v169, v170
	ds_write_b8 v184, v171 offset:416
	s_barrier
	ds_read_b64 v[122:123], v106 offset:416
	ds_read_b64 v[124:125], v106 offset:424
	ds_read_b64 v[126:127], v106 offset:432
	s_waitcnt lgkmcnt(3)
	s_barrier
	ds_read_b64 v[128:129], v106 offset:512
	ds_read_b64 v[130:131], v106 offset:520
	ds_read_b64 v[132:133], v106 offset:528
	s_waitcnt lgkmcnt(3)
	v_mfma_scale_f32_16x16x128_f8f6f4 v[134:137], v[122:127], v[2:7], 0, v178, v115 op_sel_hi:[0,0,0] cbsz:2 blgp:2
	v_mfma_scale_f32_16x16x128_f8f6f4 v[138:141], v[122:127], v[14:19], 0, v178, v115 op_sel_hi:[0,0,0] cbsz:2 blgp:2
	v_mfma_scale_f32_16x16x128_f8f6f4 v[142:145], v[122:127], v[26:31], v[188:191], v178, v115 op_sel_hi:[0,0,0] cbsz:2 blgp:2
	v_mfma_scale_f32_16x16x128_f8f6f4 v[134:137], v[122:127], v[38:43], v[134:137], v179, v115 op_sel_hi:[0,0,0] cbsz:2 blgp:2
	v_mfma_scale_f32_16x16x128_f8f6f4 v[138:141], v[122:127], v[50:55], v[138:141], v179, v115 op_sel_hi:[0,0,0] cbsz:2 blgp:2
	v_mfma_scale_f32_16x16x128_f8f6f4 v[142:145], v[122:127], v[62:67], v[142:145], v179, v115 op_sel_hi:[0,0,0] cbsz:2 blgp:2
	s_waitcnt lgkmcnt(0)
	v_mfma_scale_f32_16x16x128_f8f6f4 v[134:137], v[128:133], v[8:13], v[134:137], v178, v115 op_sel_hi:[0,0,0] cbsz:2 blgp:2
	v_mfma_scale_f32_16x16x128_f8f6f4 v[134:137], v[128:133], v[44:49], v[134:137], v179, v115 op_sel_hi:[0,0,0] cbsz:2 blgp:2
	v_mfma_scale_f32_16x16x128_f8f6f4 v[138:141], v[128:133], v[20:25], v[138:141], v178, v115 op_sel_hi:[0,0,0] cbsz:2 blgp:2
	v_mfma_scale_f32_16x16x128_f8f6f4 v[138:141], v[128:133], v[56:61], v[138:141], v179, v115 op_sel_hi:[0,0,0] cbsz:2 blgp:2
	v_mfma_scale_f32_16x16x128_f8f6f4 v[142:145], v[128:133], v[32:37], v[142:145], v178, v115 op_sel_hi:[0,0,0] cbsz:2 blgp:2
	v_mfma_scale_f32_16x16x128_f8f6f4 v[142:145], v[128:133], v[68:73], v[142:145], v179, v115 op_sel_hi:[0,0,0] cbsz:2 blgp:2
	v_fma_mix_f32 v158, v134, v1, v82 op_sel:[0,0,1] op_sel_hi:[0,0,1]
	v_exp_f32_e32 v158, v158
	v_fma_mix_f32 v159, v138, v99, v74 op_sel:[0,0,1] op_sel_hi:[0,0,1]
	v_exp_f32_e32 v159, v159
	v_fma_f32 v158, v158, v186, v186
	v_rcp_f32_e32 v158, v158
	v_add_f32_e32 v159, 1.0, v159
	v_rcp_f32_e32 v159, v159
	s_nop 0
	v_fma_mix_f32 v161, v158, v142, v78 op_sel:[0,0,1] op_sel_hi:[0,0,1]
	v_exp_f32_e32 v161, v161
	s_add_u32 s48, s48, s40
	v_add_f32_e32 v161, 1.0, v161
	v_rcp_f32_e32 v161, v161
	s_addc_u32 s49, s49, s41
	v_fma_f32 v162, v161, -2.0, 1.0
	v_sub_f32_e32 v163, v176, v162
	v_fma_f32 v176, v159, v163, v162
	v_fma_f32 v164, |v176|, s16, v117
	v_fma_f32 v165, |v176|, s17, v118
	v_fma_f32 v166, |v176|, s18, v119
	v_lshrrev_b32_e32 v167, 26, v176
	v_min3_u32 v164, v164, v165, v166
	v_bfi_b32 v168, 31, v164, v167
	v_lshrrev_b32_e32 v169, v181, v168
	global_store_short_d16_hi v185, v176, s[48:49]
	v_mul_u32_u24_dpp v170, v168, v180 quad_perm:[1,2,3,3] row_mask:0xf bank_mask:0xf bound_ctrl:1
	v_or_b32_e32 v171, v169, v170
	ds_write_b8 v184, v171
	s_barrier
	ds_read_b64 v[122:123], v106 offset:0
	ds_read_b64 v[124:125], v106 offset:8
	ds_read_b64 v[126:127], v106 offset:16
	s_waitcnt lgkmcnt(3)
	s_barrier
	ds_read_b64 v[128:129], v106 offset:96
	ds_read_b64 v[130:131], v106 offset:104
	ds_read_b64 v[132:133], v106 offset:112
	s_waitcnt lgkmcnt(3)
	v_mfma_scale_f32_16x16x128_f8f6f4 v[134:137], v[122:127], v[2:7], 0, v178, v115 op_sel_hi:[0,0,0] cbsz:2 blgp:2
	v_mfma_scale_f32_16x16x128_f8f6f4 v[138:141], v[122:127], v[14:19], 0, v178, v115 op_sel_hi:[0,0,0] cbsz:2 blgp:2
	v_mfma_scale_f32_16x16x128_f8f6f4 v[142:145], v[122:127], v[26:31], v[188:191], v178, v115 op_sel_hi:[0,0,0] cbsz:2 blgp:2
	v_mfma_scale_f32_16x16x128_f8f6f4 v[134:137], v[122:127], v[38:43], v[134:137], v179, v115 op_sel_hi:[0,0,0] cbsz:2 blgp:2
	v_mfma_scale_f32_16x16x128_f8f6f4 v[138:141], v[122:127], v[50:55], v[138:141], v179, v115 op_sel_hi:[0,0,0] cbsz:2 blgp:2
	v_mfma_scale_f32_16x16x128_f8f6f4 v[142:145], v[122:127], v[62:67], v[142:145], v179, v115 op_sel_hi:[0,0,0] cbsz:2 blgp:2
	s_waitcnt lgkmcnt(0)
	v_mfma_scale_f32_16x16x128_f8f6f4 v[134:137], v[128:133], v[8:13], v[134:137], v178, v115 op_sel_hi:[0,0,0] cbsz:2 blgp:2
	v_mfma_scale_f32_16x16x128_f8f6f4 v[134:137], v[128:133], v[44:49], v[134:137], v179, v115 op_sel_hi:[0,0,0] cbsz:2 blgp:2
	v_mfma_scale_f32_16x16x128_f8f6f4 v[138:141], v[128:133], v[20:25], v[138:141], v178, v115 op_sel_hi:[0,0,0] cbsz:2 blgp:2
	v_mfma_scale_f32_16x16x128_f8f6f4 v[138:141], v[128:133], v[56:61], v[138:141], v179, v115 op_sel_hi:[0,0,0] cbsz:2 blgp:2
	v_mfma_scale_f32_16x16x128_f8f6f4 v[142:145], v[128:133], v[32:37], v[142:145], v178, v115 op_sel_hi:[0,0,0] cbsz:2 blgp:2
	v_mfma_scale_f32_16x16x128_f8f6f4 v[142:145], v[128:133], v[68:73], v[142:145], v179, v115 op_sel_hi:[0,0,0] cbsz:2 blgp:2
	v_fma_mix_f32 v158, v134, v1, v83 op_sel_hi:[0,0,1]
	v_exp_f32_e32 v158, v158
	v_fma_mix_f32 v159, v138, v99, v75 op_sel_hi:[0,0,1]
	v_exp_f32_e32 v159, v159
	v_fma_f32 v158, v158, v186, v186
	v_rcp_f32_e32 v158, v158
	v_add_f32_e32 v159, 1.0, v159
	v_rcp_f32_e32 v159, v159
	s_nop 0
	v_fma_mix_f32 v161, v158, v142, v79 op_sel_hi:[0,0,1]
	v_exp_f32_e32 v161, v161
	s_add_u32 s48, s48, s40
	v_add_f32_e32 v161, 1.0, v161
	v_rcp_f32_e32 v161, v161
	s_addc_u32 s49, s49, s41
	v_fma_f32 v162, v161, -2.0, 1.0
	v_sub_f32_e32 v163, v176, v162
	v_fma_f32 v176, v159, v163, v162
	v_fma_f32 v164, |v176|, s16, v117
	v_fma_f32 v165, |v176|, s17, v118
	v_fma_f32 v166, |v176|, s18, v119
	v_lshrrev_b32_e32 v167, 26, v176
	v_min3_u32 v164, v164, v165, v166
	v_bfi_b32 v168, 31, v164, v167
	v_lshrrev_b32_e32 v169, v181, v168
	global_store_short_d16_hi v185, v176, s[48:49]
	v_mul_u32_u24_dpp v170, v168, v180 quad_perm:[1,2,3,3] row_mask:0xf bank_mask:0xf bound_ctrl:1
	v_or_b32_e32 v171, v169, v170
	ds_write_b8 v184, v171 offset:416
	s_barrier
	ds_read_b64 v[122:123], v106 offset:416
	ds_read_b64 v[124:125], v106 offset:424
	ds_read_b64 v[126:127], v106 offset:432
	s_waitcnt lgkmcnt(3)
	s_barrier
	ds_read_b64 v[128:129], v106 offset:512
	ds_read_b64 v[130:131], v106 offset:520
	ds_read_b64 v[132:133], v106 offset:528
	s_waitcnt lgkmcnt(3)
	v_mfma_scale_f32_16x16x128_f8f6f4 v[134:137], v[122:127], v[2:7], 0, v178, v115 op_sel_hi:[0,0,0] cbsz:2 blgp:2
	v_mfma_scale_f32_16x16x128_f8f6f4 v[138:141], v[122:127], v[14:19], 0, v178, v115 op_sel_hi:[0,0,0] cbsz:2 blgp:2
	v_mfma_scale_f32_16x16x128_f8f6f4 v[142:145], v[122:127], v[26:31], v[188:191], v178, v115 op_sel_hi:[0,0,0] cbsz:2 blgp:2
	v_mfma_scale_f32_16x16x128_f8f6f4 v[134:137], v[122:127], v[38:43], v[134:137], v179, v115 op_sel_hi:[0,0,0] cbsz:2 blgp:2
	v_mfma_scale_f32_16x16x128_f8f6f4 v[138:141], v[122:127], v[50:55], v[138:141], v179, v115 op_sel_hi:[0,0,0] cbsz:2 blgp:2
	v_mfma_scale_f32_16x16x128_f8f6f4 v[142:145], v[122:127], v[62:67], v[142:145], v179, v115 op_sel_hi:[0,0,0] cbsz:2 blgp:2
	s_waitcnt lgkmcnt(0)
	v_mfma_scale_f32_16x16x128_f8f6f4 v[134:137], v[128:133], v[8:13], v[134:137], v178, v115 op_sel_hi:[0,0,0] cbsz:2 blgp:2
	v_mfma_scale_f32_16x16x128_f8f6f4 v[134:137], v[128:133], v[44:49], v[134:137], v179, v115 op_sel_hi:[0,0,0] cbsz:2 blgp:2
	v_mfma_scale_f32_16x16x128_f8f6f4 v[138:141], v[128:133], v[20:25], v[138:141], v178, v115 op_sel_hi:[0,0,0] cbsz:2 blgp:2
	v_mfma_scale_f32_16x16x128_f8f6f4 v[138:141], v[128:133], v[56:61], v[138:141], v179, v115 op_sel_hi:[0,0,0] cbsz:2 blgp:2
	v_mfma_scale_f32_16x16x128_f8f6f4 v[142:145], v[128:133], v[32:37], v[142:145], v178, v115 op_sel_hi:[0,0,0] cbsz:2 blgp:2
	v_mfma_scale_f32_16x16x128_f8f6f4 v[142:145], v[128:133], v[68:73], v[142:145], v179, v115 op_sel_hi:[0,0,0] cbsz:2 blgp:2
	v_fma_mix_f32 v158, v134, v1, v83 op_sel:[0,0,1] op_sel_hi:[0,0,1]
	v_exp_f32_e32 v158, v158
	v_fma_mix_f32 v159, v138, v99, v75 op_sel:[0,0,1] op_sel_hi:[0,0,1]
	v_exp_f32_e32 v159, v159
	v_fma_f32 v158, v158, v186, v186
	v_rcp_f32_e32 v158, v158
	v_add_f32_e32 v159, 1.0, v159
	v_rcp_f32_e32 v159, v159
	s_nop 0
	v_fma_mix_f32 v161, v158, v142, v79 op_sel:[0,0,1] op_sel_hi:[0,0,1]
	v_exp_f32_e32 v161, v161
	s_add_u32 s48, s48, s40
	v_add_f32_e32 v161, 1.0, v161
	v_rcp_f32_e32 v161, v161
	s_addc_u32 s49, s49, s41
	v_fma_f32 v162, v161, -2.0, 1.0
	v_sub_f32_e32 v163, v176, v162
	v_fma_f32 v176, v159, v163, v162
	v_fma_f32 v164, |v176|, s16, v117
	v_fma_f32 v165, |v176|, s17, v118
	v_fma_f32 v166, |v176|, s18, v119
	v_lshrrev_b32_e32 v167, 26, v176
	v_min3_u32 v164, v164, v165, v166
	v_bfi_b32 v168, 31, v164, v167
	v_lshrrev_b32_e32 v169, v181, v168
	global_store_short_d16_hi v185, v176, s[48:49]
	v_mul_u32_u24_dpp v170, v168, v180 quad_perm:[1,2,3,3] row_mask:0xf bank_mask:0xf bound_ctrl:1
	v_or_b32_e32 v171, v169, v170
	ds_write_b8 v184, v171
	s_barrier
	ds_read_b64 v[122:123], v106 offset:0
	ds_read_b64 v[124:125], v106 offset:8
	ds_read_b64 v[126:127], v106 offset:16
	s_waitcnt lgkmcnt(3)
	s_barrier
	ds_read_b64 v[128:129], v106 offset:96
	ds_read_b64 v[130:131], v106 offset:104
	ds_read_b64 v[132:133], v106 offset:112
	s_waitcnt lgkmcnt(3)
	v_mfma_scale_f32_16x16x128_f8f6f4 v[134:137], v[122:127], v[2:7], 0, v178, v115 op_sel_hi:[0,0,0] cbsz:2 blgp:2
	v_mfma_scale_f32_16x16x128_f8f6f4 v[138:141], v[122:127], v[14:19], 0, v178, v115 op_sel_hi:[0,0,0] cbsz:2 blgp:2
	v_mfma_scale_f32_16x16x128_f8f6f4 v[142:145], v[122:127], v[26:31], v[188:191], v178, v115 op_sel_hi:[0,0,0] cbsz:2 blgp:2
	v_mfma_scale_f32_16x16x128_f8f6f4 v[134:137], v[122:127], v[38:43], v[134:137], v179, v115 op_sel_hi:[0,0,0] cbsz:2 blgp:2
	v_mfma_scale_f32_16x16x128_f8f6f4 v[138:141], v[122:127], v[50:55], v[138:141], v179, v115 op_sel_hi:[0,0,0] cbsz:2 blgp:2
	v_mfma_scale_f32_16x16x128_f8f6f4 v[142:145], v[122:127], v[62:67], v[142:145], v179, v115 op_sel_hi:[0,0,0] cbsz:2 blgp:2
	s_waitcnt lgkmcnt(0)
	v_mfma_scale_f32_16x16x128_f8f6f4 v[134:137], v[128:133], v[8:13], v[134:137], v178, v115 op_sel_hi:[0,0,0] cbsz:2 blgp:2
	v_mfma_scale_f32_16x16x128_f8f6f4 v[134:137], v[128:133], v[44:49], v[134:137], v179, v115 op_sel_hi:[0,0,0] cbsz:2 blgp:2
	v_mfma_scale_f32_16x16x128_f8f6f4 v[138:141], v[128:133], v[20:25], v[138:141], v178, v115 op_sel_hi:[0,0,0] cbsz:2 blgp:2
	v_mfma_scale_f32_16x16x128_f8f6f4 v[138:141], v[128:133], v[56:61], v[138:141], v179, v115 op_sel_hi:[0,0,0] cbsz:2 blgp:2
	v_mfma_scale_f32_16x16x128_f8f6f4 v[142:145], v[128:133], v[32:37], v[142:145], v178, v115 op_sel_hi:[0,0,0] cbsz:2 blgp:2
	v_mfma_scale_f32_16x16x128_f8f6f4 v[142:145], v[128:133], v[68:73], v[142:145], v179, v115 op_sel_hi:[0,0,0] cbsz:2 blgp:2
	v_fma_mix_f32 v158, v134, v1, v84 op_sel_hi:[0,0,1]
	v_exp_f32_e32 v158, v158
	v_fma_mix_f32 v159, v138, v99, v76 op_sel_hi:[0,0,1]
	v_exp_f32_e32 v159, v159
	v_fma_f32 v158, v158, v186, v186
	v_rcp_f32_e32 v158, v158
	v_add_f32_e32 v159, 1.0, v159
	v_rcp_f32_e32 v159, v159
	s_nop 0
	v_fma_mix_f32 v161, v158, v142, v80 op_sel_hi:[0,0,1]
	v_exp_f32_e32 v161, v161
	s_add_u32 s48, s48, s40
	v_add_f32_e32 v161, 1.0, v161
	v_rcp_f32_e32 v161, v161
	s_addc_u32 s49, s49, s41
	v_fma_f32 v162, v161, -2.0, 1.0
	v_sub_f32_e32 v163, v176, v162
	v_fma_f32 v176, v159, v163, v162
	v_fma_f32 v164, |v176|, s16, v117
	v_fma_f32 v165, |v176|, s17, v118
	v_fma_f32 v166, |v176|, s18, v119
	v_lshrrev_b32_e32 v167, 26, v176
	v_min3_u32 v164, v164, v165, v166
	v_bfi_b32 v168, 31, v164, v167
	v_lshrrev_b32_e32 v169, v181, v168
	global_store_short_d16_hi v185, v176, s[48:49]
	v_mul_u32_u24_dpp v170, v168, v180 quad_perm:[1,2,3,3] row_mask:0xf bank_mask:0xf bound_ctrl:1
	v_or_b32_e32 v171, v169, v170
	ds_write_b8 v184, v171 offset:416
	s_barrier
	ds_read_b64 v[122:123], v106 offset:416
	ds_read_b64 v[124:125], v106 offset:424
	ds_read_b64 v[126:127], v106 offset:432
	s_waitcnt lgkmcnt(3)
	s_barrier
	ds_read_b64 v[128:129], v106 offset:512
	ds_read_b64 v[130:131], v106 offset:520
	ds_read_b64 v[132:133], v106 offset:528
	s_waitcnt lgkmcnt(3)
	v_mfma_scale_f32_16x16x128_f8f6f4 v[134:137], v[122:127], v[2:7], 0, v178, v115 op_sel_hi:[0,0,0] cbsz:2 blgp:2
	v_mfma_scale_f32_16x16x128_f8f6f4 v[138:141], v[122:127], v[14:19], 0, v178, v115 op_sel_hi:[0,0,0] cbsz:2 blgp:2
	v_mfma_scale_f32_16x16x128_f8f6f4 v[142:145], v[122:127], v[26:31], v[188:191], v178, v115 op_sel_hi:[0,0,0] cbsz:2 blgp:2
	v_mfma_scale_f32_16x16x128_f8f6f4 v[134:137], v[122:127], v[38:43], v[134:137], v179, v115 op_sel_hi:[0,0,0] cbsz:2 blgp:2
	v_mfma_scale_f32_16x16x128_f8f6f4 v[138:141], v[122:127], v[50:55], v[138:141], v179, v115 op_sel_hi:[0,0,0] cbsz:2 blgp:2
	v_mfma_scale_f32_16x16x128_f8f6f4 v[142:145], v[122:127], v[62:67], v[142:145], v179, v115 op_sel_hi:[0,0,0] cbsz:2 blgp:2
	s_waitcnt lgkmcnt(0)
	v_mfma_scale_f32_16x16x128_f8f6f4 v[134:137], v[128:133], v[8:13], v[134:137], v178, v115 op_sel_hi:[0,0,0] cbsz:2 blgp:2
	v_mfma_scale_f32_16x16x128_f8f6f4 v[134:137], v[128:133], v[44:49], v[134:137], v179, v115 op_sel_hi:[0,0,0] cbsz:2 blgp:2
	v_mfma_scale_f32_16x16x128_f8f6f4 v[138:141], v[128:133], v[20:25], v[138:141], v178, v115 op_sel_hi:[0,0,0] cbsz:2 blgp:2
	v_mfma_scale_f32_16x16x128_f8f6f4 v[138:141], v[128:133], v[56:61], v[138:141], v179, v115 op_sel_hi:[0,0,0] cbsz:2 blgp:2
	v_mfma_scale_f32_16x16x128_f8f6f4 v[142:145], v[128:133], v[32:37], v[142:145], v178, v115 op_sel_hi:[0,0,0] cbsz:2 blgp:2
	v_mfma_scale_f32_16x16x128_f8f6f4 v[142:145], v[128:133], v[68:73], v[142:145], v179, v115 op_sel_hi:[0,0,0] cbsz:2 blgp:2
	v_fma_mix_f32 v158, v134, v1, v84 op_sel:[0,0,1] op_sel_hi:[0,0,1]
	v_exp_f32_e32 v158, v158
	v_fma_mix_f32 v159, v138, v99, v76 op_sel:[0,0,1] op_sel_hi:[0,0,1]
	v_exp_f32_e32 v159, v159
	v_fma_f32 v158, v158, v186, v186
	v_rcp_f32_e32 v158, v158
	v_add_f32_e32 v159, 1.0, v159
	v_rcp_f32_e32 v159, v159
	s_nop 0
	v_fma_mix_f32 v161, v158, v142, v80 op_sel:[0,0,1] op_sel_hi:[0,0,1]
	v_exp_f32_e32 v161, v161
	s_add_u32 s48, s48, s40
	v_add_f32_e32 v161, 1.0, v161
	v_rcp_f32_e32 v161, v161
	s_addc_u32 s49, s49, s41
	v_fma_f32 v162, v161, -2.0, 1.0
	v_sub_f32_e32 v163, v176, v162
	v_fma_f32 v176, v159, v163, v162
	v_fma_f32 v164, |v176|, s16, v117
	v_fma_f32 v165, |v176|, s17, v118
	v_fma_f32 v166, |v176|, s18, v119
	v_lshrrev_b32_e32 v167, 26, v176
	v_min3_u32 v164, v164, v165, v166
	v_bfi_b32 v168, 31, v164, v167
	v_lshrrev_b32_e32 v169, v181, v168
	global_store_short_d16_hi v185, v176, s[48:49]
	v_mul_u32_u24_dpp v170, v168, v180 quad_perm:[1,2,3,3] row_mask:0xf bank_mask:0xf bound_ctrl:1
	v_or_b32_e32 v171, v169, v170
	ds_write_b8 v184, v171
	s_barrier
	ds_read_b64 v[122:123], v106 offset:0
	ds_read_b64 v[124:125], v106 offset:8
	ds_read_b64 v[126:127], v106 offset:16
	s_waitcnt lgkmcnt(3)
	s_barrier
	ds_read_b64 v[128:129], v106 offset:96
	ds_read_b64 v[130:131], v106 offset:104
	ds_read_b64 v[132:133], v106 offset:112
	s_waitcnt lgkmcnt(3)
	v_mfma_scale_f32_16x16x128_f8f6f4 v[134:137], v[122:127], v[2:7], 0, v178, v115 op_sel_hi:[0,0,0] cbsz:2 blgp:2
	v_mfma_scale_f32_16x16x128_f8f6f4 v[138:141], v[122:127], v[14:19], 0, v178, v115 op_sel_hi:[0,0,0] cbsz:2 blgp:2
	v_mfma_scale_f32_16x16x128_f8f6f4 v[142:145], v[122:127], v[26:31], v[188:191], v178, v115 op_sel_hi:[0,0,0] cbsz:2 blgp:2
	v_mfma_scale_f32_16x16x128_f8f6f4 v[134:137], v[122:127], v[38:43], v[134:137], v179, v115 op_sel_hi:[0,0,0] cbsz:2 blgp:2
	v_mfma_scale_f32_16x16x128_f8f6f4 v[138:141], v[122:127], v[50:55], v[138:141], v179, v115 op_sel_hi:[0,0,0] cbsz:2 blgp:2
	v_mfma_scale_f32_16x16x128_f8f6f4 v[142:145], v[122:127], v[62:67], v[142:145], v179, v115 op_sel_hi:[0,0,0] cbsz:2 blgp:2
	s_waitcnt lgkmcnt(0)
	v_mfma_scale_f32_16x16x128_f8f6f4 v[134:137], v[128:133], v[8:13], v[134:137], v178, v115 op_sel_hi:[0,0,0] cbsz:2 blgp:2
	v_mfma_scale_f32_16x16x128_f8f6f4 v[134:137], v[128:133], v[44:49], v[134:137], v179, v115 op_sel_hi:[0,0,0] cbsz:2 blgp:2
	v_mfma_scale_f32_16x16x128_f8f6f4 v[138:141], v[128:133], v[20:25], v[138:141], v178, v115 op_sel_hi:[0,0,0] cbsz:2 blgp:2
	v_mfma_scale_f32_16x16x128_f8f6f4 v[138:141], v[128:133], v[56:61], v[138:141], v179, v115 op_sel_hi:[0,0,0] cbsz:2 blgp:2
	v_mfma_scale_f32_16x16x128_f8f6f4 v[142:145], v[128:133], v[32:37], v[142:145], v178, v115 op_sel_hi:[0,0,0] cbsz:2 blgp:2
	v_mfma_scale_f32_16x16x128_f8f6f4 v[142:145], v[128:133], v[68:73], v[142:145], v179, v115 op_sel_hi:[0,0,0] cbsz:2 blgp:2
	v_fma_mix_f32 v158, v134, v1, v85 op_sel_hi:[0,0,1]
	v_exp_f32_e32 v158, v158
	v_fma_mix_f32 v159, v138, v99, v77 op_sel_hi:[0,0,1]
	v_exp_f32_e32 v159, v159
	v_fma_f32 v158, v158, v186, v186
	v_rcp_f32_e32 v158, v158
	v_add_f32_e32 v159, 1.0, v159
	v_rcp_f32_e32 v159, v159
	s_nop 0
	v_fma_mix_f32 v161, v158, v142, v81 op_sel_hi:[0,0,1]
	v_exp_f32_e32 v161, v161
	s_add_u32 s48, s48, s40
	v_add_f32_e32 v161, 1.0, v161
	v_rcp_f32_e32 v161, v161
	s_addc_u32 s49, s49, s41
	v_fma_f32 v162, v161, -2.0, 1.0
	v_sub_f32_e32 v163, v176, v162
	v_fma_f32 v176, v159, v163, v162
	v_fma_f32 v164, |v176|, s16, v117
	v_fma_f32 v165, |v176|, s17, v118
	v_fma_f32 v166, |v176|, s18, v119
	v_lshrrev_b32_e32 v167, 26, v176
	v_min3_u32 v164, v164, v165, v166
	v_bfi_b32 v168, 31, v164, v167
	v_lshrrev_b32_e32 v169, v181, v168
	global_store_short_d16_hi v185, v176, s[48:49]
	v_mul_u32_u24_dpp v170, v168, v180 quad_perm:[1,2,3,3] row_mask:0xf bank_mask:0xf bound_ctrl:1
	v_or_b32_e32 v171, v169, v170
	ds_write_b8 v184, v171 offset:416
	s_barrier
	ds_read_b64 v[122:123], v106 offset:416
	ds_read_b64 v[124:125], v106 offset:424
	ds_read_b64 v[126:127], v106 offset:432
	s_waitcnt lgkmcnt(3)
	s_barrier
	ds_read_b64 v[128:129], v106 offset:512
	ds_read_b64 v[130:131], v106 offset:520
	ds_read_b64 v[132:133], v106 offset:528
	s_waitcnt lgkmcnt(3)
	v_mfma_scale_f32_16x16x128_f8f6f4 v[134:137], v[122:127], v[2:7], 0, v178, v115 op_sel_hi:[0,0,0] cbsz:2 blgp:2
	v_mfma_scale_f32_16x16x128_f8f6f4 v[138:141], v[122:127], v[14:19], 0, v178, v115 op_sel_hi:[0,0,0] cbsz:2 blgp:2
	v_mfma_scale_f32_16x16x128_f8f6f4 v[142:145], v[122:127], v[26:31], v[188:191], v178, v115 op_sel_hi:[0,0,0] cbsz:2 blgp:2
	v_mfma_scale_f32_16x16x128_f8f6f4 v[134:137], v[122:127], v[38:43], v[134:137], v179, v115 op_sel_hi:[0,0,0] cbsz:2 blgp:2
	v_mfma_scale_f32_16x16x128_f8f6f4 v[138:141], v[122:127], v[50:55], v[138:141], v179, v115 op_sel_hi:[0,0,0] cbsz:2 blgp:2
	v_mfma_scale_f32_16x16x128_f8f6f4 v[142:145], v[122:127], v[62:67], v[142:145], v179, v115 op_sel_hi:[0,0,0] cbsz:2 blgp:2
	s_waitcnt lgkmcnt(0)
	v_mfma_scale_f32_16x16x128_f8f6f4 v[134:137], v[128:133], v[8:13], v[134:137], v178, v115 op_sel_hi:[0,0,0] cbsz:2 blgp:2
	v_mfma_scale_f32_16x16x128_f8f6f4 v[134:137], v[128:133], v[44:49], v[134:137], v179, v115 op_sel_hi:[0,0,0] cbsz:2 blgp:2
	v_mfma_scale_f32_16x16x128_f8f6f4 v[138:141], v[128:133], v[20:25], v[138:141], v178, v115 op_sel_hi:[0,0,0] cbsz:2 blgp:2
	v_mfma_scale_f32_16x16x128_f8f6f4 v[138:141], v[128:133], v[56:61], v[138:141], v179, v115 op_sel_hi:[0,0,0] cbsz:2 blgp:2
	v_mfma_scale_f32_16x16x128_f8f6f4 v[142:145], v[128:133], v[32:37], v[142:145], v178, v115 op_sel_hi:[0,0,0] cbsz:2 blgp:2
	v_mfma_scale_f32_16x16x128_f8f6f4 v[142:145], v[128:133], v[68:73], v[142:145], v179, v115 op_sel_hi:[0,0,0] cbsz:2 blgp:2
	v_fma_mix_f32 v158, v134, v1, v85 op_sel:[0,0,1] op_sel_hi:[0,0,1]
	v_exp_f32_e32 v158, v158
	v_fma_mix_f32 v159, v138, v99, v77 op_sel:[0,0,1] op_sel_hi:[0,0,1]
	v_exp_f32_e32 v159, v159
	v_fma_f32 v158, v158, v186, v186
	v_rcp_f32_e32 v158, v158
	v_add_f32_e32 v159, 1.0, v159
	v_rcp_f32_e32 v159, v159
	s_nop 0
	v_fma_mix_f32 v161, v158, v142, v81 op_sel:[0,0,1] op_sel_hi:[0,0,1]
	v_exp_f32_e32 v161, v161
	s_add_u32 s48, s48, s40
	v_add_f32_e32 v161, 1.0, v161
	v_rcp_f32_e32 v161, v161
	s_addc_u32 s49, s49, s41
	v_fma_f32 v162, v161, -2.0, 1.0
	v_sub_f32_e32 v163, v176, v162
	v_fma_f32 v176, v159, v163, v162
	v_fma_f32 v164, |v176|, s16, v117
	v_fma_f32 v165, |v176|, s17, v118
	v_fma_f32 v166, |v176|, s18, v119
	v_lshrrev_b32_e32 v167, 26, v176
	v_min3_u32 v164, v164, v165, v166
	v_bfi_b32 v168, 31, v164, v167
	v_lshrrev_b32_e32 v169, v181, v168
	global_store_short_d16_hi v185, v176, s[48:49]
	v_mul_u32_u24_dpp v170, v168, v180 quad_perm:[1,2,3,3] row_mask:0xf bank_mask:0xf bound_ctrl:1
	v_or_b32_e32 v171, v169, v170
	ds_write_b8 v184, v171
	s_barrier
	ds_read_b64 v[122:123], v106 offset:0
	ds_read_b64 v[124:125], v106 offset:8
	ds_read_b64 v[126:127], v106 offset:16
	s_waitcnt lgkmcnt(3)
	s_barrier
	ds_read_b64 v[128:129], v106 offset:96
	ds_read_b64 v[130:131], v106 offset:104
	ds_read_b64 v[132:133], v106 offset:112
	s_waitcnt vmcnt(8)
	global_load_dwordx4 v[82:85], v[196:197], off
	global_load_dwordx4 v[74:77], v[196:197], off offset:512
	global_load_dwordx4 v[78:81], v[196:197], off offset:1024
	v_lshl_add_u64 v[196:197], v[196:197], 0, s[42:43]
	s_waitcnt lgkmcnt(3)
	v_mfma_scale_f32_16x16x128_f8f6f4 v[134:137], v[122:127], v[2:7], 0, v178, v115 op_sel_hi:[0,0,0] cbsz:2 blgp:2
	v_mfma_scale_f32_16x16x128_f8f6f4 v[138:141], v[122:127], v[14:19], 0, v178, v115 op_sel_hi:[0,0,0] cbsz:2 blgp:2
	v_mfma_scale_f32_16x16x128_f8f6f4 v[142:145], v[122:127], v[26:31], v[188:191], v178, v115 op_sel_hi:[0,0,0] cbsz:2 blgp:2
	v_mfma_scale_f32_16x16x128_f8f6f4 v[134:137], v[122:127], v[38:43], v[134:137], v179, v115 op_sel_hi:[0,0,0] cbsz:2 blgp:2
	v_mfma_scale_f32_16x16x128_f8f6f4 v[138:141], v[122:127], v[50:55], v[138:141], v179, v115 op_sel_hi:[0,0,0] cbsz:2 blgp:2
	v_mfma_scale_f32_16x16x128_f8f6f4 v[142:145], v[122:127], v[62:67], v[142:145], v179, v115 op_sel_hi:[0,0,0] cbsz:2 blgp:2
	s_waitcnt lgkmcnt(0)
	v_mfma_scale_f32_16x16x128_f8f6f4 v[134:137], v[128:133], v[8:13], v[134:137], v178, v115 op_sel_hi:[0,0,0] cbsz:2 blgp:2
	v_mfma_scale_f32_16x16x128_f8f6f4 v[134:137], v[128:133], v[44:49], v[134:137], v179, v115 op_sel_hi:[0,0,0] cbsz:2 blgp:2
	v_mfma_scale_f32_16x16x128_f8f6f4 v[138:141], v[128:133], v[20:25], v[138:141], v178, v115 op_sel_hi:[0,0,0] cbsz:2 blgp:2
	v_mfma_scale_f32_16x16x128_f8f6f4 v[138:141], v[128:133], v[56:61], v[138:141], v179, v115 op_sel_hi:[0,0,0] cbsz:2 blgp:2
	v_mfma_scale_f32_16x16x128_f8f6f4 v[142:145], v[128:133], v[32:37], v[142:145], v178, v115 op_sel_hi:[0,0,0] cbsz:2 blgp:2
	v_mfma_scale_f32_16x16x128_f8f6f4 v[142:145], v[128:133], v[68:73], v[142:145], v179, v115 op_sel_hi:[0,0,0] cbsz:2 blgp:2
	v_fma_mix_f32 v158, v134, v1, v146 op_sel_hi:[0,0,1]
	v_exp_f32_e32 v158, v158
	v_fma_mix_f32 v159, v138, v99, v150 op_sel_hi:[0,0,1]
	v_exp_f32_e32 v159, v159
	v_fma_f32 v158, v158, v186, v186
	v_rcp_f32_e32 v158, v158
	v_add_f32_e32 v159, 1.0, v159
	v_rcp_f32_e32 v159, v159
	s_nop 0
	v_fma_mix_f32 v161, v158, v142, v154 op_sel_hi:[0,0,1]
	v_exp_f32_e32 v161, v161
	s_add_u32 s48, s48, s40
	v_add_f32_e32 v161, 1.0, v161
	v_rcp_f32_e32 v161, v161
	s_addc_u32 s49, s49, s41
	v_fma_f32 v162, v161, -2.0, 1.0
	v_sub_f32_e32 v163, v176, v162
	v_fma_f32 v176, v159, v163, v162
	v_fma_f32 v164, |v176|, s16, v117
	v_fma_f32 v165, |v176|, s17, v118
	v_fma_f32 v166, |v176|, s18, v119
	v_lshrrev_b32_e32 v167, 26, v176
	v_min3_u32 v164, v164, v165, v166
	v_bfi_b32 v168, 31, v164, v167
	v_lshrrev_b32_e32 v169, v181, v168
	global_store_short_d16_hi v185, v176, s[48:49]
	v_mul_u32_u24_dpp v170, v168, v180 quad_perm:[1,2,3,3] row_mask:0xf bank_mask:0xf bound_ctrl:1
	v_or_b32_e32 v171, v169, v170
	ds_write_b8 v184, v171 offset:416
	s_barrier
	ds_read_b64 v[122:123], v106 offset:416
	ds_read_b64 v[124:125], v106 offset:424
	ds_read_b64 v[126:127], v106 offset:432
	s_waitcnt lgkmcnt(3)
	s_barrier
	ds_read_b64 v[128:129], v106 offset:512
	ds_read_b64 v[130:131], v106 offset:520
	ds_read_b64 v[132:133], v106 offset:528
	s_waitcnt lgkmcnt(3)
	v_mfma_scale_f32_16x16x128_f8f6f4 v[134:137], v[122:127], v[2:7], 0, v178, v115 op_sel_hi:[0,0,0] cbsz:2 blgp:2
	v_mfma_scale_f32_16x16x128_f8f6f4 v[138:141], v[122:127], v[14:19], 0, v178, v115 op_sel_hi:[0,0,0] cbsz:2 blgp:2
	v_mfma_scale_f32_16x16x128_f8f6f4 v[142:145], v[122:127], v[26:31], v[188:191], v178, v115 op_sel_hi:[0,0,0] cbsz:2 blgp:2
	v_mfma_scale_f32_16x16x128_f8f6f4 v[134:137], v[122:127], v[38:43], v[134:137], v179, v115 op_sel_hi:[0,0,0] cbsz:2 blgp:2
	v_mfma_scale_f32_16x16x128_f8f6f4 v[138:141], v[122:127], v[50:55], v[138:141], v179, v115 op_sel_hi:[0,0,0] cbsz:2 blgp:2
	v_mfma_scale_f32_16x16x128_f8f6f4 v[142:145], v[122:127], v[62:67], v[142:145], v179, v115 op_sel_hi:[0,0,0] cbsz:2 blgp:2
	s_waitcnt lgkmcnt(0)
	v_mfma_scale_f32_16x16x128_f8f6f4 v[134:137], v[128:133], v[8:13], v[134:137], v178, v115 op_sel_hi:[0,0,0] cbsz:2 blgp:2
	v_mfma_scale_f32_16x16x128_f8f6f4 v[134:137], v[128:133], v[44:49], v[134:137], v179, v115 op_sel_hi:[0,0,0] cbsz:2 blgp:2
	v_mfma_scale_f32_16x16x128_f8f6f4 v[138:141], v[128:133], v[20:25], v[138:141], v178, v115 op_sel_hi:[0,0,0] cbsz:2 blgp:2
	v_mfma_scale_f32_16x16x128_f8f6f4 v[138:141], v[128:133], v[56:61], v[138:141], v179, v115 op_sel_hi:[0,0,0] cbsz:2 blgp:2
	v_mfma_scale_f32_16x16x128_f8f6f4 v[142:145], v[128:133], v[32:37], v[142:145], v178, v115 op_sel_hi:[0,0,0] cbsz:2 blgp:2
	v_mfma_scale_f32_16x16x128_f8f6f4 v[142:145], v[128:133], v[68:73], v[142:145], v179, v115 op_sel_hi:[0,0,0] cbsz:2 blgp:2
	v_fma_mix_f32 v158, v134, v1, v146 op_sel:[0,0,1] op_sel_hi:[0,0,1]
	v_exp_f32_e32 v158, v158
	v_fma_mix_f32 v159, v138, v99, v150 op_sel:[0,0,1] op_sel_hi:[0,0,1]
	v_exp_f32_e32 v159, v159
	v_fma_f32 v158, v158, v186, v186
	v_rcp_f32_e32 v158, v158
	v_add_f32_e32 v159, 1.0, v159
	v_rcp_f32_e32 v159, v159
	s_nop 0
	v_fma_mix_f32 v161, v158, v142, v154 op_sel:[0,0,1] op_sel_hi:[0,0,1]
	v_exp_f32_e32 v161, v161
	s_add_u32 s48, s48, s40
	v_add_f32_e32 v161, 1.0, v161
	v_rcp_f32_e32 v161, v161
	s_addc_u32 s49, s49, s41
	v_fma_f32 v162, v161, -2.0, 1.0
	v_sub_f32_e32 v163, v176, v162
	v_fma_f32 v176, v159, v163, v162
	v_fma_f32 v164, |v176|, s16, v117
	v_fma_f32 v165, |v176|, s17, v118
	v_fma_f32 v166, |v176|, s18, v119
	v_lshrrev_b32_e32 v167, 26, v176
	v_min3_u32 v164, v164, v165, v166
	v_bfi_b32 v168, 31, v164, v167
	v_lshrrev_b32_e32 v169, v181, v168
	global_store_short_d16_hi v185, v176, s[48:49]
	v_mul_u32_u24_dpp v170, v168, v180 quad_perm:[1,2,3,3] row_mask:0xf bank_mask:0xf bound_ctrl:1
	v_or_b32_e32 v171, v169, v170
	ds_write_b8 v184, v171
	s_barrier
	ds_read_b64 v[122:123], v106 offset:0
	ds_read_b64 v[124:125], v106 offset:8
	ds_read_b64 v[126:127], v106 offset:16
	s_waitcnt lgkmcnt(3)
	s_barrier
	ds_read_b64 v[128:129], v106 offset:96
	ds_read_b64 v[130:131], v106 offset:104
	ds_read_b64 v[132:133], v106 offset:112
	s_waitcnt lgkmcnt(3)
	v_mfma_scale_f32_16x16x128_f8f6f4 v[134:137], v[122:127], v[2:7], 0, v178, v115 op_sel_hi:[0,0,0] cbsz:2 blgp:2
	v_mfma_scale_f32_16x16x128_f8f6f4 v[138:141], v[122:127], v[14:19], 0, v178, v115 op_sel_hi:[0,0,0] cbsz:2 blgp:2
	v_mfma_scale_f32_16x16x128_f8f6f4 v[142:145], v[122:127], v[26:31], v[188:191], v178, v115 op_sel_hi:[0,0,0] cbsz:2 blgp:2
	v_mfma_scale_f32_16x16x128_f8f6f4 v[134:137], v[122:127], v[38:43], v[134:137], v179, v115 op_sel_hi:[0,0,0] cbsz:2 blgp:2
	v_mfma_scale_f32_16x16x128_f8f6f4 v[138:141], v[122:127], v[50:55], v[138:141], v179, v115 op_sel_hi:[0,0,0] cbsz:2 blgp:2
	v_mfma_scale_f32_16x16x128_f8f6f4 v[142:145], v[122:127], v[62:67], v[142:145], v179, v115 op_sel_hi:[0,0,0] cbsz:2 blgp:2
	s_waitcnt lgkmcnt(0)
	v_mfma_scale_f32_16x16x128_f8f6f4 v[134:137], v[128:133], v[8:13], v[134:137], v178, v115 op_sel_hi:[0,0,0] cbsz:2 blgp:2
	v_mfma_scale_f32_16x16x128_f8f6f4 v[134:137], v[128:133], v[44:49], v[134:137], v179, v115 op_sel_hi:[0,0,0] cbsz:2 blgp:2
	v_mfma_scale_f32_16x16x128_f8f6f4 v[138:141], v[128:133], v[20:25], v[138:141], v178, v115 op_sel_hi:[0,0,0] cbsz:2 blgp:2
	v_mfma_scale_f32_16x16x128_f8f6f4 v[138:141], v[128:133], v[56:61], v[138:141], v179, v115 op_sel_hi:[0,0,0] cbsz:2 blgp:2
	v_mfma_scale_f32_16x16x128_f8f6f4 v[142:145], v[128:133], v[32:37], v[142:145], v178, v115 op_sel_hi:[0,0,0] cbsz:2 blgp:2
	v_mfma_scale_f32_16x16x128_f8f6f4 v[142:145], v[128:133], v[68:73], v[142:145], v179, v115 op_sel_hi:[0,0,0] cbsz:2 blgp:2
	v_fma_mix_f32 v158, v134, v1, v147 op_sel_hi:[0,0,1]
	v_exp_f32_e32 v158, v158
	v_fma_mix_f32 v159, v138, v99, v151 op_sel_hi:[0,0,1]
	v_exp_f32_e32 v159, v159
	v_fma_f32 v158, v158, v186, v186
	v_rcp_f32_e32 v158, v158
	v_add_f32_e32 v159, 1.0, v159
	v_rcp_f32_e32 v159, v159
	s_nop 0
	v_fma_mix_f32 v161, v158, v142, v155 op_sel_hi:[0,0,1]
	v_exp_f32_e32 v161, v161
	s_add_u32 s48, s48, s40
	v_add_f32_e32 v161, 1.0, v161
	v_rcp_f32_e32 v161, v161
	s_addc_u32 s49, s49, s41
	v_fma_f32 v162, v161, -2.0, 1.0
	v_sub_f32_e32 v163, v176, v162
	v_fma_f32 v176, v159, v163, v162
	v_fma_f32 v164, |v176|, s16, v117
	v_fma_f32 v165, |v176|, s17, v118
	v_fma_f32 v166, |v176|, s18, v119
	v_lshrrev_b32_e32 v167, 26, v176
	v_min3_u32 v164, v164, v165, v166
	v_bfi_b32 v168, 31, v164, v167
	v_lshrrev_b32_e32 v169, v181, v168
	global_store_short_d16_hi v185, v176, s[48:49]
	v_mul_u32_u24_dpp v170, v168, v180 quad_perm:[1,2,3,3] row_mask:0xf bank_mask:0xf bound_ctrl:1
	v_or_b32_e32 v171, v169, v170
	ds_write_b8 v184, v171 offset:416
	s_barrier
	ds_read_b64 v[122:123], v106 offset:416
	ds_read_b64 v[124:125], v106 offset:424
	ds_read_b64 v[126:127], v106 offset:432
	s_waitcnt lgkmcnt(3)
	s_barrier
	ds_read_b64 v[128:129], v106 offset:512
	ds_read_b64 v[130:131], v106 offset:520
	ds_read_b64 v[132:133], v106 offset:528
	s_waitcnt lgkmcnt(3)
	v_mfma_scale_f32_16x16x128_f8f6f4 v[134:137], v[122:127], v[2:7], 0, v178, v115 op_sel_hi:[0,0,0] cbsz:2 blgp:2
	v_mfma_scale_f32_16x16x128_f8f6f4 v[138:141], v[122:127], v[14:19], 0, v178, v115 op_sel_hi:[0,0,0] cbsz:2 blgp:2
	v_mfma_scale_f32_16x16x128_f8f6f4 v[142:145], v[122:127], v[26:31], v[188:191], v178, v115 op_sel_hi:[0,0,0] cbsz:2 blgp:2
	v_mfma_scale_f32_16x16x128_f8f6f4 v[134:137], v[122:127], v[38:43], v[134:137], v179, v115 op_sel_hi:[0,0,0] cbsz:2 blgp:2
	v_mfma_scale_f32_16x16x128_f8f6f4 v[138:141], v[122:127], v[50:55], v[138:141], v179, v115 op_sel_hi:[0,0,0] cbsz:2 blgp:2
	v_mfma_scale_f32_16x16x128_f8f6f4 v[142:145], v[122:127], v[62:67], v[142:145], v179, v115 op_sel_hi:[0,0,0] cbsz:2 blgp:2
	s_waitcnt lgkmcnt(0)
	v_mfma_scale_f32_16x16x128_f8f6f4 v[134:137], v[128:133], v[8:13], v[134:137], v178, v115 op_sel_hi:[0,0,0] cbsz:2 blgp:2
	v_mfma_scale_f32_16x16x128_f8f6f4 v[134:137], v[128:133], v[44:49], v[134:137], v179, v115 op_sel_hi:[0,0,0] cbsz:2 blgp:2
	v_mfma_scale_f32_16x16x128_f8f6f4 v[138:141], v[128:133], v[20:25], v[138:141], v178, v115 op_sel_hi:[0,0,0] cbsz:2 blgp:2
	v_mfma_scale_f32_16x16x128_f8f6f4 v[138:141], v[128:133], v[56:61], v[138:141], v179, v115 op_sel_hi:[0,0,0] cbsz:2 blgp:2
	v_mfma_scale_f32_16x16x128_f8f6f4 v[142:145], v[128:133], v[32:37], v[142:145], v178, v115 op_sel_hi:[0,0,0] cbsz:2 blgp:2
	v_mfma_scale_f32_16x16x128_f8f6f4 v[142:145], v[128:133], v[68:73], v[142:145], v179, v115 op_sel_hi:[0,0,0] cbsz:2 blgp:2
	v_fma_mix_f32 v158, v134, v1, v147 op_sel:[0,0,1] op_sel_hi:[0,0,1]
	v_exp_f32_e32 v158, v158
	v_fma_mix_f32 v159, v138, v99, v151 op_sel:[0,0,1] op_sel_hi:[0,0,1]
	v_exp_f32_e32 v159, v159
	v_fma_f32 v158, v158, v186, v186
	v_rcp_f32_e32 v158, v158
	v_add_f32_e32 v159, 1.0, v159
	v_rcp_f32_e32 v159, v159
	s_nop 0
	v_fma_mix_f32 v161, v158, v142, v155 op_sel:[0,0,1] op_sel_hi:[0,0,1]
	v_exp_f32_e32 v161, v161
	s_add_u32 s48, s48, s40
	v_add_f32_e32 v161, 1.0, v161
	v_rcp_f32_e32 v161, v161
	s_addc_u32 s49, s49, s41
	v_fma_f32 v162, v161, -2.0, 1.0
	v_sub_f32_e32 v163, v176, v162
	v_fma_f32 v176, v159, v163, v162
	v_fma_f32 v164, |v176|, s16, v117
	v_fma_f32 v165, |v176|, s17, v118
	v_fma_f32 v166, |v176|, s18, v119
	v_lshrrev_b32_e32 v167, 26, v176
	v_min3_u32 v164, v164, v165, v166
	v_bfi_b32 v168, 31, v164, v167
	v_lshrrev_b32_e32 v169, v181, v168
	global_store_short_d16_hi v185, v176, s[48:49]
	v_mul_u32_u24_dpp v170, v168, v180 quad_perm:[1,2,3,3] row_mask:0xf bank_mask:0xf bound_ctrl:1
	v_or_b32_e32 v171, v169, v170
	ds_write_b8 v184, v171
	s_barrier
	ds_read_b64 v[122:123], v106 offset:0
	ds_read_b64 v[124:125], v106 offset:8
	ds_read_b64 v[126:127], v106 offset:16
	s_waitcnt lgkmcnt(3)
	s_barrier
	ds_read_b64 v[128:129], v106 offset:96
	ds_read_b64 v[130:131], v106 offset:104
	ds_read_b64 v[132:133], v106 offset:112
	s_waitcnt lgkmcnt(3)
	v_mfma_scale_f32_16x16x128_f8f6f4 v[134:137], v[122:127], v[2:7], 0, v178, v115 op_sel_hi:[0,0,0] cbsz:2 blgp:2
	v_mfma_scale_f32_16x16x128_f8f6f4 v[138:141], v[122:127], v[14:19], 0, v178, v115 op_sel_hi:[0,0,0] cbsz:2 blgp:2
	v_mfma_scale_f32_16x16x128_f8f6f4 v[142:145], v[122:127], v[26:31], v[188:191], v178, v115 op_sel_hi:[0,0,0] cbsz:2 blgp:2
	v_mfma_scale_f32_16x16x128_f8f6f4 v[134:137], v[122:127], v[38:43], v[134:137], v179, v115 op_sel_hi:[0,0,0] cbsz:2 blgp:2
	v_mfma_scale_f32_16x16x128_f8f6f4 v[138:141], v[122:127], v[50:55], v[138:141], v179, v115 op_sel_hi:[0,0,0] cbsz:2 blgp:2
	v_mfma_scale_f32_16x16x128_f8f6f4 v[142:145], v[122:127], v[62:67], v[142:145], v179, v115 op_sel_hi:[0,0,0] cbsz:2 blgp:2
	s_waitcnt lgkmcnt(0)
	v_mfma_scale_f32_16x16x128_f8f6f4 v[134:137], v[128:133], v[8:13], v[134:137], v178, v115 op_sel_hi:[0,0,0] cbsz:2 blgp:2
	v_mfma_scale_f32_16x16x128_f8f6f4 v[134:137], v[128:133], v[44:49], v[134:137], v179, v115 op_sel_hi:[0,0,0] cbsz:2 blgp:2
	v_mfma_scale_f32_16x16x128_f8f6f4 v[138:141], v[128:133], v[20:25], v[138:141], v178, v115 op_sel_hi:[0,0,0] cbsz:2 blgp:2
	v_mfma_scale_f32_16x16x128_f8f6f4 v[138:141], v[128:133], v[56:61], v[138:141], v179, v115 op_sel_hi:[0,0,0] cbsz:2 blgp:2
	v_mfma_scale_f32_16x16x128_f8f6f4 v[142:145], v[128:133], v[32:37], v[142:145], v178, v115 op_sel_hi:[0,0,0] cbsz:2 blgp:2
	v_mfma_scale_f32_16x16x128_f8f6f4 v[142:145], v[128:133], v[68:73], v[142:145], v179, v115 op_sel_hi:[0,0,0] cbsz:2 blgp:2
	v_fma_mix_f32 v158, v134, v1, v148 op_sel_hi:[0,0,1]
	v_exp_f32_e32 v158, v158
	v_fma_mix_f32 v159, v138, v99, v152 op_sel_hi:[0,0,1]
	v_exp_f32_e32 v159, v159
	v_fma_f32 v158, v158, v186, v186
	v_rcp_f32_e32 v158, v158
	v_add_f32_e32 v159, 1.0, v159
	v_rcp_f32_e32 v159, v159
	s_nop 0
	v_fma_mix_f32 v161, v158, v142, v156 op_sel_hi:[0,0,1]
	v_exp_f32_e32 v161, v161
	s_add_u32 s48, s48, s40
	v_add_f32_e32 v161, 1.0, v161
	v_rcp_f32_e32 v161, v161
	s_addc_u32 s49, s49, s41
	v_fma_f32 v162, v161, -2.0, 1.0
	v_sub_f32_e32 v163, v176, v162
	v_fma_f32 v176, v159, v163, v162
	v_fma_f32 v164, |v176|, s16, v117
	v_fma_f32 v165, |v176|, s17, v118
	v_fma_f32 v166, |v176|, s18, v119
	v_lshrrev_b32_e32 v167, 26, v176
	v_min3_u32 v164, v164, v165, v166
	v_bfi_b32 v168, 31, v164, v167
	v_lshrrev_b32_e32 v169, v181, v168
	global_store_short_d16_hi v185, v176, s[48:49]
	v_mul_u32_u24_dpp v170, v168, v180 quad_perm:[1,2,3,3] row_mask:0xf bank_mask:0xf bound_ctrl:1
	v_or_b32_e32 v171, v169, v170
	ds_write_b8 v184, v171 offset:416
	s_barrier
	ds_read_b64 v[122:123], v106 offset:416
	ds_read_b64 v[124:125], v106 offset:424
	ds_read_b64 v[126:127], v106 offset:432
	s_waitcnt lgkmcnt(3)
	s_barrier
	ds_read_b64 v[128:129], v106 offset:512
	ds_read_b64 v[130:131], v106 offset:520
	ds_read_b64 v[132:133], v106 offset:528
	s_waitcnt lgkmcnt(3)
	v_mfma_scale_f32_16x16x128_f8f6f4 v[134:137], v[122:127], v[2:7], 0, v178, v115 op_sel_hi:[0,0,0] cbsz:2 blgp:2
	v_mfma_scale_f32_16x16x128_f8f6f4 v[138:141], v[122:127], v[14:19], 0, v178, v115 op_sel_hi:[0,0,0] cbsz:2 blgp:2
	v_mfma_scale_f32_16x16x128_f8f6f4 v[142:145], v[122:127], v[26:31], v[188:191], v178, v115 op_sel_hi:[0,0,0] cbsz:2 blgp:2
	v_mfma_scale_f32_16x16x128_f8f6f4 v[134:137], v[122:127], v[38:43], v[134:137], v179, v115 op_sel_hi:[0,0,0] cbsz:2 blgp:2
	v_mfma_scale_f32_16x16x128_f8f6f4 v[138:141], v[122:127], v[50:55], v[138:141], v179, v115 op_sel_hi:[0,0,0] cbsz:2 blgp:2
	v_mfma_scale_f32_16x16x128_f8f6f4 v[142:145], v[122:127], v[62:67], v[142:145], v179, v115 op_sel_hi:[0,0,0] cbsz:2 blgp:2
	s_waitcnt lgkmcnt(0)
	v_mfma_scale_f32_16x16x128_f8f6f4 v[134:137], v[128:133], v[8:13], v[134:137], v178, v115 op_sel_hi:[0,0,0] cbsz:2 blgp:2
	v_mfma_scale_f32_16x16x128_f8f6f4 v[134:137], v[128:133], v[44:49], v[134:137], v179, v115 op_sel_hi:[0,0,0] cbsz:2 blgp:2
	v_mfma_scale_f32_16x16x128_f8f6f4 v[138:141], v[128:133], v[20:25], v[138:141], v178, v115 op_sel_hi:[0,0,0] cbsz:2 blgp:2
	v_mfma_scale_f32_16x16x128_f8f6f4 v[138:141], v[128:133], v[56:61], v[138:141], v179, v115 op_sel_hi:[0,0,0] cbsz:2 blgp:2
	v_mfma_scale_f32_16x16x128_f8f6f4 v[142:145], v[128:133], v[32:37], v[142:145], v178, v115 op_sel_hi:[0,0,0] cbsz:2 blgp:2
	v_mfma_scale_f32_16x16x128_f8f6f4 v[142:145], v[128:133], v[68:73], v[142:145], v179, v115 op_sel_hi:[0,0,0] cbsz:2 blgp:2
	v_fma_mix_f32 v158, v134, v1, v148 op_sel:[0,0,1] op_sel_hi:[0,0,1]
	v_exp_f32_e32 v158, v158
	v_fma_mix_f32 v159, v138, v99, v152 op_sel:[0,0,1] op_sel_hi:[0,0,1]
	v_exp_f32_e32 v159, v159
	v_fma_f32 v158, v158, v186, v186
	v_rcp_f32_e32 v158, v158
	v_add_f32_e32 v159, 1.0, v159
	v_rcp_f32_e32 v159, v159
	s_nop 0
	v_fma_mix_f32 v161, v158, v142, v156 op_sel:[0,0,1] op_sel_hi:[0,0,1]
	v_exp_f32_e32 v161, v161
	s_add_u32 s48, s48, s40
	v_add_f32_e32 v161, 1.0, v161
	v_rcp_f32_e32 v161, v161
	s_addc_u32 s49, s49, s41
	v_fma_f32 v162, v161, -2.0, 1.0
	v_sub_f32_e32 v163, v176, v162
	v_fma_f32 v176, v159, v163, v162
	v_fma_f32 v164, |v176|, s16, v117
	v_fma_f32 v165, |v176|, s17, v118
	v_fma_f32 v166, |v176|, s18, v119
	v_lshrrev_b32_e32 v167, 26, v176
	v_min3_u32 v164, v164, v165, v166
	v_bfi_b32 v168, 31, v164, v167
	v_lshrrev_b32_e32 v169, v181, v168
	global_store_short_d16_hi v185, v176, s[48:49]
	v_mul_u32_u24_dpp v170, v168, v180 quad_perm:[1,2,3,3] row_mask:0xf bank_mask:0xf bound_ctrl:1
	v_or_b32_e32 v171, v169, v170
	ds_write_b8 v184, v171
	s_barrier
	ds_read_b64 v[122:123], v106 offset:0
	ds_read_b64 v[124:125], v106 offset:8
	ds_read_b64 v[126:127], v106 offset:16
	s_waitcnt lgkmcnt(3)
	s_barrier
	ds_read_b64 v[128:129], v106 offset:96
	ds_read_b64 v[130:131], v106 offset:104
	ds_read_b64 v[132:133], v106 offset:112
	s_waitcnt lgkmcnt(3)
	v_mfma_scale_f32_16x16x128_f8f6f4 v[134:137], v[122:127], v[2:7], 0, v178, v115 op_sel_hi:[0,0,0] cbsz:2 blgp:2
	v_mfma_scale_f32_16x16x128_f8f6f4 v[138:141], v[122:127], v[14:19], 0, v178, v115 op_sel_hi:[0,0,0] cbsz:2 blgp:2
	v_mfma_scale_f32_16x16x128_f8f6f4 v[142:145], v[122:127], v[26:31], v[188:191], v178, v115 op_sel_hi:[0,0,0] cbsz:2 blgp:2
	v_mfma_scale_f32_16x16x128_f8f6f4 v[134:137], v[122:127], v[38:43], v[134:137], v179, v115 op_sel_hi:[0,0,0] cbsz:2 blgp:2
	v_mfma_scale_f32_16x16x128_f8f6f4 v[138:141], v[122:127], v[50:55], v[138:141], v179, v115 op_sel_hi:[0,0,0] cbsz:2 blgp:2
	v_mfma_scale_f32_16x16x128_f8f6f4 v[142:145], v[122:127], v[62:67], v[142:145], v179, v115 op_sel_hi:[0,0,0] cbsz:2 blgp:2
	s_waitcnt lgkmcnt(0)
	v_mfma_scale_f32_16x16x128_f8f6f4 v[134:137], v[128:133], v[8:13], v[134:137], v178, v115 op_sel_hi:[0,0,0] cbsz:2 blgp:2
	v_mfma_scale_f32_16x16x128_f8f6f4 v[134:137], v[128:133], v[44:49], v[134:137], v179, v115 op_sel_hi:[0,0,0] cbsz:2 blgp:2
	v_mfma_scale_f32_16x16x128_f8f6f4 v[138:141], v[128:133], v[20:25], v[138:141], v178, v115 op_sel_hi:[0,0,0] cbsz:2 blgp:2
	v_mfma_scale_f32_16x16x128_f8f6f4 v[138:141], v[128:133], v[56:61], v[138:141], v179, v115 op_sel_hi:[0,0,0] cbsz:2 blgp:2
	v_mfma_scale_f32_16x16x128_f8f6f4 v[142:145], v[128:133], v[32:37], v[142:145], v178, v115 op_sel_hi:[0,0,0] cbsz:2 blgp:2
	v_mfma_scale_f32_16x16x128_f8f6f4 v[142:145], v[128:133], v[68:73], v[142:145], v179, v115 op_sel_hi:[0,0,0] cbsz:2 blgp:2
	v_fma_mix_f32 v158, v134, v1, v149 op_sel_hi:[0,0,1]
	v_exp_f32_e32 v158, v158
	v_fma_mix_f32 v159, v138, v99, v153 op_sel_hi:[0,0,1]
	v_exp_f32_e32 v159, v159
	v_fma_f32 v158, v158, v186, v186
	v_rcp_f32_e32 v158, v158
	v_add_f32_e32 v159, 1.0, v159
	v_rcp_f32_e32 v159, v159
	s_nop 0
	v_fma_mix_f32 v161, v158, v142, v157 op_sel_hi:[0,0,1]
	v_exp_f32_e32 v161, v161
	s_add_u32 s48, s48, s40
	v_add_f32_e32 v161, 1.0, v161
	v_rcp_f32_e32 v161, v161
	s_addc_u32 s49, s49, s41
	v_fma_f32 v162, v161, -2.0, 1.0
	v_sub_f32_e32 v163, v176, v162
	v_fma_f32 v176, v159, v163, v162
	v_fma_f32 v164, |v176|, s16, v117
	v_fma_f32 v165, |v176|, s17, v118
	v_fma_f32 v166, |v176|, s18, v119
	v_lshrrev_b32_e32 v167, 26, v176
	v_min3_u32 v164, v164, v165, v166
	v_bfi_b32 v168, 31, v164, v167
	v_lshrrev_b32_e32 v169, v181, v168
	global_store_short_d16_hi v185, v176, s[48:49]
	v_mul_u32_u24_dpp v170, v168, v180 quad_perm:[1,2,3,3] row_mask:0xf bank_mask:0xf bound_ctrl:1
	v_or_b32_e32 v171, v169, v170
	ds_write_b8 v184, v171 offset:416
	s_barrier
	ds_read_b64 v[122:123], v106 offset:416
	ds_read_b64 v[124:125], v106 offset:424
	ds_read_b64 v[126:127], v106 offset:432
	s_waitcnt lgkmcnt(3)
	s_barrier
	ds_read_b64 v[128:129], v106 offset:512
	ds_read_b64 v[130:131], v106 offset:520
	ds_read_b64 v[132:133], v106 offset:528
	s_add_i32 s44, s44, 16
	s_waitcnt lgkmcnt(3)
	v_mfma_scale_f32_16x16x128_f8f6f4 v[134:137], v[122:127], v[2:7], 0, v178, v115 op_sel_hi:[0,0,0] cbsz:2 blgp:2
	v_mfma_scale_f32_16x16x128_f8f6f4 v[138:141], v[122:127], v[14:19], 0, v178, v115 op_sel_hi:[0,0,0] cbsz:2 blgp:2
	v_mfma_scale_f32_16x16x128_f8f6f4 v[142:145], v[122:127], v[26:31], v[188:191], v178, v115 op_sel_hi:[0,0,0] cbsz:2 blgp:2
	v_mfma_scale_f32_16x16x128_f8f6f4 v[134:137], v[122:127], v[38:43], v[134:137], v179, v115 op_sel_hi:[0,0,0] cbsz:2 blgp:2
	v_mfma_scale_f32_16x16x128_f8f6f4 v[138:141], v[122:127], v[50:55], v[138:141], v179, v115 op_sel_hi:[0,0,0] cbsz:2 blgp:2
	v_mfma_scale_f32_16x16x128_f8f6f4 v[142:145], v[122:127], v[62:67], v[142:145], v179, v115 op_sel_hi:[0,0,0] cbsz:2 blgp:2
	s_waitcnt lgkmcnt(0)
	v_mfma_scale_f32_16x16x128_f8f6f4 v[134:137], v[128:133], v[8:13], v[134:137], v178, v115 op_sel_hi:[0,0,0] cbsz:2 blgp:2
	v_mfma_scale_f32_16x16x128_f8f6f4 v[134:137], v[128:133], v[44:49], v[134:137], v179, v115 op_sel_hi:[0,0,0] cbsz:2 blgp:2
	v_mfma_scale_f32_16x16x128_f8f6f4 v[138:141], v[128:133], v[20:25], v[138:141], v178, v115 op_sel_hi:[0,0,0] cbsz:2 blgp:2
	v_mfma_scale_f32_16x16x128_f8f6f4 v[138:141], v[128:133], v[56:61], v[138:141], v179, v115 op_sel_hi:[0,0,0] cbsz:2 blgp:2
	v_mfma_scale_f32_16x16x128_f8f6f4 v[142:145], v[128:133], v[32:37], v[142:145], v178, v115 op_sel_hi:[0,0,0] cbsz:2 blgp:2
	v_mfma_scale_f32_16x16x128_f8f6f4 v[142:145], v[128:133], v[68:73], v[142:145], v179, v115 op_sel_hi:[0,0,0] cbsz:2 blgp:2
	v_fma_mix_f32 v158, v134, v1, v149 op_sel:[0,0,1] op_sel_hi:[0,0,1]
	v_exp_f32_e32 v158, v158
	v_fma_mix_f32 v159, v138, v99, v153 op_sel:[0,0,1] op_sel_hi:[0,0,1]
	v_exp_f32_e32 v159, v159
	v_fma_f32 v158, v158, v186, v186
	v_rcp_f32_e32 v158, v158
	v_add_f32_e32 v159, 1.0, v159
	v_rcp_f32_e32 v159, v159
	s_nop 0
	v_fma_mix_f32 v161, v158, v142, v157 op_sel:[0,0,1] op_sel_hi:[0,0,1]
	v_exp_f32_e32 v161, v161
	s_add_u32 s48, s48, s40
	v_add_f32_e32 v161, 1.0, v161
	v_rcp_f32_e32 v161, v161
	s_addc_u32 s49, s49, s41
	v_fma_f32 v162, v161, -2.0, 1.0
	v_sub_f32_e32 v163, v176, v162
	v_fma_f32 v176, v159, v163, v162
	v_fma_f32 v164, |v176|, s16, v117
	v_fma_f32 v165, |v176|, s17, v118
	v_fma_f32 v166, |v176|, s18, v119
	v_lshrrev_b32_e32 v167, 26, v176
	v_min3_u32 v164, v164, v165, v166
	v_bfi_b32 v168, 31, v164, v167
	v_lshrrev_b32_e32 v169, v181, v168
	global_store_short_d16_hi v185, v176, s[48:49]
	v_mul_u32_u24_dpp v170, v168, v180 quad_perm:[1,2,3,3] row_mask:0xf bank_mask:0xf bound_ctrl:1
	v_or_b32_e32 v171, v169, v170
	ds_write_b8 v184, v171
	s_barrier
	ds_read_b64 v[122:123], v106 offset:0
	ds_read_b64 v[124:125], v106 offset:8
	ds_read_b64 v[126:127], v106 offset:16
	s_cmp_lt_i32 s44, s45
	s_waitcnt lgkmcnt(3)
	s_barrier
	s_cbranch_scc1 .Lscan_loop_b_st

.LBB2_12:
	s_or_b64 exec, exec, s[0:1]
	v_and_b32_e32 v97, 1, v74
	v_mov_b32_e32 v74, s8
	v_mov_b32_e32 v75, s9
	v_lshl_or_b32 v76, s2, 9, v0
	v_mov_b32_e32 v77, v87
	v_lshl_add_u64 v[74:75], v[76:77], 2, v[74:75]
	s_waitcnt lgkmcnt(0)
	s_barrier
	global_load_dword v118, v[74:75], off
	v_and_b32_e32 v74, 4, v90
	v_mov_b32_e32 v75, 0xd0
	v_cmp_ne_u32_e32 vcc, 0, v74
	v_and_b32_e32 v110, 3, v0
	v_cmp_gt_u32_e64 s[0:1], 12, v90
	v_cndmask_b32_e32 v74, 0, v75, vcc
	v_cmp_eq_u32_e32 vcc, 0, v110
	s_and_b64 s[4:5], vcc, s[0:1]
	s_lshl_b32 s1, s2, 21
	v_add_u32_e32 v109, v74, v86
	s_mul_i32 s0, s2, 0x600000
	v_lshl_or_b32 v74, v89, 1, v88
	s_and_b32 s2, s1, 0x1e00000
	v_mul_u32_u24_e32 v74, 0x60, v74
	v_lshlrev_b32_e32 v75, 1, v90
	s_add_u32 s0, s14, s0
	s_addc_u32 s1, s15, 0
	v_or3_b32 v86, v74, v75, v97
	v_lshl_add_u64 v[98:99], v[86:87], 4, s[0:1]
	s_mov_b64 s[0:1], 0x5a0000
	v_lshl_add_u64 v[100:101], v[98:99], 0, s[0:1]
	s_mov_b32 s0, 0x5a0000
	v_add_co_u32_e32 v102, vcc, s0, v98
	s_waitcnt vmcnt(4)
	v_mul_f32_e32 v86, 0xbfb8aa3b, v95
	v_addc_co_u32_e32 v103, vcc, 0, v99, vcc
	global_load_dwordx4 v[82:85], v[102:103], off
	global_load_dwordx4 v[74:77], v[100:101], off offset:512
	global_load_dwordx4 v[78:81], v[100:101], off offset:1024
	v_mul_f32_e32 v100, 0x3c91a2b4, v86
	s_waitcnt vmcnt(6)
	v_mul_f32_e32 v86, 0xbfb8aa3b, v94
	v_mul_f32_e32 v101, 0x3c91a2b4, v86
	s_waitcnt vmcnt(5)
	v_mul_f32_e32 v86, 0x4038aa3b, v93
	v_and_b32_e32 v0, 12, v0
	v_mul_f32_e32 v102, 0x3c91a2b4, v86
	v_lshrrev_b32_e32 v86, 2, v90
	v_mul_u32_u24_e32 v90, 0xd0, v97
	v_mad_u32_u24 v0, v89, 24, v0
	v_mul_u32_u24_e32 v88, 12, v88
	v_add3_u32 v93, v0, v90, v88
	v_or_b32_e32 v0, s2, v1
	v_lshlrev_b32_e32 v104, 3, v86
	v_lshlrev_b32_e32 v89, 20, v97
	v_lshl_add_u32 v0, s22, 8, v0
	v_sub_u32_e32 v86, 0, v104
	v_or3_b32 v0, v0, v89, v92
	v_and_b32_e32 v111, 24, v86
	v_lshlrev_b32_e32 v86, 1, v0
	s_mov_b64 s[6:7], 0x5a6000
	v_lshl_add_u64 v[0:1], s[12:13], 0, v[86:87]
	v_lshl_add_u64 v[86:87], v[98:99], 0, s[6:7]
	s_mov_b64 s[6:7], 0x5a6200
	v_lshl_add_u64 v[88:89], v[98:99], 0, s[6:7]
	s_mov_b64 s[6:7], 0x5a6400
	v_cmp_lt_u32_e64 s[0:1], 1, v91
	s_waitcnt vmcnt(4)
	v_mul_f32_e32 v103, 0x4038aa3b, v96
	s_mov_b32 s3, 0
	v_or_b32_e32 v105, 0x1c400, v109
	v_add_u32_e32 v106, 0x1c410, v109
	v_add_u32_e32 v107, 0x1c470, v109
	v_add_u32_e32 v108, 0x1c5b0, v109
	v_add_u32_e32 v109, 0x1c610, v109
	v_mul_u32_u24_e32 v110, 6, v110
	v_lshl_add_u64 v[90:91], v[98:99], 0, s[6:7]
	s_movk_i32 s22, 0x780
	s_movk_i32 s14, 0x7f
	s_movk_i32 s15, 0xf0
	v_mov_b32_e32 v112, 0x7f7f7f7f
	s_mov_b32 s17, 0x42700000
	s_mov_b32 s18, 0x41f00000
	s_mov_b32 s19, 0x41700000
	s_mov_b64 s[6:7], 0x12000
	s_mov_b64 s[8:9], 0x12200
	s_mov_b64 s[10:11], 0x12400
	v_mov_b32_e32 v113, 0x4b400000
	v_mov_b32_e32 v114, 0x4b400008
	v_mov_b32_e32 v115, 0x4b400010
	v_add_u32_e32 v116, 0x1c5a0, v93
	v_add_u32_e32 v117, 0x1c400, v93
	v_mbcnt_lo_u32_b32 v200, -1, 0
	v_mbcnt_hi_u32_b32 v200, -1, v200
	v_and_b32_e32 v201, 3, v200
	v_and_b32_e32 v202, 15, v200
	v_cmp_gt_u32_e32 vcc, 8, v202
	s_nop 1
	v_cndmask_b32_e64 v178, 0, v112, vcc
	v_cndmask_b32_e64 v179, v112, 0, vcc
	v_lshlrev_b32_e32 v181, 1, v201
	v_sub_u32_e32 v202, 6, v181
	v_lshlrev_b32_e64 v180, v202, 1
	v_lshrrev_b32_e32 v202, 3, v104
	v_sub_u32_e32 v184, v117, v202
	v_add_u32_e32 v184, v184, v201
	v_add_u32_e32 v202, 0x1c4c0, v202
	v_cmp_eq_u32_e32 vcc, 3, v201
	s_nop 1
	v_cndmask_b32_e32 v184, v184, v202, vcc
	v_subrev_u32_e32 v185, s12, v0
	s_movk_i32 s44, 0x780
	s_movk_i32 s45, 0x800
	s_lshr_b32 s46, s44, 3
	s_add_i32 s46, s46, 1
	s_mul_i32 s46, s46, 0x6000
	s_mov_b32 s47, 0
	v_lshl_add_u64 v[196:197], v[98:99], 0, s[46:47]
	s_mov_b32 s42, 0x6000
	s_mov_b32 s43, 0
	s_sub_i32 s46, s44, 1
	s_sub_i32 s47, 0x800, s44
	s_and_b64 s[40:41], s[20:21], exec
	s_cselect_b32 s46, s46, s47
	s_cselect_b32 s41, 0, -1
	s_xor_b32 s40, s41, 0x400
	s_sub_i32 s40, s40, s41
	s_ashr_i32 s47, s46, 31
	s_lshl_b64 s[46:47], s[46:47], 10
	s_add_u32 s48, s12, s46
	s_addc_u32 s49, s13, s47
	v_readfirstlane_b32 s51, v117
	s_waitcnt vmcnt(0) lgkmcnt(0)
	v_mov_b32_e32 v176, v118
	v_rcp_f32_e32 v186, v102
	s_nop 1
	v_mul_f32_e32 v188, v103, v186
	v_mov_b32_e32 v189, 0
	v_mov_b32_e32 v190, 0
	v_mov_b32_e32 v191, 0
	s_nop 1
	s_sub_u32 s51, s51, 0x1c400
	s_cmp_lt_i32 s44, s45
	s_cbranch_scc0 .Lscan_exit_f2
	ds_read_b64 v[122:123], v105 offset:0
	ds_read_b64 v[124:125], v105 offset:8
	ds_read_b64 v[126:127], v105 offset:16
	s_waitcnt lgkmcnt(0)
	s_cmp_lt_u32 s51, 96
	s_cbranch_scc0 .Lscan_loop_b_f2
.Lscan_loop_a_f2:
	ds_read_b64 v[128:129], v105 offset:96
	ds_read_b64 v[130:131], v105 offset:104
	ds_read_b64 v[132:133], v105 offset:112
	s_waitcnt vmcnt(8)
	global_load_dwordx4 v[146:149], v[196:197], off
	global_load_dwordx4 v[150:153], v[196:197], off offset:512
	global_load_dwordx4 v[154:157], v[196:197], off offset:1024
	v_lshl_add_u64 v[196:197], v[196:197], 0, s[42:43]
	s_waitcnt lgkmcnt(3)
	v_mfma_scale_f32_16x16x128_f8f6f4 v[134:137], v[122:127], v[2:7], 0, v178, v112 op_sel_hi:[0,0,0] cbsz:2 blgp:2
	v_mfma_scale_f32_16x16x128_f8f6f4 v[138:141], v[122:127], v[14:19], 0, v178, v112 op_sel_hi:[0,0,0] cbsz:2 blgp:2
	v_mfma_scale_f32_16x16x128_f8f6f4 v[142:145], v[122:127], v[26:31], v[188:191], v178, v112 op_sel_hi:[0,0,0] cbsz:2 blgp:2
	v_mfma_scale_f32_16x16x128_f8f6f4 v[134:137], v[122:127], v[38:43], v[134:137], v179, v112 op_sel_hi:[0,0,0] cbsz:2 blgp:2
	v_mfma_scale_f32_16x16x128_f8f6f4 v[138:141], v[122:127], v[50:55], v[138:141], v179, v112 op_sel_hi:[0,0,0] cbsz:2 blgp:2
	v_mfma_scale_f32_16x16x128_f8f6f4 v[142:145], v[122:127], v[62:67], v[142:145], v179, v112 op_sel_hi:[0,0,0] cbsz:2 blgp:2
	s_waitcnt lgkmcnt(0)
	v_mfma_scale_f32_16x16x128_f8f6f4 v[134:137], v[128:133], v[8:13], v[134:137], v178, v112 op_sel_hi:[0,0,0] cbsz:2 blgp:2
	v_mfma_scale_f32_16x16x128_f8f6f4 v[134:137], v[128:133], v[44:49], v[134:137], v179, v112 op_sel_hi:[0,0,0] cbsz:2 blgp:2
	v_mfma_scale_f32_16x16x128_f8f6f4 v[138:141], v[128:133], v[20:25], v[138:141], v178, v112 op_sel_hi:[0,0,0] cbsz:2 blgp:2
	v_mfma_scale_f32_16x16x128_f8f6f4 v[138:141], v[128:133], v[56:61], v[138:141], v179, v112 op_sel_hi:[0,0,0] cbsz:2 blgp:2
	v_mfma_scale_f32_16x16x128_f8f6f4 v[142:145], v[128:133], v[32:37], v[142:145], v178, v112 op_sel_hi:[0,0,0] cbsz:2 blgp:2
	v_mfma_scale_f32_16x16x128_f8f6f4 v[142:145], v[128:133], v[68:73], v[142:145], v179, v112 op_sel_hi:[0,0,0] cbsz:2 blgp:2
	v_fma_mix_f32 v158, v134, v100, v82 op_sel_hi:[0,0,1]
	v_exp_f32_e32 v158, v158
	v_fma_mix_f32 v159, v138, v101, v74 op_sel_hi:[0,0,1]
	v_exp_f32_e32 v159, v159
	v_fma_f32 v158, v158, v186, v186
	v_rcp_f32_e32 v158, v158
	v_add_f32_e32 v159, 1.0, v159
	v_rcp_f32_e32 v159, v159
	s_nop 0
	v_fma_mix_f32 v161, v158, v142, v78 op_sel_hi:[0,0,1]
	v_exp_f32_e32 v161, v161
	s_add_u32 s48, s48, s40
	v_add_f32_e32 v161, 1.0, v161
	v_rcp_f32_e32 v161, v161
	s_addc_u32 s49, s49, s41
	v_fma_f32 v162, v161, -2.0, 1.0
	v_sub_f32_e32 v163, v176, v162
	v_fma_f32 v176, v159, v163, v162
	v_fma_f32 v164, |v176|, s17, v113
	v_fma_f32 v165, |v176|, s18, v114
	v_fma_f32 v166, |v176|, s19, v115
	v_lshrrev_b32_e32 v167, 26, v176
	v_min3_u32 v164, v164, v165, v166
	v_bfi_b32 v168, 31, v164, v167
	v_lshrrev_b32_e32 v169, v181, v168
	global_store_short_d16_hi v185, v176, s[48:49]
	v_mul_u32_u24_dpp v170, v168, v180 quad_perm:[1,2,3,3] row_mask:0xf bank_mask:0xf bound_ctrl:1
	v_or_b32_e32 v171, v169, v170
	ds_write_b8 v184, v171 offset:416
	s_waitcnt lgkmcnt(0)
	s_barrier
	ds_read_b64 v[122:123], v105 offset:416
	ds_read_b64 v[124:125], v105 offset:424
	ds_read_b64 v[126:127], v105 offset:432
	s_barrier
	ds_read_b64 v[128:129], v105 offset:512
	ds_read_b64 v[130:131], v105 offset:520
	ds_read_b64 v[132:133], v105 offset:528
	s_waitcnt lgkmcnt(3)
	v_mfma_scale_f32_16x16x128_f8f6f4 v[134:137], v[122:127], v[2:7], 0, v178, v112 op_sel_hi:[0,0,0] cbsz:2 blgp:2
	v_mfma_scale_f32_16x16x128_f8f6f4 v[138:141], v[122:127], v[14:19], 0, v178, v112 op_sel_hi:[0,0,0] cbsz:2 blgp:2
	v_mfma_scale_f32_16x16x128_f8f6f4 v[142:145], v[122:127], v[26:31], v[188:191], v178, v112 op_sel_hi:[0,0,0] cbsz:2 blgp:2
	v_mfma_scale_f32_16x16x128_f8f6f4 v[134:137], v[122:127], v[38:43], v[134:137], v179, v112 op_sel_hi:[0,0,0] cbsz:2 blgp:2
	v_mfma_scale_f32_16x16x128_f8f6f4 v[138:141], v[122:127], v[50:55], v[138:141], v179, v112 op_sel_hi:[0,0,0] cbsz:2 blgp:2
	v_mfma_scale_f32_16x16x128_f8f6f4 v[142:145], v[122:127], v[62:67], v[142:145], v179, v112 op_sel_hi:[0,0,0] cbsz:2 blgp:2
	s_waitcnt lgkmcnt(0)
	v_mfma_scale_f32_16x16x128_f8f6f4 v[134:137], v[128:133], v[8:13], v[134:137], v178, v112 op_sel_hi:[0,0,0] cbsz:2 blgp:2
	v_mfma_scale_f32_16x16x128_f8f6f4 v[134:137], v[128:133], v[44:49], v[134:137], v179, v112 op_sel_hi:[0,0,0] cbsz:2 blgp:2
	v_mfma_scale_f32_16x16x128_f8f6f4 v[138:141], v[128:133], v[20:25], v[138:141], v178, v112 op_sel_hi:[0,0,0] cbsz:2 blgp:2
	v_mfma_scale_f32_16x16x128_f8f6f4 v[138:141], v[128:133], v[56:61], v[138:141], v179, v112 op_sel_hi:[0,0,0] cbsz:2 blgp:2
	v_mfma_scale_f32_16x16x128_f8f6f4 v[142:145], v[128:133], v[32:37], v[142:145], v178, v112 op_sel_hi:[0,0,0] cbsz:2 blgp:2
	v_mfma_scale_f32_16x16x128_f8f6f4 v[142:145], v[128:133], v[68:73], v[142:145], v179, v112 op_sel_hi:[0,0,0] cbsz:2 blgp:2
	v_fma_mix_f32 v158, v134, v100, v82 op_sel:[0,0,1] op_sel_hi:[0,0,1]
	v_exp_f32_e32 v158, v158
	v_fma_mix_f32 v159, v138, v101, v74 op_sel:[0,0,1] op_sel_hi:[0,0,1]
	v_exp_f32_e32 v159, v159
	v_fma_f32 v158, v158, v186, v186
	v_rcp_f32_e32 v158, v158
	v_add_f32_e32 v159, 1.0, v159
	v_rcp_f32_e32 v159, v159
	s_nop 0
	v_fma_mix_f32 v161, v158, v142, v78 op_sel:[0,0,1] op_sel_hi:[0,0,1]
	v_exp_f32_e32 v161, v161
	s_add_u32 s48, s48, s40
	v_add_f32_e32 v161, 1.0, v161
	v_rcp_f32_e32 v161, v161
	s_addc_u32 s49, s49, s41
	v_fma_f32 v162, v161, -2.0, 1.0
	v_sub_f32_e32 v163, v176, v162
	v_fma_f32 v176, v159, v163, v162
	v_fma_f32 v164, |v176|, s17, v113
	v_fma_f32 v165, |v176|, s18, v114
	v_fma_f32 v166, |v176|, s19, v115
	v_lshrrev_b32_e32 v167, 26, v176
	v_min3_u32 v164, v164, v165, v166
	v_bfi_b32 v168, 31, v164, v167
	v_lshrrev_b32_e32 v169, v181, v168
	global_store_short_d16_hi v185, v176, s[48:49]
	v_mul_u32_u24_dpp v170, v168, v180 quad_perm:[1,2,3,3] row_mask:0xf bank_mask:0xf bound_ctrl:1
	v_or_b32_e32 v171, v169, v170
	ds_write_b8 v184, v171
	s_waitcnt lgkmcnt(0)
	s_barrier
	ds_read_b64 v[122:123], v105 offset:0
	ds_read_b64 v[124:125], v105 offset:8
	ds_read_b64 v[126:127], v105 offset:16
	s_barrier
	ds_read_b64 v[128:129], v105 offset:96
	ds_read_b64 v[130:131], v105 offset:104
	ds_read_b64 v[132:133], v105 offset:112
	s_waitcnt lgkmcnt(3)
	v_mfma_scale_f32_16x16x128_f8f6f4 v[134:137], v[122:127], v[2:7], 0, v178, v112 op_sel_hi:[0,0,0] cbsz:2 blgp:2
	v_mfma_scale_f32_16x16x128_f8f6f4 v[138:141], v[122:127], v[14:19], 0, v178, v112 op_sel_hi:[0,0,0] cbsz:2 blgp:2
	v_mfma_scale_f32_16x16x128_f8f6f4 v[142:145], v[122:127], v[26:31], v[188:191], v178, v112 op_sel_hi:[0,0,0] cbsz:2 blgp:2
	v_mfma_scale_f32_16x16x128_f8f6f4 v[134:137], v[122:127], v[38:43], v[134:137], v179, v112 op_sel_hi:[0,0,0] cbsz:2 blgp:2
	v_mfma_scale_f32_16x16x128_f8f6f4 v[138:141], v[122:127], v[50:55], v[138:141], v179, v112 op_sel_hi:[0,0,0] cbsz:2 blgp:2
	v_mfma_scale_f32_16x16x128_f8f6f4 v[142:145], v[122:127], v[62:67], v[142:145], v179, v112 op_sel_hi:[0,0,0] cbsz:2 blgp:2
	s_waitcnt lgkmcnt(0)
	v_mfma_scale_f32_16x16x128_f8f6f4 v[134:137], v[128:133], v[8:13], v[134:137], v178, v112 op_sel_hi:[0,0,0] cbsz:2 blgp:2
	v_mfma_scale_f32_16x16x128_f8f6f4 v[134:137], v[128:133], v[44:49], v[134:137], v179, v112 op_sel_hi:[0,0,0] cbsz:2 blgp:2
	v_mfma_scale_f32_16x16x128_f8f6f4 v[138:141], v[128:133], v[20:25], v[138:141], v178, v112 op_sel_hi:[0,0,0] cbsz:2 blgp:2
	v_mfma_scale_f32_16x16x128_f8f6f4 v[138:141], v[128:133], v[56:61], v[138:141], v179, v112 op_sel_hi:[0,0,0] cbsz:2 blgp:2
	v_mfma_scale_f32_16x16x128_f8f6f4 v[142:145], v[128:133], v[32:37], v[142:145], v178, v112 op_sel_hi:[0,0,0] cbsz:2 blgp:2
	v_mfma_scale_f32_16x16x128_f8f6f4 v[142:145], v[128:133], v[68:73], v[142:145], v179, v112 op_sel_hi:[0,0,0] cbsz:2 blgp:2
	v_fma_mix_f32 v158, v134, v100, v83 op_sel_hi:[0,0,1]
	v_exp_f32_e32 v158, v158
	v_fma_mix_f32 v159, v138, v101, v75 op_sel_hi:[0,0,1]
	v_exp_f32_e32 v159, v159
	v_fma_f32 v158, v158, v186, v186
	v_rcp_f32_e32 v158, v158
	v_add_f32_e32 v159, 1.0, v159
	v_rcp_f32_e32 v159, v159
	s_nop 0
	v_fma_mix_f32 v161, v158, v142, v79 op_sel_hi:[0,0,1]
	v_exp_f32_e32 v161, v161
	s_add_u32 s48, s48, s40
	v_add_f32_e32 v161, 1.0, v161
	v_rcp_f32_e32 v161, v161
	s_addc_u32 s49, s49, s41
	v_fma_f32 v162, v161, -2.0, 1.0
	v_sub_f32_e32 v163, v176, v162
	v_fma_f32 v176, v159, v163, v162
	v_fma_f32 v164, |v176|, s17, v113
	v_fma_f32 v165, |v176|, s18, v114
	v_fma_f32 v166, |v176|, s19, v115
	v_lshrrev_b32_e32 v167, 26, v176
	v_min3_u32 v164, v164, v165, v166
	v_bfi_b32 v168, 31, v164, v167
	v_lshrrev_b32_e32 v169, v181, v168
	global_store_short_d16_hi v185, v176, s[48:49]
	v_mul_u32_u24_dpp v170, v168, v180 quad_perm:[1,2,3,3] row_mask:0xf bank_mask:0xf bound_ctrl:1
	v_or_b32_e32 v171, v169, v170
	ds_write_b8 v184, v171 offset:416
	s_waitcnt lgkmcnt(0)
	s_barrier
	ds_read_b64 v[122:123], v105 offset:416
	ds_read_b64 v[124:125], v105 offset:424
	ds_read_b64 v[126:127], v105 offset:432
	s_barrier
	ds_read_b64 v[128:129], v105 offset:512
	ds_read_b64 v[130:131], v105 offset:520
	ds_read_b64 v[132:133], v105 offset:528
	s_waitcnt lgkmcnt(3)
	v_mfma_scale_f32_16x16x128_f8f6f4 v[134:137], v[122:127], v[2:7], 0, v178, v112 op_sel_hi:[0,0,0] cbsz:2 blgp:2
	v_mfma_scale_f32_16x16x128_f8f6f4 v[138:141], v[122:127], v[14:19], 0, v178, v112 op_sel_hi:[0,0,0] cbsz:2 blgp:2
	v_mfma_scale_f32_16x16x128_f8f6f4 v[142:145], v[122:127], v[26:31], v[188:191], v178, v112 op_sel_hi:[0,0,0] cbsz:2 blgp:2
	v_mfma_scale_f32_16x16x128_f8f6f4 v[134:137], v[122:127], v[38:43], v[134:137], v179, v112 op_sel_hi:[0,0,0] cbsz:2 blgp:2
	v_mfma_scale_f32_16x16x128_f8f6f4 v[138:141], v[122:127], v[50:55], v[138:141], v179, v112 op_sel_hi:[0,0,0] cbsz:2 blgp:2
	v_mfma_scale_f32_16x16x128_f8f6f4 v[142:145], v[122:127], v[62:67], v[142:145], v179, v112 op_sel_hi:[0,0,0] cbsz:2 blgp:2
	s_waitcnt lgkmcnt(0)
	v_mfma_scale_f32_16x16x128_f8f6f4 v[134:137], v[128:133], v[8:13], v[134:137], v178, v112 op_sel_hi:[0,0,0] cbsz:2 blgp:2
	v_mfma_scale_f32_16x16x128_f8f6f4 v[134:137], v[128:133], v[44:49], v[134:137], v179, v112 op_sel_hi:[0,0,0] cbsz:2 blgp:2
	v_mfma_scale_f32_16x16x128_f8f6f4 v[138:141], v[128:133], v[20:25], v[138:141], v178, v112 op_sel_hi:[0,0,0] cbsz:2 blgp:2
	v_mfma_scale_f32_16x16x128_f8f6f4 v[138:141], v[128:133], v[56:61], v[138:141], v179, v112 op_sel_hi:[0,0,0] cbsz:2 blgp:2
	v_mfma_scale_f32_16x16x128_f8f6f4 v[142:145], v[128:133], v[32:37], v[142:145], v178, v112 op_sel_hi:[0,0,0] cbsz:2 blgp:2
	v_mfma_scale_f32_16x16x128_f8f6f4 v[142:145], v[128:133], v[68:73], v[142:145], v179, v112 op_sel_hi:[0,0,0] cbsz:2 blgp:2
	v_fma_mix_f32 v158, v134, v100, v83 op_sel:[0,0,1] op_sel_hi:[0,0,1]
	v_exp_f32_e32 v158, v158
	v_fma_mix_f32 v159, v138, v101, v75 op_sel:[0,0,1] op_sel_hi:[0,0,1]
	v_exp_f32_e32 v159, v159
	v_fma_f32 v158, v158, v186, v186
	v_rcp_f32_e32 v158, v158
	v_add_f32_e32 v159, 1.0, v159
	v_rcp_f32_e32 v159, v159
	s_nop 0
	v_fma_mix_f32 v161, v158, v142, v79 op_sel:[0,0,1] op_sel_hi:[0,0,1]
	v_exp_f32_e32 v161, v161
	s_add_u32 s48, s48, s40
	v_add_f32_e32 v161, 1.0, v161
	v_rcp_f32_e32 v161, v161
	s_addc_u32 s49, s49, s41
	v_fma_f32 v162, v161, -2.0, 1.0
	v_sub_f32_e32 v163, v176, v162
	v_fma_f32 v176, v159, v163, v162
	v_fma_f32 v164, |v176|, s17, v113
	v_fma_f32 v165, |v176|, s18, v114
	v_fma_f32 v166, |v176|, s19, v115
	v_lshrrev_b32_e32 v167, 26, v176
	v_min3_u32 v164, v164, v165, v166
	v_bfi_b32 v168, 31, v164, v167
	v_lshrrev_b32_e32 v169, v181, v168
	global_store_short_d16_hi v185, v176, s[48:49]
	v_mul_u32_u24_dpp v170, v168, v180 quad_perm:[1,2,3,3] row_mask:0xf bank_mask:0xf bound_ctrl:1
	v_or_b32_e32 v171, v169, v170
	ds_write_b8 v184, v171
	s_waitcnt lgkmcnt(0)
	s_barrier
	ds_read_b64 v[122:123], v105 offset:0
	ds_read_b64 v[124:125], v105 offset:8
	ds_read_b64 v[126:127], v105 offset:16
	s_barrier
	ds_read_b64 v[128:129], v105 offset:96
	ds_read_b64 v[130:131], v105 offset:104
	ds_read_b64 v[132:133], v105 offset:112
	s_waitcnt lgkmcnt(3)
	v_mfma_scale_f32_16x16x128_f8f6f4 v[134:137], v[122:127], v[2:7], 0, v178, v112 op_sel_hi:[0,0,0] cbsz:2 blgp:2
	v_mfma_scale_f32_16x16x128_f8f6f4 v[138:141], v[122:127], v[14:19], 0, v178, v112 op_sel_hi:[0,0,0] cbsz:2 blgp:2
	v_mfma_scale_f32_16x16x128_f8f6f4 v[142:145], v[122:127], v[26:31], v[188:191], v178, v112 op_sel_hi:[0,0,0] cbsz:2 blgp:2
	v_mfma_scale_f32_16x16x128_f8f6f4 v[134:137], v[122:127], v[38:43], v[134:137], v179, v112 op_sel_hi:[0,0,0] cbsz:2 blgp:2
	v_mfma_scale_f32_16x16x128_f8f6f4 v[138:141], v[122:127], v[50:55], v[138:141], v179, v112 op_sel_hi:[0,0,0] cbsz:2 blgp:2
	v_mfma_scale_f32_16x16x128_f8f6f4 v[142:145], v[122:127], v[62:67], v[142:145], v179, v112 op_sel_hi:[0,0,0] cbsz:2 blgp:2
	s_waitcnt lgkmcnt(0)
	v_mfma_scale_f32_16x16x128_f8f6f4 v[134:137], v[128:133], v[8:13], v[134:137], v178, v112 op_sel_hi:[0,0,0] cbsz:2 blgp:2
	v_mfma_scale_f32_16x16x128_f8f6f4 v[134:137], v[128:133], v[44:49], v[134:137], v179, v112 op_sel_hi:[0,0,0] cbsz:2 blgp:2
	v_mfma_scale_f32_16x16x128_f8f6f4 v[138:141], v[128:133], v[20:25], v[138:141], v178, v112 op_sel_hi:[0,0,0] cbsz:2 blgp:2
	v_mfma_scale_f32_16x16x128_f8f6f4 v[138:141], v[128:133], v[56:61], v[138:141], v179, v112 op_sel_hi:[0,0,0] cbsz:2 blgp:2
	v_mfma_scale_f32_16x16x128_f8f6f4 v[142:145], v[128:133], v[32:37], v[142:145], v178, v112 op_sel_hi:[0,0,0] cbsz:2 blgp:2
	v_mfma_scale_f32_16x16x128_f8f6f4 v[142:145], v[128:133], v[68:73], v[142:145], v179, v112 op_sel_hi:[0,0,0] cbsz:2 blgp:2
	v_fma_mix_f32 v158, v134, v100, v84 op_sel_hi:[0,0,1]
	v_exp_f32_e32 v158, v158
	v_fma_mix_f32 v159, v138, v101, v76 op_sel_hi:[0,0,1]
	v_exp_f32_e32 v159, v159
	v_fma_f32 v158, v158, v186, v186
	v_rcp_f32_e32 v158, v158
	v_add_f32_e32 v159, 1.0, v159
	v_rcp_f32_e32 v159, v159
	s_nop 0
	v_fma_mix_f32 v161, v158, v142, v80 op_sel_hi:[0,0,1]
	v_exp_f32_e32 v161, v161
	s_add_u32 s48, s48, s40
	v_add_f32_e32 v161, 1.0, v161
	v_rcp_f32_e32 v161, v161
	s_addc_u32 s49, s49, s41
	v_fma_f32 v162, v161, -2.0, 1.0
	v_sub_f32_e32 v163, v176, v162
	v_fma_f32 v176, v159, v163, v162
	v_fma_f32 v164, |v176|, s17, v113
	v_fma_f32 v165, |v176|, s18, v114
	v_fma_f32 v166, |v176|, s19, v115
	v_lshrrev_b32_e32 v167, 26, v176
	v_min3_u32 v164, v164, v165, v166
	v_bfi_b32 v168, 31, v164, v167
	v_lshrrev_b32_e32 v169, v181, v168
	global_store_short_d16_hi v185, v176, s[48:49]
	v_mul_u32_u24_dpp v170, v168, v180 quad_perm:[1,2,3,3] row_mask:0xf bank_mask:0xf bound_ctrl:1
	v_or_b32_e32 v171, v169, v170
	ds_write_b8 v184, v171 offset:416
	s_waitcnt lgkmcnt(0)
	s_barrier
	ds_read_b64 v[122:123], v105 offset:416
	ds_read_b64 v[124:125], v105 offset:424
	ds_read_b64 v[126:127], v105 offset:432
	s_barrier
	ds_read_b64 v[128:129], v105 offset:512
	ds_read_b64 v[130:131], v105 offset:520
	ds_read_b64 v[132:133], v105 offset:528
	s_waitcnt lgkmcnt(3)
	v_mfma_scale_f32_16x16x128_f8f6f4 v[134:137], v[122:127], v[2:7], 0, v178, v112 op_sel_hi:[0,0,0] cbsz:2 blgp:2
	v_mfma_scale_f32_16x16x128_f8f6f4 v[138:141], v[122:127], v[14:19], 0, v178, v112 op_sel_hi:[0,0,0] cbsz:2 blgp:2
	v_mfma_scale_f32_16x16x128_f8f6f4 v[142:145], v[122:127], v[26:31], v[188:191], v178, v112 op_sel_hi:[0,0,0] cbsz:2 blgp:2
	v_mfma_scale_f32_16x16x128_f8f6f4 v[134:137], v[122:127], v[38:43], v[134:137], v179, v112 op_sel_hi:[0,0,0] cbsz:2 blgp:2
	v_mfma_scale_f32_16x16x128_f8f6f4 v[138:141], v[122:127], v[50:55], v[138:141], v179, v112 op_sel_hi:[0,0,0] cbsz:2 blgp:2
	v_mfma_scale_f32_16x16x128_f8f6f4 v[142:145], v[122:127], v[62:67], v[142:145], v179, v112 op_sel_hi:[0,0,0] cbsz:2 blgp:2
	s_waitcnt lgkmcnt(0)
	v_mfma_scale_f32_16x16x128_f8f6f4 v[134:137], v[128:133], v[8:13], v[134:137], v178, v112 op_sel_hi:[0,0,0] cbsz:2 blgp:2
	v_mfma_scale_f32_16x16x128_f8f6f4 v[134:137], v[128:133], v[44:49], v[134:137], v179, v112 op_sel_hi:[0,0,0] cbsz:2 blgp:2
	v_mfma_scale_f32_16x16x128_f8f6f4 v[138:141], v[128:133], v[20:25], v[138:141], v178, v112 op_sel_hi:[0,0,0] cbsz:2 blgp:2
	v_mfma_scale_f32_16x16x128_f8f6f4 v[138:141], v[128:133], v[56:61], v[138:141], v179, v112 op_sel_hi:[0,0,0] cbsz:2 blgp:2
	v_mfma_scale_f32_16x16x128_f8f6f4 v[142:145], v[128:133], v[32:37], v[142:145], v178, v112 op_sel_hi:[0,0,0] cbsz:2 blgp:2
	v_mfma_scale_f32_16x16x128_f8f6f4 v[142:145], v[128:133], v[68:73], v[142:145], v179, v112 op_sel_hi:[0,0,0] cbsz:2 blgp:2
	v_fma_mix_f32 v158, v134, v100, v84 op_sel:[0,0,1] op_sel_hi:[0,0,1]
	v_exp_f32_e32 v158, v158
	v_fma_mix_f32 v159, v138, v101, v76 op_sel:[0,0,1] op_sel_hi:[0,0,1]
	v_exp_f32_e32 v159, v159
	v_fma_f32 v158, v158, v186, v186
	v_rcp_f32_e32 v158, v158
	v_add_f32_e32 v159, 1.0, v159
	v_rcp_f32_e32 v159, v159
	s_nop 0
	v_fma_mix_f32 v161, v158, v142, v80 op_sel:[0,0,1] op_sel_hi:[0,0,1]
	v_exp_f32_e32 v161, v161
	s_add_u32 s48, s48, s40
	v_add_f32_e32 v161, 1.0, v161
	v_rcp_f32_e32 v161, v161
	s_addc_u32 s49, s49, s41
	v_fma_f32 v162, v161, -2.0, 1.0
	v_sub_f32_e32 v163, v176, v162
	v_fma_f32 v176, v159, v163, v162
	v_fma_f32 v164, |v176|, s17, v113
	v_fma_f32 v165, |v176|, s18, v114
	v_fma_f32 v166, |v176|, s19, v115
	v_lshrrev_b32_e32 v167, 26, v176
	v_min3_u32 v164, v164, v165, v166
	v_bfi_b32 v168, 31, v164, v167
	v_lshrrev_b32_e32 v169, v181, v168
	global_store_short_d16_hi v185, v176, s[48:49]
	v_mul_u32_u24_dpp v170, v168, v180 quad_perm:[1,2,3,3] row_mask:0xf bank_mask:0xf bound_ctrl:1
	v_or_b32_e32 v171, v169, v170
	ds_write_b8 v184, v171
	s_waitcnt lgkmcnt(0)
	s_barrier
	ds_read_b64 v[122:123], v105 offset:0
	ds_read_b64 v[124:125], v105 offset:8
	ds_read_b64 v[126:127], v105 offset:16
	s_barrier
	ds_read_b64 v[128:129], v105 offset:96
	ds_read_b64 v[130:131], v105 offset:104
	ds_read_b64 v[132:133], v105 offset:112
	s_waitcnt lgkmcnt(3)
	v_mfma_scale_f32_16x16x128_f8f6f4 v[134:137], v[122:127], v[2:7], 0, v178, v112 op_sel_hi:[0,0,0] cbsz:2 blgp:2
	v_mfma_scale_f32_16x16x128_f8f6f4 v[138:141], v[122:127], v[14:19], 0, v178, v112 op_sel_hi:[0,0,0] cbsz:2 blgp:2
	v_mfma_scale_f32_16x16x128_f8f6f4 v[142:145], v[122:127], v[26:31], v[188:191], v178, v112 op_sel_hi:[0,0,0] cbsz:2 blgp:2
	v_mfma_scale_f32_16x16x128_f8f6f4 v[134:137], v[122:127], v[38:43], v[134:137], v179, v112 op_sel_hi:[0,0,0] cbsz:2 blgp:2
	v_mfma_scale_f32_16x16x128_f8f6f4 v[138:141], v[122:127], v[50:55], v[138:141], v179, v112 op_sel_hi:[0,0,0] cbsz:2 blgp:2
	v_mfma_scale_f32_16x16x128_f8f6f4 v[142:145], v[122:127], v[62:67], v[142:145], v179, v112 op_sel_hi:[0,0,0] cbsz:2 blgp:2
	s_waitcnt lgkmcnt(0)
	v_mfma_scale_f32_16x16x128_f8f6f4 v[134:137], v[128:133], v[8:13], v[134:137], v178, v112 op_sel_hi:[0,0,0] cbsz:2 blgp:2
	v_mfma_scale_f32_16x16x128_f8f6f4 v[134:137], v[128:133], v[44:49], v[134:137], v179, v112 op_sel_hi:[0,0,0] cbsz:2 blgp:2
	v_mfma_scale_f32_16x16x128_f8f6f4 v[138:141], v[128:133], v[20:25], v[138:141], v178, v112 op_sel_hi:[0,0,0] cbsz:2 blgp:2
	v_mfma_scale_f32_16x16x128_f8f6f4 v[138:141], v[128:133], v[56:61], v[138:141], v179, v112 op_sel_hi:[0,0,0] cbsz:2 blgp:2
	v_mfma_scale_f32_16x16x128_f8f6f4 v[142:145], v[128:133], v[32:37], v[142:145], v178, v112 op_sel_hi:[0,0,0] cbsz:2 blgp:2
	v_mfma_scale_f32_16x16x128_f8f6f4 v[142:145], v[128:133], v[68:73], v[142:145], v179, v112 op_sel_hi:[0,0,0] cbsz:2 blgp:2
	v_fma_mix_f32 v158, v134, v100, v85 op_sel_hi:[0,0,1]
	v_exp_f32_e32 v158, v158
	v_fma_mix_f32 v159, v138, v101, v77 op_sel_hi:[0,0,1]
	v_exp_f32_e32 v159, v159
	v_fma_f32 v158, v158, v186, v186
	v_rcp_f32_e32 v158, v158
	v_add_f32_e32 v159, 1.0, v159
	v_rcp_f32_e32 v159, v159
	s_nop 0
	v_fma_mix_f32 v161, v158, v142, v81 op_sel_hi:[0,0,1]
	v_exp_f32_e32 v161, v161
	s_add_u32 s48, s48, s40
	v_add_f32_e32 v161, 1.0, v161
	v_rcp_f32_e32 v161, v161
	s_addc_u32 s49, s49, s41
	v_fma_f32 v162, v161, -2.0, 1.0
	v_sub_f32_e32 v163, v176, v162
	v_fma_f32 v176, v159, v163, v162
	v_fma_f32 v164, |v176|, s17, v113
	v_fma_f32 v165, |v176|, s18, v114
	v_fma_f32 v166, |v176|, s19, v115
	v_lshrrev_b32_e32 v167, 26, v176
	v_min3_u32 v164, v164, v165, v166
	v_bfi_b32 v168, 31, v164, v167
	v_lshrrev_b32_e32 v169, v181, v168
	global_store_short_d16_hi v185, v176, s[48:49]
	v_mul_u32_u24_dpp v170, v168, v180 quad_perm:[1,2,3,3] row_mask:0xf bank_mask:0xf bound_ctrl:1
	v_or_b32_e32 v171, v169, v170
	ds_write_b8 v184, v171 offset:416
	s_waitcnt lgkmcnt(0)
	s_barrier
	ds_read_b64 v[122:123], v105 offset:416
	ds_read_b64 v[124:125], v105 offset:424
	ds_read_b64 v[126:127], v105 offset:432
	s_barrier
	ds_read_b64 v[128:129], v105 offset:512
	ds_read_b64 v[130:131], v105 offset:520
	ds_read_b64 v[132:133], v105 offset:528
	s_waitcnt lgkmcnt(3)
	v_mfma_scale_f32_16x16x128_f8f6f4 v[134:137], v[122:127], v[2:7], 0, v178, v112 op_sel_hi:[0,0,0] cbsz:2 blgp:2
	v_mfma_scale_f32_16x16x128_f8f6f4 v[138:141], v[122:127], v[14:19], 0, v178, v112 op_sel_hi:[0,0,0] cbsz:2 blgp:2
	v_mfma_scale_f32_16x16x128_f8f6f4 v[142:145], v[122:127], v[26:31], v[188:191], v178, v112 op_sel_hi:[0,0,0] cbsz:2 blgp:2
	v_mfma_scale_f32_16x16x128_f8f6f4 v[134:137], v[122:127], v[38:43], v[134:137], v179, v112 op_sel_hi:[0,0,0] cbsz:2 blgp:2
	v_mfma_scale_f32_16x16x128_f8f6f4 v[138:141], v[122:127], v[50:55], v[138:141], v179, v112 op_sel_hi:[0,0,0] cbsz:2 blgp:2
	v_mfma_scale_f32_16x16x128_f8f6f4 v[142:145], v[122:127], v[62:67], v[142:145], v179, v112 op_sel_hi:[0,0,0] cbsz:2 blgp:2
	s_waitcnt lgkmcnt(0)
	v_mfma_scale_f32_16x16x128_f8f6f4 v[134:137], v[128:133], v[8:13], v[134:137], v178, v112 op_sel_hi:[0,0,0] cbsz:2 blgp:2
	v_mfma_scale_f32_16x16x128_f8f6f4 v[134:137], v[128:133], v[44:49], v[134:137], v179, v112 op_sel_hi:[0,0,0] cbsz:2 blgp:2
	v_mfma_scale_f32_16x16x128_f8f6f4 v[138:141], v[128:133], v[20:25], v[138:141], v178, v112 op_sel_hi:[0,0,0] cbsz:2 blgp:2
	v_mfma_scale_f32_16x16x128_f8f6f4 v[138:141], v[128:133], v[56:61], v[138:141], v179, v112 op_sel_hi:[0,0,0] cbsz:2 blgp:2
	v_mfma_scale_f32_16x16x128_f8f6f4 v[142:145], v[128:133], v[32:37], v[142:145], v178, v112 op_sel_hi:[0,0,0] cbsz:2 blgp:2
	v_mfma_scale_f32_16x16x128_f8f6f4 v[142:145], v[128:133], v[68:73], v[142:145], v179, v112 op_sel_hi:[0,0,0] cbsz:2 blgp:2
	v_fma_mix_f32 v158, v134, v100, v85 op_sel:[0,0,1] op_sel_hi:[0,0,1]
	v_exp_f32_e32 v158, v158
	v_fma_mix_f32 v159, v138, v101, v77 op_sel:[0,0,1] op_sel_hi:[0,0,1]
	v_exp_f32_e32 v159, v159
	v_fma_f32 v158, v158, v186, v186
	v_rcp_f32_e32 v158, v158
	v_add_f32_e32 v159, 1.0, v159
	v_rcp_f32_e32 v159, v159
	s_nop 0
	v_fma_mix_f32 v161, v158, v142, v81 op_sel:[0,0,1] op_sel_hi:[0,0,1]
	v_exp_f32_e32 v161, v161
	s_add_u32 s48, s48, s40
	v_add_f32_e32 v161, 1.0, v161
	v_rcp_f32_e32 v161, v161
	s_addc_u32 s49, s49, s41
	v_fma_f32 v162, v161, -2.0, 1.0
	v_sub_f32_e32 v163, v176, v162
	v_fma_f32 v176, v159, v163, v162
	v_fma_f32 v164, |v176|, s17, v113
	v_fma_f32 v165, |v176|, s18, v114
	v_fma_f32 v166, |v176|, s19, v115
	v_lshrrev_b32_e32 v167, 26, v176
	v_min3_u32 v164, v164, v165, v166
	v_bfi_b32 v168, 31, v164, v167
	v_lshrrev_b32_e32 v169, v181, v168
	global_store_short_d16_hi v185, v176, s[48:49]
	v_mul_u32_u24_dpp v170, v168, v180 quad_perm:[1,2,3,3] row_mask:0xf bank_mask:0xf bound_ctrl:1
	v_or_b32_e32 v171, v169, v170
	ds_write_b8 v184, v171
	s_waitcnt lgkmcnt(0)
	s_barrier
	ds_read_b64 v[122:123], v105 offset:0
	ds_read_b64 v[124:125], v105 offset:8
	ds_read_b64 v[126:127], v105 offset:16
	s_barrier
	ds_read_b64 v[128:129], v105 offset:96
	ds_read_b64 v[130:131], v105 offset:104
	ds_read_b64 v[132:133], v105 offset:112
	s_waitcnt vmcnt(8)
	global_load_dwordx4 v[82:85], v[196:197], off
	global_load_dwordx4 v[74:77], v[196:197], off offset:512
	global_load_dwordx4 v[78:81], v[196:197], off offset:1024
	v_lshl_add_u64 v[196:197], v[196:197], 0, s[42:43]
	s_waitcnt lgkmcnt(3)
	v_mfma_scale_f32_16x16x128_f8f6f4 v[134:137], v[122:127], v[2:7], 0, v178, v112 op_sel_hi:[0,0,0] cbsz:2 blgp:2
	v_mfma_scale_f32_16x16x128_f8f6f4 v[138:141], v[122:127], v[14:19], 0, v178, v112 op_sel_hi:[0,0,0] cbsz:2 blgp:2
	v_mfma_scale_f32_16x16x128_f8f6f4 v[142:145], v[122:127], v[26:31], v[188:191], v178, v112 op_sel_hi:[0,0,0] cbsz:2 blgp:2
	v_mfma_scale_f32_16x16x128_f8f6f4 v[134:137], v[122:127], v[38:43], v[134:137], v179, v112 op_sel_hi:[0,0,0] cbsz:2 blgp:2
	v_mfma_scale_f32_16x16x128_f8f6f4 v[138:141], v[122:127], v[50:55], v[138:141], v179, v112 op_sel_hi:[0,0,0] cbsz:2 blgp:2
	v_mfma_scale_f32_16x16x128_f8f6f4 v[142:145], v[122:127], v[62:67], v[142:145], v179, v112 op_sel_hi:[0,0,0] cbsz:2 blgp:2
	s_waitcnt lgkmcnt(0)
	v_mfma_scale_f32_16x16x128_f8f6f4 v[134:137], v[128:133], v[8:13], v[134:137], v178, v112 op_sel_hi:[0,0,0] cbsz:2 blgp:2
	v_mfma_scale_f32_16x16x128_f8f6f4 v[134:137], v[128:133], v[44:49], v[134:137], v179, v112 op_sel_hi:[0,0,0] cbsz:2 blgp:2
	v_mfma_scale_f32_16x16x128_f8f6f4 v[138:141], v[128:133], v[20:25], v[138:141], v178, v112 op_sel_hi:[0,0,0] cbsz:2 blgp:2
	v_mfma_scale_f32_16x16x128_f8f6f4 v[138:141], v[128:133], v[56:61], v[138:141], v179, v112 op_sel_hi:[0,0,0] cbsz:2 blgp:2
	v_mfma_scale_f32_16x16x128_f8f6f4 v[142:145], v[128:133], v[32:37], v[142:145], v178, v112 op_sel_hi:[0,0,0] cbsz:2 blgp:2
	v_mfma_scale_f32_16x16x128_f8f6f4 v[142:145], v[128:133], v[68:73], v[142:145], v179, v112 op_sel_hi:[0,0,0] cbsz:2 blgp:2
	v_fma_mix_f32 v158, v134, v100, v146 op_sel_hi:[0,0,1]
	v_exp_f32_e32 v158, v158
	v_fma_mix_f32 v159, v138, v101, v150 op_sel_hi:[0,0,1]
	v_exp_f32_e32 v159, v159
	v_fma_f32 v158, v158, v186, v186
	v_rcp_f32_e32 v158, v158
	v_add_f32_e32 v159, 1.0, v159
	v_rcp_f32_e32 v159, v159
	s_nop 0
	v_fma_mix_f32 v161, v158, v142, v154 op_sel_hi:[0,0,1]
	v_exp_f32_e32 v161, v161
	s_add_u32 s48, s48, s40
	v_add_f32_e32 v161, 1.0, v161
	v_rcp_f32_e32 v161, v161
	s_addc_u32 s49, s49, s41
	v_fma_f32 v162, v161, -2.0, 1.0
	v_sub_f32_e32 v163, v176, v162
	v_fma_f32 v176, v159, v163, v162
	v_fma_f32 v164, |v176|, s17, v113
	v_fma_f32 v165, |v176|, s18, v114
	v_fma_f32 v166, |v176|, s19, v115
	v_lshrrev_b32_e32 v167, 26, v176
	v_min3_u32 v164, v164, v165, v166
	v_bfi_b32 v168, 31, v164, v167
	v_lshrrev_b32_e32 v169, v181, v168
	global_store_short_d16_hi v185, v176, s[48:49]
	v_mul_u32_u24_dpp v170, v168, v180 quad_perm:[1,2,3,3] row_mask:0xf bank_mask:0xf bound_ctrl:1
	v_or_b32_e32 v171, v169, v170
	ds_write_b8 v184, v171 offset:416
	s_waitcnt lgkmcnt(0)
	s_barrier
	ds_read_b64 v[122:123], v105 offset:416
	ds_read_b64 v[124:125], v105 offset:424
	ds_read_b64 v[126:127], v105 offset:432
	s_barrier
	ds_read_b64 v[128:129], v105 offset:512
	ds_read_b64 v[130:131], v105 offset:520
	ds_read_b64 v[132:133], v105 offset:528
	s_waitcnt lgkmcnt(3)
	v_mfma_scale_f32_16x16x128_f8f6f4 v[134:137], v[122:127], v[2:7], 0, v178, v112 op_sel_hi:[0,0,0] cbsz:2 blgp:2
	v_mfma_scale_f32_16x16x128_f8f6f4 v[138:141], v[122:127], v[14:19], 0, v178, v112 op_sel_hi:[0,0,0] cbsz:2 blgp:2
	v_mfma_scale_f32_16x16x128_f8f6f4 v[142:145], v[122:127], v[26:31], v[188:191], v178, v112 op_sel_hi:[0,0,0] cbsz:2 blgp:2
	v_mfma_scale_f32_16x16x128_f8f6f4 v[134:137], v[122:127], v[38:43], v[134:137], v179, v112 op_sel_hi:[0,0,0] cbsz:2 blgp:2
	v_mfma_scale_f32_16x16x128_f8f6f4 v[138:141], v[122:127], v[50:55], v[138:141], v179, v112 op_sel_hi:[0,0,0] cbsz:2 blgp:2
	v_mfma_scale_f32_16x16x128_f8f6f4 v[142:145], v[122:127], v[62:67], v[142:145], v179, v112 op_sel_hi:[0,0,0] cbsz:2 blgp:2
	s_waitcnt lgkmcnt(0)
	v_mfma_scale_f32_16x16x128_f8f6f4 v[134:137], v[128:133], v[8:13], v[134:137], v178, v112 op_sel_hi:[0,0,0] cbsz:2 blgp:2
	v_mfma_scale_f32_16x16x128_f8f6f4 v[134:137], v[128:133], v[44:49], v[134:137], v179, v112 op_sel_hi:[0,0,0] cbsz:2 blgp:2
	v_mfma_scale_f32_16x16x128_f8f6f4 v[138:141], v[128:133], v[20:25], v[138:141], v178, v112 op_sel_hi:[0,0,0] cbsz:2 blgp:2
	v_mfma_scale_f32_16x16x128_f8f6f4 v[138:141], v[128:133], v[56:61], v[138:141], v179, v112 op_sel_hi:[0,0,0] cbsz:2 blgp:2
	v_mfma_scale_f32_16x16x128_f8f6f4 v[142:145], v[128:133], v[32:37], v[142:145], v178, v112 op_sel_hi:[0,0,0] cbsz:2 blgp:2
	v_mfma_scale_f32_16x16x128_f8f6f4 v[142:145], v[128:133], v[68:73], v[142:145], v179, v112 op_sel_hi:[0,0,0] cbsz:2 blgp:2
	v_fma_mix_f32 v158, v134, v100, v146 op_sel:[0,0,1] op_sel_hi:[0,0,1]
	v_exp_f32_e32 v158, v158
	v_fma_mix_f32 v159, v138, v101, v150 op_sel:[0,0,1] op_sel_hi:[0,0,1]
	v_exp_f32_e32 v159, v159
	v_fma_f32 v158, v158, v186, v186
	v_rcp_f32_e32 v158, v158
	v_add_f32_e32 v159, 1.0, v159
	v_rcp_f32_e32 v159, v159
	s_nop 0
	v_fma_mix_f32 v161, v158, v142, v154 op_sel:[0,0,1] op_sel_hi:[0,0,1]
	v_exp_f32_e32 v161, v161
	s_add_u32 s48, s48, s40
	v_add_f32_e32 v161, 1.0, v161
	v_rcp_f32_e32 v161, v161
	s_addc_u32 s49, s49, s41
	v_fma_f32 v162, v161, -2.0, 1.0
	v_sub_f32_e32 v163, v176, v162
	v_fma_f32 v176, v159, v163, v162
	v_fma_f32 v164, |v176|, s17, v113
	v_fma_f32 v165, |v176|, s18, v114
	v_fma_f32 v166, |v176|, s19, v115
	v_lshrrev_b32_e32 v167, 26, v176
	v_min3_u32 v164, v164, v165, v166
	v_bfi_b32 v168, 31, v164, v167
	v_lshrrev_b32_e32 v169, v181, v168
	global_store_short_d16_hi v185, v176, s[48:49]
	v_mul_u32_u24_dpp v170, v168, v180 quad_perm:[1,2,3,3] row_mask:0xf bank_mask:0xf bound_ctrl:1
	v_or_b32_e32 v171, v169, v170
	ds_write_b8 v184, v171
	s_waitcnt lgkmcnt(0)
	s_barrier
	ds_read_b64 v[122:123], v105 offset:0
	ds_read_b64 v[124:125], v105 offset:8
	ds_read_b64 v[126:127], v105 offset:16
	s_barrier
	ds_read_b64 v[128:129], v105 offset:96
	ds_read_b64 v[130:131], v105 offset:104
	ds_read_b64 v[132:133], v105 offset:112
	s_waitcnt lgkmcnt(3)
	v_mfma_scale_f32_16x16x128_f8f6f4 v[134:137], v[122:127], v[2:7], 0, v178, v112 op_sel_hi:[0,0,0] cbsz:2 blgp:2
	v_mfma_scale_f32_16x16x128_f8f6f4 v[138:141], v[122:127], v[14:19], 0, v178, v112 op_sel_hi:[0,0,0] cbsz:2 blgp:2
	v_mfma_scale_f32_16x16x128_f8f6f4 v[142:145], v[122:127], v[26:31], v[188:191], v178, v112 op_sel_hi:[0,0,0] cbsz:2 blgp:2
	v_mfma_scale_f32_16x16x128_f8f6f4 v[134:137], v[122:127], v[38:43], v[134:137], v179, v112 op_sel_hi:[0,0,0] cbsz:2 blgp:2
	v_mfma_scale_f32_16x16x128_f8f6f4 v[138:141], v[122:127], v[50:55], v[138:141], v179, v112 op_sel_hi:[0,0,0] cbsz:2 blgp:2
	v_mfma_scale_f32_16x16x128_f8f6f4 v[142:145], v[122:127], v[62:67], v[142:145], v179, v112 op_sel_hi:[0,0,0] cbsz:2 blgp:2
	s_waitcnt lgkmcnt(0)
	v_mfma_scale_f32_16x16x128_f8f6f4 v[134:137], v[128:133], v[8:13], v[134:137], v178, v112 op_sel_hi:[0,0,0] cbsz:2 blgp:2
	v_mfma_scale_f32_16x16x128_f8f6f4 v[134:137], v[128:133], v[44:49], v[134:137], v179, v112 op_sel_hi:[0,0,0] cbsz:2 blgp:2
	v_mfma_scale_f32_16x16x128_f8f6f4 v[138:141], v[128:133], v[20:25], v[138:141], v178, v112 op_sel_hi:[0,0,0] cbsz:2 blgp:2
	v_mfma_scale_f32_16x16x128_f8f6f4 v[138:141], v[128:133], v[56:61], v[138:141], v179, v112 op_sel_hi:[0,0,0] cbsz:2 blgp:2
	v_mfma_scale_f32_16x16x128_f8f6f4 v[142:145], v[128:133], v[32:37], v[142:145], v178, v112 op_sel_hi:[0,0,0] cbsz:2 blgp:2
	v_mfma_scale_f32_16x16x128_f8f6f4 v[142:145], v[128:133], v[68:73], v[142:145], v179, v112 op_sel_hi:[0,0,0] cbsz:2 blgp:2
	v_fma_mix_f32 v158, v134, v100, v147 op_sel_hi:[0,0,1]
	v_exp_f32_e32 v158, v158
	v_fma_mix_f32 v159, v138, v101, v151 op_sel_hi:[0,0,1]
	v_exp_f32_e32 v159, v159
	v_fma_f32 v158, v158, v186, v186
	v_rcp_f32_e32 v158, v158
	v_add_f32_e32 v159, 1.0, v159
	v_rcp_f32_e32 v159, v159
	s_nop 0
	v_fma_mix_f32 v161, v158, v142, v155 op_sel_hi:[0,0,1]
	v_exp_f32_e32 v161, v161
	s_add_u32 s48, s48, s40
	v_add_f32_e32 v161, 1.0, v161
	v_rcp_f32_e32 v161, v161
	s_addc_u32 s49, s49, s41
	v_fma_f32 v162, v161, -2.0, 1.0
	v_sub_f32_e32 v163, v176, v162
	v_fma_f32 v176, v159, v163, v162
	v_fma_f32 v164, |v176|, s17, v113
	v_fma_f32 v165, |v176|, s18, v114
	v_fma_f32 v166, |v176|, s19, v115
	v_lshrrev_b32_e32 v167, 26, v176
	v_min3_u32 v164, v164, v165, v166
	v_bfi_b32 v168, 31, v164, v167
	v_lshrrev_b32_e32 v169, v181, v168
	global_store_short_d16_hi v185, v176, s[48:49]
	v_mul_u32_u24_dpp v170, v168, v180 quad_perm:[1,2,3,3] row_mask:0xf bank_mask:0xf bound_ctrl:1
	v_or_b32_e32 v171, v169, v170
	ds_write_b8 v184, v171 offset:416
	s_waitcnt lgkmcnt(0)
	s_barrier
	ds_read_b64 v[122:123], v105 offset:416
	ds_read_b64 v[124:125], v105 offset:424
	ds_read_b64 v[126:127], v105 offset:432
	s_barrier
	ds_read_b64 v[128:129], v105 offset:512
	ds_read_b64 v[130:131], v105 offset:520
	ds_read_b64 v[132:133], v105 offset:528
	s_waitcnt lgkmcnt(3)
	v_mfma_scale_f32_16x16x128_f8f6f4 v[134:137], v[122:127], v[2:7], 0, v178, v112 op_sel_hi:[0,0,0] cbsz:2 blgp:2
	v_mfma_scale_f32_16x16x128_f8f6f4 v[138:141], v[122:127], v[14:19], 0, v178, v112 op_sel_hi:[0,0,0] cbsz:2 blgp:2
	v_mfma_scale_f32_16x16x128_f8f6f4 v[142:145], v[122:127], v[26:31], v[188:191], v178, v112 op_sel_hi:[0,0,0] cbsz:2 blgp:2
	v_mfma_scale_f32_16x16x128_f8f6f4 v[134:137], v[122:127], v[38:43], v[134:137], v179, v112 op_sel_hi:[0,0,0] cbsz:2 blgp:2
	v_mfma_scale_f32_16x16x128_f8f6f4 v[138:141], v[122:127], v[50:55], v[138:141], v179, v112 op_sel_hi:[0,0,0] cbsz:2 blgp:2
	v_mfma_scale_f32_16x16x128_f8f6f4 v[142:145], v[122:127], v[62:67], v[142:145], v179, v112 op_sel_hi:[0,0,0] cbsz:2 blgp:2
	s_waitcnt lgkmcnt(0)
	v_mfma_scale_f32_16x16x128_f8f6f4 v[134:137], v[128:133], v[8:13], v[134:137], v178, v112 op_sel_hi:[0,0,0] cbsz:2 blgp:2
	v_mfma_scale_f32_16x16x128_f8f6f4 v[134:137], v[128:133], v[44:49], v[134:137], v179, v112 op_sel_hi:[0,0,0] cbsz:2 blgp:2
	v_mfma_scale_f32_16x16x128_f8f6f4 v[138:141], v[128:133], v[20:25], v[138:141], v178, v112 op_sel_hi:[0,0,0] cbsz:2 blgp:2
	v_mfma_scale_f32_16x16x128_f8f6f4 v[138:141], v[128:133], v[56:61], v[138:141], v179, v112 op_sel_hi:[0,0,0] cbsz:2 blgp:2
	v_mfma_scale_f32_16x16x128_f8f6f4 v[142:145], v[128:133], v[32:37], v[142:145], v178, v112 op_sel_hi:[0,0,0] cbsz:2 blgp:2
	v_mfma_scale_f32_16x16x128_f8f6f4 v[142:145], v[128:133], v[68:73], v[142:145], v179, v112 op_sel_hi:[0,0,0] cbsz:2 blgp:2
	v_fma_mix_f32 v158, v134, v100, v147 op_sel:[0,0,1] op_sel_hi:[0,0,1]
	v_exp_f32_e32 v158, v158
	v_fma_mix_f32 v159, v138, v101, v151 op_sel:[0,0,1] op_sel_hi:[0,0,1]
	v_exp_f32_e32 v159, v159
	v_fma_f32 v158, v158, v186, v186
	v_rcp_f32_e32 v158, v158
	v_add_f32_e32 v159, 1.0, v159
	v_rcp_f32_e32 v159, v159
	s_nop 0
	v_fma_mix_f32 v161, v158, v142, v155 op_sel:[0,0,1] op_sel_hi:[0,0,1]
	v_exp_f32_e32 v161, v161
	s_add_u32 s48, s48, s40
	v_add_f32_e32 v161, 1.0, v161
	v_rcp_f32_e32 v161, v161
	s_addc_u32 s49, s49, s41
	v_fma_f32 v162, v161, -2.0, 1.0
	v_sub_f32_e32 v163, v176, v162
	v_fma_f32 v176, v159, v163, v162
	v_fma_f32 v164, |v176|, s17, v113
	v_fma_f32 v165, |v176|, s18, v114
	v_fma_f32 v166, |v176|, s19, v115
	v_lshrrev_b32_e32 v167, 26, v176
	v_min3_u32 v164, v164, v165, v166
	v_bfi_b32 v168, 31, v164, v167
	v_lshrrev_b32_e32 v169, v181, v168
	global_store_short_d16_hi v185, v176, s[48:49]
	v_mul_u32_u24_dpp v170, v168, v180 quad_perm:[1,2,3,3] row_mask:0xf bank_mask:0xf bound_ctrl:1
	v_or_b32_e32 v171, v169, v170
	ds_write_b8 v184, v171
	s_waitcnt lgkmcnt(0)
	s_barrier
	ds_read_b64 v[122:123], v105 offset:0
	ds_read_b64 v[124:125], v105 offset:8
	ds_read_b64 v[126:127], v105 offset:16
	s_barrier
	ds_read_b64 v[128:129], v105 offset:96
	ds_read_b64 v[130:131], v105 offset:104
	ds_read_b64 v[132:133], v105 offset:112
	s_waitcnt lgkmcnt(3)
	v_mfma_scale_f32_16x16x128_f8f6f4 v[134:137], v[122:127], v[2:7], 0, v178, v112 op_sel_hi:[0,0,0] cbsz:2 blgp:2
	v_mfma_scale_f32_16x16x128_f8f6f4 v[138:141], v[122:127], v[14:19], 0, v178, v112 op_sel_hi:[0,0,0] cbsz:2 blgp:2
	v_mfma_scale_f32_16x16x128_f8f6f4 v[142:145], v[122:127], v[26:31], v[188:191], v178, v112 op_sel_hi:[0,0,0] cbsz:2 blgp:2
	v_mfma_scale_f32_16x16x128_f8f6f4 v[134:137], v[122:127], v[38:43], v[134:137], v179, v112 op_sel_hi:[0,0,0] cbsz:2 blgp:2
	v_mfma_scale_f32_16x16x128_f8f6f4 v[138:141], v[122:127], v[50:55], v[138:141], v179, v112 op_sel_hi:[0,0,0] cbsz:2 blgp:2
	v_mfma_scale_f32_16x16x128_f8f6f4 v[142:145], v[122:127], v[62:67], v[142:145], v179, v112 op_sel_hi:[0,0,0] cbsz:2 blgp:2
	s_waitcnt lgkmcnt(0)
	v_mfma_scale_f32_16x16x128_f8f6f4 v[134:137], v[128:133], v[8:13], v[134:137], v178, v112 op_sel_hi:[0,0,0] cbsz:2 blgp:2
	v_mfma_scale_f32_16x16x128_f8f6f4 v[134:137], v[128:133], v[44:49], v[134:137], v179, v112 op_sel_hi:[0,0,0] cbsz:2 blgp:2
	v_mfma_scale_f32_16x16x128_f8f6f4 v[138:141], v[128:133], v[20:25], v[138:141], v178, v112 op_sel_hi:[0,0,0] cbsz:2 blgp:2
	v_mfma_scale_f32_16x16x128_f8f6f4 v[138:141], v[128:133], v[56:61], v[138:141], v179, v112 op_sel_hi:[0,0,0] cbsz:2 blgp:2
	v_mfma_scale_f32_16x16x128_f8f6f4 v[142:145], v[128:133], v[32:37], v[142:145], v178, v112 op_sel_hi:[0,0,0] cbsz:2 blgp:2
	v_mfma_scale_f32_16x16x128_f8f6f4 v[142:145], v[128:133], v[68:73], v[142:145], v179, v112 op_sel_hi:[0,0,0] cbsz:2 blgp:2
	v_fma_mix_f32 v158, v134, v100, v148 op_sel_hi:[0,0,1]
	v_exp_f32_e32 v158, v158
	v_fma_mix_f32 v159, v138, v101, v152 op_sel_hi:[0,0,1]
	v_exp_f32_e32 v159, v159
	v_fma_f32 v158, v158, v186, v186
	v_rcp_f32_e32 v158, v158
	v_add_f32_e32 v159, 1.0, v159
	v_rcp_f32_e32 v159, v159
	s_nop 0
	v_fma_mix_f32 v161, v158, v142, v156 op_sel_hi:[0,0,1]
	v_exp_f32_e32 v161, v161
	s_add_u32 s48, s48, s40
	v_add_f32_e32 v161, 1.0, v161
	v_rcp_f32_e32 v161, v161
	s_addc_u32 s49, s49, s41
	v_fma_f32 v162, v161, -2.0, 1.0
	v_sub_f32_e32 v163, v176, v162
	v_fma_f32 v176, v159, v163, v162
	v_fma_f32 v164, |v176|, s17, v113
	v_fma_f32 v165, |v176|, s18, v114
	v_fma_f32 v166, |v176|, s19, v115
	v_lshrrev_b32_e32 v167, 26, v176
	v_min3_u32 v164, v164, v165, v166
	v_bfi_b32 v168, 31, v164, v167
	v_lshrrev_b32_e32 v169, v181, v168
	global_store_short_d16_hi v185, v176, s[48:49]
	v_mul_u32_u24_dpp v170, v168, v180 quad_perm:[1,2,3,3] row_mask:0xf bank_mask:0xf bound_ctrl:1
	v_or_b32_e32 v171, v169, v170
	ds_write_b8 v184, v171 offset:416
	s_waitcnt lgkmcnt(0)
	s_barrier
	ds_read_b64 v[122:123], v105 offset:416
	ds_read_b64 v[124:125], v105 offset:424
	ds_read_b64 v[126:127], v105 offset:432
	s_barrier
	ds_read_b64 v[128:129], v105 offset:512
	ds_read_b64 v[130:131], v105 offset:520
	ds_read_b64 v[132:133], v105 offset:528
	s_waitcnt lgkmcnt(3)
	v_mfma_scale_f32_16x16x128_f8f6f4 v[134:137], v[122:127], v[2:7], 0, v178, v112 op_sel_hi:[0,0,0] cbsz:2 blgp:2
	v_mfma_scale_f32_16x16x128_f8f6f4 v[138:141], v[122:127], v[14:19], 0, v178, v112 op_sel_hi:[0,0,0] cbsz:2 blgp:2
	v_mfma_scale_f32_16x16x128_f8f6f4 v[142:145], v[122:127], v[26:31], v[188:191], v178, v112 op_sel_hi:[0,0,0] cbsz:2 blgp:2
	v_mfma_scale_f32_16x16x128_f8f6f4 v[134:137], v[122:127], v[38:43], v[134:137], v179, v112 op_sel_hi:[0,0,0] cbsz:2 blgp:2
	v_mfma_scale_f32_16x16x128_f8f6f4 v[138:141], v[122:127], v[50:55], v[138:141], v179, v112 op_sel_hi:[0,0,0] cbsz:2 blgp:2
	v_mfma_scale_f32_16x16x128_f8f6f4 v[142:145], v[122:127], v[62:67], v[142:145], v179, v112 op_sel_hi:[0,0,0] cbsz:2 blgp:2
	s_waitcnt lgkmcnt(0)
	v_mfma_scale_f32_16x16x128_f8f6f4 v[134:137], v[128:133], v[8:13], v[134:137], v178, v112 op_sel_hi:[0,0,0] cbsz:2 blgp:2
	v_mfma_scale_f32_16x16x128_f8f6f4 v[134:137], v[128:133], v[44:49], v[134:137], v179, v112 op_sel_hi:[0,0,0] cbsz:2 blgp:2
	v_mfma_scale_f32_16x16x128_f8f6f4 v[138:141], v[128:133], v[20:25], v[138:141], v178, v112 op_sel_hi:[0,0,0] cbsz:2 blgp:2
	v_mfma_scale_f32_16x16x128_f8f6f4 v[138:141], v[128:133], v[56:61], v[138:141], v179, v112 op_sel_hi:[0,0,0] cbsz:2 blgp:2
	v_mfma_scale_f32_16x16x128_f8f6f4 v[142:145], v[128:133], v[32:37], v[142:145], v178, v112 op_sel_hi:[0,0,0] cbsz:2 blgp:2
	v_mfma_scale_f32_16x16x128_f8f6f4 v[142:145], v[128:133], v[68:73], v[142:145], v179, v112 op_sel_hi:[0,0,0] cbsz:2 blgp:2
	v_fma_mix_f32 v158, v134, v100, v148 op_sel:[0,0,1] op_sel_hi:[0,0,1]
	v_exp_f32_e32 v158, v158
	v_fma_mix_f32 v159, v138, v101, v152 op_sel:[0,0,1] op_sel_hi:[0,0,1]
	v_exp_f32_e32 v159, v159
	v_fma_f32 v158, v158, v186, v186
	v_rcp_f32_e32 v158, v158
	v_add_f32_e32 v159, 1.0, v159
	v_rcp_f32_e32 v159, v159
	s_nop 0
	v_fma_mix_f32 v161, v158, v142, v156 op_sel:[0,0,1] op_sel_hi:[0,0,1]
	v_exp_f32_e32 v161, v161
	s_add_u32 s48, s48, s40
	v_add_f32_e32 v161, 1.0, v161
	v_rcp_f32_e32 v161, v161
	s_addc_u32 s49, s49, s41
	v_fma_f32 v162, v161, -2.0, 1.0
	v_sub_f32_e32 v163, v176, v162
	v_fma_f32 v176, v159, v163, v162
	v_fma_f32 v164, |v176|, s17, v113
	v_fma_f32 v165, |v176|, s18, v114
	v_fma_f32 v166, |v176|, s19, v115
	v_lshrrev_b32_e32 v167, 26, v176
	v_min3_u32 v164, v164, v165, v166
	v_bfi_b32 v168, 31, v164, v167
	v_lshrrev_b32_e32 v169, v181, v168
	global_store_short_d16_hi v185, v176, s[48:49]
	v_mul_u32_u24_dpp v170, v168, v180 quad_perm:[1,2,3,3] row_mask:0xf bank_mask:0xf bound_ctrl:1
	v_or_b32_e32 v171, v169, v170
	ds_write_b8 v184, v171
	s_waitcnt lgkmcnt(0)
	s_barrier
	ds_read_b64 v[122:123], v105 offset:0
	ds_read_b64 v[124:125], v105 offset:8
	ds_read_b64 v[126:127], v105 offset:16
	s_barrier
	ds_read_b64 v[128:129], v105 offset:96
	ds_read_b64 v[130:131], v105 offset:104
	ds_read_b64 v[132:133], v105 offset:112
	s_waitcnt lgkmcnt(3)
	v_mfma_scale_f32_16x16x128_f8f6f4 v[134:137], v[122:127], v[2:7], 0, v178, v112 op_sel_hi:[0,0,0] cbsz:2 blgp:2
	v_mfma_scale_f32_16x16x128_f8f6f4 v[138:141], v[122:127], v[14:19], 0, v178, v112 op_sel_hi:[0,0,0] cbsz:2 blgp:2
	v_mfma_scale_f32_16x16x128_f8f6f4 v[142:145], v[122:127], v[26:31], v[188:191], v178, v112 op_sel_hi:[0,0,0] cbsz:2 blgp:2
	v_mfma_scale_f32_16x16x128_f8f6f4 v[134:137], v[122:127], v[38:43], v[134:137], v179, v112 op_sel_hi:[0,0,0] cbsz:2 blgp:2
	v_mfma_scale_f32_16x16x128_f8f6f4 v[138:141], v[122:127], v[50:55], v[138:141], v179, v112 op_sel_hi:[0,0,0] cbsz:2 blgp:2
	v_mfma_scale_f32_16x16x128_f8f6f4 v[142:145], v[122:127], v[62:67], v[142:145], v179, v112 op_sel_hi:[0,0,0] cbsz:2 blgp:2
	s_waitcnt lgkmcnt(0)
	v_mfma_scale_f32_16x16x128_f8f6f4 v[134:137], v[128:133], v[8:13], v[134:137], v178, v112 op_sel_hi:[0,0,0] cbsz:2 blgp:2
	v_mfma_scale_f32_16x16x128_f8f6f4 v[134:137], v[128:133], v[44:49], v[134:137], v179, v112 op_sel_hi:[0,0,0] cbsz:2 blgp:2
	v_mfma_scale_f32_16x16x128_f8f6f4 v[138:141], v[128:133], v[20:25], v[138:141], v178, v112 op_sel_hi:[0,0,0] cbsz:2 blgp:2
	v_mfma_scale_f32_16x16x128_f8f6f4 v[138:141], v[128:133], v[56:61], v[138:141], v179, v112 op_sel_hi:[0,0,0] cbsz:2 blgp:2
	v_mfma_scale_f32_16x16x128_f8f6f4 v[142:145], v[128:133], v[32:37], v[142:145], v178, v112 op_sel_hi:[0,0,0] cbsz:2 blgp:2
	v_mfma_scale_f32_16x16x128_f8f6f4 v[142:145], v[128:133], v[68:73], v[142:145], v179, v112 op_sel_hi:[0,0,0] cbsz:2 blgp:2
	v_fma_mix_f32 v158, v134, v100, v149 op_sel_hi:[0,0,1]
	v_exp_f32_e32 v158, v158
	v_fma_mix_f32 v159, v138, v101, v153 op_sel_hi:[0,0,1]
	v_exp_f32_e32 v159, v159
	v_fma_f32 v158, v158, v186, v186
	v_rcp_f32_e32 v158, v158
	v_add_f32_e32 v159, 1.0, v159
	v_rcp_f32_e32 v159, v159
	s_nop 0
	v_fma_mix_f32 v161, v158, v142, v157 op_sel_hi:[0,0,1]
	v_exp_f32_e32 v161, v161
	s_add_u32 s48, s48, s40
	v_add_f32_e32 v161, 1.0, v161
	v_rcp_f32_e32 v161, v161
	s_addc_u32 s49, s49, s41
	v_fma_f32 v162, v161, -2.0, 1.0
	v_sub_f32_e32 v163, v176, v162
	v_fma_f32 v176, v159, v163, v162
	v_fma_f32 v164, |v176|, s17, v113
	v_fma_f32 v165, |v176|, s18, v114
	v_fma_f32 v166, |v176|, s19, v115
	v_lshrrev_b32_e32 v167, 26, v176
	v_min3_u32 v164, v164, v165, v166
	v_bfi_b32 v168, 31, v164, v167
	v_lshrrev_b32_e32 v169, v181, v168
	global_store_short_d16_hi v185, v176, s[48:49]
	v_mul_u32_u24_dpp v170, v168, v180 quad_perm:[1,2,3,3] row_mask:0xf bank_mask:0xf bound_ctrl:1
	v_or_b32_e32 v171, v169, v170
	ds_write_b8 v184, v171 offset:416
	s_waitcnt lgkmcnt(0)
	s_barrier
	ds_read_b64 v[122:123], v105 offset:416
	ds_read_b64 v[124:125], v105 offset:424
	ds_read_b64 v[126:127], v105 offset:432
	s_barrier
	ds_read_b64 v[128:129], v105 offset:512
	ds_read_b64 v[130:131], v105 offset:520
	ds_read_b64 v[132:133], v105 offset:528
	s_add_i32 s44, s44, 16
	s_waitcnt lgkmcnt(3)
	v_mfma_scale_f32_16x16x128_f8f6f4 v[134:137], v[122:127], v[2:7], 0, v178, v112 op_sel_hi:[0,0,0] cbsz:2 blgp:2
	v_mfma_scale_f32_16x16x128_f8f6f4 v[138:141], v[122:127], v[14:19], 0, v178, v112 op_sel_hi:[0,0,0] cbsz:2 blgp:2
	v_mfma_scale_f32_16x16x128_f8f6f4 v[142:145], v[122:127], v[26:31], v[188:191], v178, v112 op_sel_hi:[0,0,0] cbsz:2 blgp:2
	v_mfma_scale_f32_16x16x128_f8f6f4 v[134:137], v[122:127], v[38:43], v[134:137], v179, v112 op_sel_hi:[0,0,0] cbsz:2 blgp:2
	v_mfma_scale_f32_16x16x128_f8f6f4 v[138:141], v[122:127], v[50:55], v[138:141], v179, v112 op_sel_hi:[0,0,0] cbsz:2 blgp:2
	v_mfma_scale_f32_16x16x128_f8f6f4 v[142:145], v[122:127], v[62:67], v[142:145], v179, v112 op_sel_hi:[0,0,0] cbsz:2 blgp:2
	s_waitcnt lgkmcnt(0)
	v_mfma_scale_f32_16x16x128_f8f6f4 v[134:137], v[128:133], v[8:13], v[134:137], v178, v112 op_sel_hi:[0,0,0] cbsz:2 blgp:2
	v_mfma_scale_f32_16x16x128_f8f6f4 v[134:137], v[128:133], v[44:49], v[134:137], v179, v112 op_sel_hi:[0,0,0] cbsz:2 blgp:2
	v_mfma_scale_f32_16x16x128_f8f6f4 v[138:141], v[128:133], v[20:25], v[138:141], v178, v112 op_sel_hi:[0,0,0] cbsz:2 blgp:2
	v_mfma_scale_f32_16x16x128_f8f6f4 v[138:141], v[128:133], v[56:61], v[138:141], v179, v112 op_sel_hi:[0,0,0] cbsz:2 blgp:2
	v_mfma_scale_f32_16x16x128_f8f6f4 v[142:145], v[128:133], v[32:37], v[142:145], v178, v112 op_sel_hi:[0,0,0] cbsz:2 blgp:2
	v_mfma_scale_f32_16x16x128_f8f6f4 v[142:145], v[128:133], v[68:73], v[142:145], v179, v112 op_sel_hi:[0,0,0] cbsz:2 blgp:2
	v_fma_mix_f32 v158, v134, v100, v149 op_sel:[0,0,1] op_sel_hi:[0,0,1]
	v_exp_f32_e32 v158, v158
	v_fma_mix_f32 v159, v138, v101, v153 op_sel:[0,0,1] op_sel_hi:[0,0,1]
	v_exp_f32_e32 v159, v159
	v_fma_f32 v158, v158, v186, v186
	v_rcp_f32_e32 v158, v158
	v_add_f32_e32 v159, 1.0, v159
	v_rcp_f32_e32 v159, v159
	s_nop 0
	v_fma_mix_f32 v161, v158, v142, v157 op_sel:[0,0,1] op_sel_hi:[0,0,1]
	v_exp_f32_e32 v161, v161
	s_add_u32 s48, s48, s40
	v_add_f32_e32 v161, 1.0, v161
	v_rcp_f32_e32 v161, v161
	s_addc_u32 s49, s49, s41
	v_fma_f32 v162, v161, -2.0, 1.0
	v_sub_f32_e32 v163, v176, v162
	v_fma_f32 v176, v159, v163, v162
	v_fma_f32 v164, |v176|, s17, v113
	v_fma_f32 v165, |v176|, s18, v114
	v_fma_f32 v166, |v176|, s19, v115
	v_lshrrev_b32_e32 v167, 26, v176
	v_min3_u32 v164, v164, v165, v166
	v_bfi_b32 v168, 31, v164, v167
	v_lshrrev_b32_e32 v169, v181, v168
	global_store_short_d16_hi v185, v176, s[48:49]
	v_mul_u32_u24_dpp v170, v168, v180 quad_perm:[1,2,3,3] row_mask:0xf bank_mask:0xf bound_ctrl:1
	v_or_b32_e32 v171, v169, v170
	ds_write_b8 v184, v171
	s_waitcnt lgkmcnt(0)
	s_barrier
	ds_read_b64 v[122:123], v105 offset:0
	ds_read_b64 v[124:125], v105 offset:8
	ds_read_b64 v[126:127], v105 offset:16
	s_cmp_lt_i32 s44, s45
	s_barrier
	s_cbranch_scc1 .Lscan_loop_a_f2
	s_branch .Lscan_exit_f2
.Lscan_loop_b_f2:
	ds_read_b64 v[128:129], v105 offset:96
	ds_read_b64 v[130:131], v105 offset:104
	ds_read_b64 v[132:133], v105 offset:112
	s_waitcnt vmcnt(8)
	global_load_dwordx4 v[146:149], v[196:197], off
	global_load_dwordx4 v[150:153], v[196:197], off offset:512
	global_load_dwordx4 v[154:157], v[196:197], off offset:1024
	v_lshl_add_u64 v[196:197], v[196:197], 0, s[42:43]
	s_waitcnt lgkmcnt(3)
	v_mfma_scale_f32_16x16x128_f8f6f4 v[134:137], v[122:127], v[2:7], 0, v178, v112 op_sel_hi:[0,0,0] cbsz:2 blgp:2
	v_mfma_scale_f32_16x16x128_f8f6f4 v[138:141], v[122:127], v[14:19], 0, v178, v112 op_sel_hi:[0,0,0] cbsz:2 blgp:2
	v_mfma_scale_f32_16x16x128_f8f6f4 v[142:145], v[122:127], v[26:31], v[188:191], v178, v112 op_sel_hi:[0,0,0] cbsz:2 blgp:2
	v_mfma_scale_f32_16x16x128_f8f6f4 v[134:137], v[122:127], v[38:43], v[134:137], v179, v112 op_sel_hi:[0,0,0] cbsz:2 blgp:2
	v_mfma_scale_f32_16x16x128_f8f6f4 v[138:141], v[122:127], v[50:55], v[138:141], v179, v112 op_sel_hi:[0,0,0] cbsz:2 blgp:2
	v_mfma_scale_f32_16x16x128_f8f6f4 v[142:145], v[122:127], v[62:67], v[142:145], v179, v112 op_sel_hi:[0,0,0] cbsz:2 blgp:2
	s_waitcnt lgkmcnt(0)
	v_mfma_scale_f32_16x16x128_f8f6f4 v[134:137], v[128:133], v[8:13], v[134:137], v178, v112 op_sel_hi:[0,0,0] cbsz:2 blgp:2
	v_mfma_scale_f32_16x16x128_f8f6f4 v[134:137], v[128:133], v[44:49], v[134:137], v179, v112 op_sel_hi:[0,0,0] cbsz:2 blgp:2
	v_mfma_scale_f32_16x16x128_f8f6f4 v[138:141], v[128:133], v[20:25], v[138:141], v178, v112 op_sel_hi:[0,0,0] cbsz:2 blgp:2
	v_mfma_scale_f32_16x16x128_f8f6f4 v[138:141], v[128:133], v[56:61], v[138:141], v179, v112 op_sel_hi:[0,0,0] cbsz:2 blgp:2
	v_mfma_scale_f32_16x16x128_f8f6f4 v[142:145], v[128:133], v[32:37], v[142:145], v178, v112 op_sel_hi:[0,0,0] cbsz:2 blgp:2
	v_mfma_scale_f32_16x16x128_f8f6f4 v[142:145], v[128:133], v[68:73], v[142:145], v179, v112 op_sel_hi:[0,0,0] cbsz:2 blgp:2
	v_fma_mix_f32 v158, v134, v100, v82 op_sel_hi:[0,0,1]
	v_exp_f32_e32 v158, v158
	v_fma_mix_f32 v159, v138, v101, v74 op_sel_hi:[0,0,1]
	v_exp_f32_e32 v159, v159
	v_fma_f32 v158, v158, v186, v186
	v_rcp_f32_e32 v158, v158
	v_add_f32_e32 v159, 1.0, v159
	v_rcp_f32_e32 v159, v159
	s_nop 0
	v_fma_mix_f32 v161, v158, v142, v78 op_sel_hi:[0,0,1]
	v_exp_f32_e32 v161, v161
	s_add_u32 s48, s48, s40
	v_add_f32_e32 v161, 1.0, v161
	v_rcp_f32_e32 v161, v161
	s_addc_u32 s49, s49, s41
	v_fma_f32 v162, v161, -2.0, 1.0
	v_sub_f32_e32 v163, v176, v162
	v_fma_f32 v176, v159, v163, v162
	v_fma_f32 v164, |v176|, s17, v113
	v_fma_f32 v165, |v176|, s18, v114
	v_fma_f32 v166, |v176|, s19, v115
	v_lshrrev_b32_e32 v167, 26, v176
	v_min3_u32 v164, v164, v165, v166
	v_bfi_b32 v168, 31, v164, v167
	v_lshrrev_b32_e32 v169, v181, v168
	global_store_short_d16_hi v185, v176, s[48:49]
	v_mul_u32_u24_dpp v170, v168, v180 quad_perm:[1,2,3,3] row_mask:0xf bank_mask:0xf bound_ctrl:1
	v_or_b32_e32 v171, v169, v170
	ds_write_b8 v184, v171 offset:416
	s_barrier
	ds_read_b64 v[122:123], v105 offset:416
	ds_read_b64 v[124:125], v105 offset:424
	ds_read_b64 v[126:127], v105 offset:432
	s_waitcnt lgkmcnt(3)
	s_barrier
	ds_read_b64 v[128:129], v105 offset:512
	ds_read_b64 v[130:131], v105 offset:520
	ds_read_b64 v[132:133], v105 offset:528
	s_waitcnt lgkmcnt(3)
	v_mfma_scale_f32_16x16x128_f8f6f4 v[134:137], v[122:127], v[2:7], 0, v178, v112 op_sel_hi:[0,0,0] cbsz:2 blgp:2
	v_mfma_scale_f32_16x16x128_f8f6f4 v[138:141], v[122:127], v[14:19], 0, v178, v112 op_sel_hi:[0,0,0] cbsz:2 blgp:2
	v_mfma_scale_f32_16x16x128_f8f6f4 v[142:145], v[122:127], v[26:31], v[188:191], v178, v112 op_sel_hi:[0,0,0] cbsz:2 blgp:2
	v_mfma_scale_f32_16x16x128_f8f6f4 v[134:137], v[122:127], v[38:43], v[134:137], v179, v112 op_sel_hi:[0,0,0] cbsz:2 blgp:2
	v_mfma_scale_f32_16x16x128_f8f6f4 v[138:141], v[122:127], v[50:55], v[138:141], v179, v112 op_sel_hi:[0,0,0] cbsz:2 blgp:2
	v_mfma_scale_f32_16x16x128_f8f6f4 v[142:145], v[122:127], v[62:67], v[142:145], v179, v112 op_sel_hi:[0,0,0] cbsz:2 blgp:2
	s_waitcnt lgkmcnt(0)
	v_mfma_scale_f32_16x16x128_f8f6f4 v[134:137], v[128:133], v[8:13], v[134:137], v178, v112 op_sel_hi:[0,0,0] cbsz:2 blgp:2
	v_mfma_scale_f32_16x16x128_f8f6f4 v[134:137], v[128:133], v[44:49], v[134:137], v179, v112 op_sel_hi:[0,0,0] cbsz:2 blgp:2
	v_mfma_scale_f32_16x16x128_f8f6f4 v[138:141], v[128:133], v[20:25], v[138:141], v178, v112 op_sel_hi:[0,0,0] cbsz:2 blgp:2
	v_mfma_scale_f32_16x16x128_f8f6f4 v[138:141], v[128:133], v[56:61], v[138:141], v179, v112 op_sel_hi:[0,0,0] cbsz:2 blgp:2
	v_mfma_scale_f32_16x16x128_f8f6f4 v[142:145], v[128:133], v[32:37], v[142:145], v178, v112 op_sel_hi:[0,0,0] cbsz:2 blgp:2
	v_mfma_scale_f32_16x16x128_f8f6f4 v[142:145], v[128:133], v[68:73], v[142:145], v179, v112 op_sel_hi:[0,0,0] cbsz:2 blgp:2
	v_fma_mix_f32 v158, v134, v100, v82 op_sel:[0,0,1] op_sel_hi:[0,0,1]
	v_exp_f32_e32 v158, v158
	v_fma_mix_f32 v159, v138, v101, v74 op_sel:[0,0,1] op_sel_hi:[0,0,1]
	v_exp_f32_e32 v159, v159
	v_fma_f32 v158, v158, v186, v186
	v_rcp_f32_e32 v158, v158
	v_add_f32_e32 v159, 1.0, v159
	v_rcp_f32_e32 v159, v159
	s_nop 0
	v_fma_mix_f32 v161, v158, v142, v78 op_sel:[0,0,1] op_sel_hi:[0,0,1]
	v_exp_f32_e32 v161, v161
	s_add_u32 s48, s48, s40
	v_add_f32_e32 v161, 1.0, v161
	v_rcp_f32_e32 v161, v161
	s_addc_u32 s49, s49, s41
	v_fma_f32 v162, v161, -2.0, 1.0
	v_sub_f32_e32 v163, v176, v162
	v_fma_f32 v176, v159, v163, v162
	v_fma_f32 v164, |v176|, s17, v113
	v_fma_f32 v165, |v176|, s18, v114
	v_fma_f32 v166, |v176|, s19, v115
	v_lshrrev_b32_e32 v167, 26, v176
	v_min3_u32 v164, v164, v165, v166
	v_bfi_b32 v168, 31, v164, v167
	v_lshrrev_b32_e32 v169, v181, v168
	global_store_short_d16_hi v185, v176, s[48:49]
	v_mul_u32_u24_dpp v170, v168, v180 quad_perm:[1,2,3,3] row_mask:0xf bank_mask:0xf bound_ctrl:1
	v_or_b32_e32 v171, v169, v170
	ds_write_b8 v184, v171
	s_barrier
	ds_read_b64 v[122:123], v105 offset:0
	ds_read_b64 v[124:125], v105 offset:8
	ds_read_b64 v[126:127], v105 offset:16
	s_waitcnt lgkmcnt(3)
	s_barrier
	ds_read_b64 v[128:129], v105 offset:96
	ds_read_b64 v[130:131], v105 offset:104
	ds_read_b64 v[132:133], v105 offset:112
	s_waitcnt lgkmcnt(3)
	v_mfma_scale_f32_16x16x128_f8f6f4 v[134:137], v[122:127], v[2:7], 0, v178, v112 op_sel_hi:[0,0,0] cbsz:2 blgp:2
	v_mfma_scale_f32_16x16x128_f8f6f4 v[138:141], v[122:127], v[14:19], 0, v178, v112 op_sel_hi:[0,0,0] cbsz:2 blgp:2
	v_mfma_scale_f32_16x16x128_f8f6f4 v[142:145], v[122:127], v[26:31], v[188:191], v178, v112 op_sel_hi:[0,0,0] cbsz:2 blgp:2
	v_mfma_scale_f32_16x16x128_f8f6f4 v[134:137], v[122:127], v[38:43], v[134:137], v179, v112 op_sel_hi:[0,0,0] cbsz:2 blgp:2
	v_mfma_scale_f32_16x16x128_f8f6f4 v[138:141], v[122:127], v[50:55], v[138:141], v179, v112 op_sel_hi:[0,0,0] cbsz:2 blgp:2
	v_mfma_scale_f32_16x16x128_f8f6f4 v[142:145], v[122:127], v[62:67], v[142:145], v179, v112 op_sel_hi:[0,0,0] cbsz:2 blgp:2
	s_waitcnt lgkmcnt(0)
	v_mfma_scale_f32_16x16x128_f8f6f4 v[134:137], v[128:133], v[8:13], v[134:137], v178, v112 op_sel_hi:[0,0,0] cbsz:2 blgp:2
	v_mfma_scale_f32_16x16x128_f8f6f4 v[134:137], v[128:133], v[44:49], v[134:137], v179, v112 op_sel_hi:[0,0,0] cbsz:2 blgp:2
	v_mfma_scale_f32_16x16x128_f8f6f4 v[138:141], v[128:133], v[20:25], v[138:141], v178, v112 op_sel_hi:[0,0,0] cbsz:2 blgp:2
	v_mfma_scale_f32_16x16x128_f8f6f4 v[138:141], v[128:133], v[56:61], v[138:141], v179, v112 op_sel_hi:[0,0,0] cbsz:2 blgp:2
	v_mfma_scale_f32_16x16x128_f8f6f4 v[142:145], v[128:133], v[32:37], v[142:145], v178, v112 op_sel_hi:[0,0,0] cbsz:2 blgp:2
	v_mfma_scale_f32_16x16x128_f8f6f4 v[142:145], v[128:133], v[68:73], v[142:145], v179, v112 op_sel_hi:[0,0,0] cbsz:2 blgp:2
	v_fma_mix_f32 v158, v134, v100, v83 op_sel_hi:[0,0,1]
	v_exp_f32_e32 v158, v158
	v_fma_mix_f32 v159, v138, v101, v75 op_sel_hi:[0,0,1]
	v_exp_f32_e32 v159, v159
	v_fma_f32 v158, v158, v186, v186
	v_rcp_f32_e32 v158, v158
	v_add_f32_e32 v159, 1.0, v159
	v_rcp_f32_e32 v159, v159
	s_nop 0
	v_fma_mix_f32 v161, v158, v142, v79 op_sel_hi:[0,0,1]
	v_exp_f32_e32 v161, v161
	s_add_u32 s48, s48, s40
	v_add_f32_e32 v161, 1.0, v161
	v_rcp_f32_e32 v161, v161
	s_addc_u32 s49, s49, s41
	v_fma_f32 v162, v161, -2.0, 1.0
	v_sub_f32_e32 v163, v176, v162
	v_fma_f32 v176, v159, v163, v162
	v_fma_f32 v164, |v176|, s17, v113
	v_fma_f32 v165, |v176|, s18, v114
	v_fma_f32 v166, |v176|, s19, v115
	v_lshrrev_b32_e32 v167, 26, v176
	v_min3_u32 v164, v164, v165, v166
	v_bfi_b32 v168, 31, v164, v167
	v_lshrrev_b32_e32 v169, v181, v168
	global_store_short_d16_hi v185, v176, s[48:49]
	v_mul_u32_u24_dpp v170, v168, v180 quad_perm:[1,2,3,3] row_mask:0xf bank_mask:0xf bound_ctrl:1
	v_or_b32_e32 v171, v169, v170
	ds_write_b8 v184, v171 offset:416
	s_barrier
	ds_read_b64 v[122:123], v105 offset:416
	ds_read_b64 v[124:125], v105 offset:424
	ds_read_b64 v[126:127], v105 offset:432
	s_waitcnt lgkmcnt(3)
	s_barrier
	ds_read_b64 v[128:129], v105 offset:512
	ds_read_b64 v[130:131], v105 offset:520
	ds_read_b64 v[132:133], v105 offset:528
	s_waitcnt lgkmcnt(3)
	v_mfma_scale_f32_16x16x128_f8f6f4 v[134:137], v[122:127], v[2:7], 0, v178, v112 op_sel_hi:[0,0,0] cbsz:2 blgp:2
	v_mfma_scale_f32_16x16x128_f8f6f4 v[138:141], v[122:127], v[14:19], 0, v178, v112 op_sel_hi:[0,0,0] cbsz:2 blgp:2
	v_mfma_scale_f32_16x16x128_f8f6f4 v[142:145], v[122:127], v[26:31], v[188:191], v178, v112 op_sel_hi:[0,0,0] cbsz:2 blgp:2
	v_mfma_scale_f32_16x16x128_f8f6f4 v[134:137], v[122:127], v[38:43], v[134:137], v179, v112 op_sel_hi:[0,0,0] cbsz:2 blgp:2
	v_mfma_scale_f32_16x16x128_f8f6f4 v[138:141], v[122:127], v[50:55], v[138:141], v179, v112 op_sel_hi:[0,0,0] cbsz:2 blgp:2
	v_mfma_scale_f32_16x16x128_f8f6f4 v[142:145], v[122:127], v[62:67], v[142:145], v179, v112 op_sel_hi:[0,0,0] cbsz:2 blgp:2
	s_waitcnt lgkmcnt(0)
	v_mfma_scale_f32_16x16x128_f8f6f4 v[134:137], v[128:133], v[8:13], v[134:137], v178, v112 op_sel_hi:[0,0,0] cbsz:2 blgp:2
	v_mfma_scale_f32_16x16x128_f8f6f4 v[134:137], v[128:133], v[44:49], v[134:137], v179, v112 op_sel_hi:[0,0,0] cbsz:2 blgp:2
	v_mfma_scale_f32_16x16x128_f8f6f4 v[138:141], v[128:133], v[20:25], v[138:141], v178, v112 op_sel_hi:[0,0,0] cbsz:2 blgp:2
	v_mfma_scale_f32_16x16x128_f8f6f4 v[138:141], v[128:133], v[56:61], v[138:141], v179, v112 op_sel_hi:[0,0,0] cbsz:2 blgp:2
	v_mfma_scale_f32_16x16x128_f8f6f4 v[142:145], v[128:133], v[32:37], v[142:145], v178, v112 op_sel_hi:[0,0,0] cbsz:2 blgp:2
	v_mfma_scale_f32_16x16x128_f8f6f4 v[142:145], v[128:133], v[68:73], v[142:145], v179, v112 op_sel_hi:[0,0,0] cbsz:2 blgp:2
	v_fma_mix_f32 v158, v134, v100, v83 op_sel:[0,0,1] op_sel_hi:[0,0,1]
	v_exp_f32_e32 v158, v158
	v_fma_mix_f32 v159, v138, v101, v75 op_sel:[0,0,1] op_sel_hi:[0,0,1]
	v_exp_f32_e32 v159, v159
	v_fma_f32 v158, v158, v186, v186
	v_rcp_f32_e32 v158, v158
	v_add_f32_e32 v159, 1.0, v159
	v_rcp_f32_e32 v159, v159
	s_nop 0
	v_fma_mix_f32 v161, v158, v142, v79 op_sel:[0,0,1] op_sel_hi:[0,0,1]
	v_exp_f32_e32 v161, v161
	s_add_u32 s48, s48, s40
	v_add_f32_e32 v161, 1.0, v161
	v_rcp_f32_e32 v161, v161
	s_addc_u32 s49, s49, s41
	v_fma_f32 v162, v161, -2.0, 1.0
	v_sub_f32_e32 v163, v176, v162
	v_fma_f32 v176, v159, v163, v162
	v_fma_f32 v164, |v176|, s17, v113
	v_fma_f32 v165, |v176|, s18, v114
	v_fma_f32 v166, |v176|, s19, v115
	v_lshrrev_b32_e32 v167, 26, v176
	v_min3_u32 v164, v164, v165, v166
	v_bfi_b32 v168, 31, v164, v167
	v_lshrrev_b32_e32 v169, v181, v168
	global_store_short_d16_hi v185, v176, s[48:49]
	v_mul_u32_u24_dpp v170, v168, v180 quad_perm:[1,2,3,3] row_mask:0xf bank_mask:0xf bound_ctrl:1
	v_or_b32_e32 v171, v169, v170
	ds_write_b8 v184, v171
	s_barrier
	ds_read_b64 v[122:123], v105 offset:0
	ds_read_b64 v[124:125], v105 offset:8
	ds_read_b64 v[126:127], v105 offset:16
	s_waitcnt lgkmcnt(3)
	s_barrier
	ds_read_b64 v[128:129], v105 offset:96
	ds_read_b64 v[130:131], v105 offset:104
	ds_read_b64 v[132:133], v105 offset:112
	s_waitcnt lgkmcnt(3)
	v_mfma_scale_f32_16x16x128_f8f6f4 v[134:137], v[122:127], v[2:7], 0, v178, v112 op_sel_hi:[0,0,0] cbsz:2 blgp:2
	v_mfma_scale_f32_16x16x128_f8f6f4 v[138:141], v[122:127], v[14:19], 0, v178, v112 op_sel_hi:[0,0,0] cbsz:2 blgp:2
	v_mfma_scale_f32_16x16x128_f8f6f4 v[142:145], v[122:127], v[26:31], v[188:191], v178, v112 op_sel_hi:[0,0,0] cbsz:2 blgp:2
	v_mfma_scale_f32_16x16x128_f8f6f4 v[134:137], v[122:127], v[38:43], v[134:137], v179, v112 op_sel_hi:[0,0,0] cbsz:2 blgp:2
	v_mfma_scale_f32_16x16x128_f8f6f4 v[138:141], v[122:127], v[50:55], v[138:141], v179, v112 op_sel_hi:[0,0,0] cbsz:2 blgp:2
	v_mfma_scale_f32_16x16x128_f8f6f4 v[142:145], v[122:127], v[62:67], v[142:145], v179, v112 op_sel_hi:[0,0,0] cbsz:2 blgp:2
	s_waitcnt lgkmcnt(0)
	v_mfma_scale_f32_16x16x128_f8f6f4 v[134:137], v[128:133], v[8:13], v[134:137], v178, v112 op_sel_hi:[0,0,0] cbsz:2 blgp:2
	v_mfma_scale_f32_16x16x128_f8f6f4 v[134:137], v[128:133], v[44:49], v[134:137], v179, v112 op_sel_hi:[0,0,0] cbsz:2 blgp:2
	v_mfma_scale_f32_16x16x128_f8f6f4 v[138:141], v[128:133], v[20:25], v[138:141], v178, v112 op_sel_hi:[0,0,0] cbsz:2 blgp:2
	v_mfma_scale_f32_16x16x128_f8f6f4 v[138:141], v[128:133], v[56:61], v[138:141], v179, v112 op_sel_hi:[0,0,0] cbsz:2 blgp:2
	v_mfma_scale_f32_16x16x128_f8f6f4 v[142:145], v[128:133], v[32:37], v[142:145], v178, v112 op_sel_hi:[0,0,0] cbsz:2 blgp:2
	v_mfma_scale_f32_16x16x128_f8f6f4 v[142:145], v[128:133], v[68:73], v[142:145], v179, v112 op_sel_hi:[0,0,0] cbsz:2 blgp:2
	v_fma_mix_f32 v158, v134, v100, v84 op_sel_hi:[0,0,1]
	v_exp_f32_e32 v158, v158
	v_fma_mix_f32 v159, v138, v101, v76 op_sel_hi:[0,0,1]
	v_exp_f32_e32 v159, v159
	v_fma_f32 v158, v158, v186, v186
	v_rcp_f32_e32 v158, v158
	v_add_f32_e32 v159, 1.0, v159
	v_rcp_f32_e32 v159, v159
	s_nop 0
	v_fma_mix_f32 v161, v158, v142, v80 op_sel_hi:[0,0,1]
	v_exp_f32_e32 v161, v161
	s_add_u32 s48, s48, s40
	v_add_f32_e32 v161, 1.0, v161
	v_rcp_f32_e32 v161, v161
	s_addc_u32 s49, s49, s41
	v_fma_f32 v162, v161, -2.0, 1.0
	v_sub_f32_e32 v163, v176, v162
	v_fma_f32 v176, v159, v163, v162
	v_fma_f32 v164, |v176|, s17, v113
	v_fma_f32 v165, |v176|, s18, v114
	v_fma_f32 v166, |v176|, s19, v115
	v_lshrrev_b32_e32 v167, 26, v176
	v_min3_u32 v164, v164, v165, v166
	v_bfi_b32 v168, 31, v164, v167
	v_lshrrev_b32_e32 v169, v181, v168
	global_store_short_d16_hi v185, v176, s[48:49]
	v_mul_u32_u24_dpp v170, v168, v180 quad_perm:[1,2,3,3] row_mask:0xf bank_mask:0xf bound_ctrl:1
	v_or_b32_e32 v171, v169, v170
	ds_write_b8 v184, v171 offset:416
	s_barrier
	ds_read_b64 v[122:123], v105 offset:416
	ds_read_b64 v[124:125], v105 offset:424
	ds_read_b64 v[126:127], v105 offset:432
	s_waitcnt lgkmcnt(3)
	s_barrier
	ds_read_b64 v[128:129], v105 offset:512
	ds_read_b64 v[130:131], v105 offset:520
	ds_read_b64 v[132:133], v105 offset:528
	s_waitcnt lgkmcnt(3)
	v_mfma_scale_f32_16x16x128_f8f6f4 v[134:137], v[122:127], v[2:7], 0, v178, v112 op_sel_hi:[0,0,0] cbsz:2 blgp:2
	v_mfma_scale_f32_16x16x128_f8f6f4 v[138:141], v[122:127], v[14:19], 0, v178, v112 op_sel_hi:[0,0,0] cbsz:2 blgp:2
	v_mfma_scale_f32_16x16x128_f8f6f4 v[142:145], v[122:127], v[26:31], v[188:191], v178, v112 op_sel_hi:[0,0,0] cbsz:2 blgp:2
	v_mfma_scale_f32_16x16x128_f8f6f4 v[134:137], v[122:127], v[38:43], v[134:137], v179, v112 op_sel_hi:[0,0,0] cbsz:2 blgp:2
	v_mfma_scale_f32_16x16x128_f8f6f4 v[138:141], v[122:127], v[50:55], v[138:141], v179, v112 op_sel_hi:[0,0,0] cbsz:2 blgp:2
	v_mfma_scale_f32_16x16x128_f8f6f4 v[142:145], v[122:127], v[62:67], v[142:145], v179, v112 op_sel_hi:[0,0,0] cbsz:2 blgp:2
	s_waitcnt lgkmcnt(0)
	v_mfma_scale_f32_16x16x128_f8f6f4 v[134:137], v[128:133], v[8:13], v[134:137], v178, v112 op_sel_hi:[0,0,0] cbsz:2 blgp:2
	v_mfma_scale_f32_16x16x128_f8f6f4 v[134:137], v[128:133], v[44:49], v[134:137], v179, v112 op_sel_hi:[0,0,0] cbsz:2 blgp:2
	v_mfma_scale_f32_16x16x128_f8f6f4 v[138:141], v[128:133], v[20:25], v[138:141], v178, v112 op_sel_hi:[0,0,0] cbsz:2 blgp:2
	v_mfma_scale_f32_16x16x128_f8f6f4 v[138:141], v[128:133], v[56:61], v[138:141], v179, v112 op_sel_hi:[0,0,0] cbsz:2 blgp:2
	v_mfma_scale_f32_16x16x128_f8f6f4 v[142:145], v[128:133], v[32:37], v[142:145], v178, v112 op_sel_hi:[0,0,0] cbsz:2 blgp:2
	v_mfma_scale_f32_16x16x128_f8f6f4 v[142:145], v[128:133], v[68:73], v[142:145], v179, v112 op_sel_hi:[0,0,0] cbsz:2 blgp:2
	v_fma_mix_f32 v158, v134, v100, v84 op_sel:[0,0,1] op_sel_hi:[0,0,1]
	v_exp_f32_e32 v158, v158
	v_fma_mix_f32 v159, v138, v101, v76 op_sel:[0,0,1] op_sel_hi:[0,0,1]
	v_exp_f32_e32 v159, v159
	v_fma_f32 v158, v158, v186, v186
	v_rcp_f32_e32 v158, v158
	v_add_f32_e32 v159, 1.0, v159
	v_rcp_f32_e32 v159, v159
	s_nop 0
	v_fma_mix_f32 v161, v158, v142, v80 op_sel:[0,0,1] op_sel_hi:[0,0,1]
	v_exp_f32_e32 v161, v161
	s_add_u32 s48, s48, s40
	v_add_f32_e32 v161, 1.0, v161
	v_rcp_f32_e32 v161, v161
	s_addc_u32 s49, s49, s41
	v_fma_f32 v162, v161, -2.0, 1.0
	v_sub_f32_e32 v163, v176, v162
	v_fma_f32 v176, v159, v163, v162
	v_fma_f32 v164, |v176|, s17, v113
	v_fma_f32 v165, |v176|, s18, v114
	v_fma_f32 v166, |v176|, s19, v115
	v_lshrrev_b32_e32 v167, 26, v176
	v_min3_u32 v164, v164, v165, v166
	v_bfi_b32 v168, 31, v164, v167
	v_lshrrev_b32_e32 v169, v181, v168
	global_store_short_d16_hi v185, v176, s[48:49]
	v_mul_u32_u24_dpp v170, v168, v180 quad_perm:[1,2,3,3] row_mask:0xf bank_mask:0xf bound_ctrl:1
	v_or_b32_e32 v171, v169, v170
	ds_write_b8 v184, v171
	s_barrier
	ds_read_b64 v[122:123], v105 offset:0
	ds_read_b64 v[124:125], v105 offset:8
	ds_read_b64 v[126:127], v105 offset:16
	s_waitcnt lgkmcnt(3)
	s_barrier
	ds_read_b64 v[128:129], v105 offset:96
	ds_read_b64 v[130:131], v105 offset:104
	ds_read_b64 v[132:133], v105 offset:112
	s_waitcnt lgkmcnt(3)
	v_mfma_scale_f32_16x16x128_f8f6f4 v[134:137], v[122:127], v[2:7], 0, v178, v112 op_sel_hi:[0,0,0] cbsz:2 blgp:2
	v_mfma_scale_f32_16x16x128_f8f6f4 v[138:141], v[122:127], v[14:19], 0, v178, v112 op_sel_hi:[0,0,0] cbsz:2 blgp:2
	v_mfma_scale_f32_16x16x128_f8f6f4 v[142:145], v[122:127], v[26:31], v[188:191], v178, v112 op_sel_hi:[0,0,0] cbsz:2 blgp:2
	v_mfma_scale_f32_16x16x128_f8f6f4 v[134:137], v[122:127], v[38:43], v[134:137], v179, v112 op_sel_hi:[0,0,0] cbsz:2 blgp:2
	v_mfma_scale_f32_16x16x128_f8f6f4 v[138:141], v[122:127], v[50:55], v[138:141], v179, v112 op_sel_hi:[0,0,0] cbsz:2 blgp:2
	v_mfma_scale_f32_16x16x128_f8f6f4 v[142:145], v[122:127], v[62:67], v[142:145], v179, v112 op_sel_hi:[0,0,0] cbsz:2 blgp:2
	s_waitcnt lgkmcnt(0)
	v_mfma_scale_f32_16x16x128_f8f6f4 v[134:137], v[128:133], v[8:13], v[134:137], v178, v112 op_sel_hi:[0,0,0] cbsz:2 blgp:2
	v_mfma_scale_f32_16x16x128_f8f6f4 v[134:137], v[128:133], v[44:49], v[134:137], v179, v112 op_sel_hi:[0,0,0] cbsz:2 blgp:2
	v_mfma_scale_f32_16x16x128_f8f6f4 v[138:141], v[128:133], v[20:25], v[138:141], v178, v112 op_sel_hi:[0,0,0] cbsz:2 blgp:2
	v_mfma_scale_f32_16x16x128_f8f6f4 v[138:141], v[128:133], v[56:61], v[138:141], v179, v112 op_sel_hi:[0,0,0] cbsz:2 blgp:2
	v_mfma_scale_f32_16x16x128_f8f6f4 v[142:145], v[128:133], v[32:37], v[142:145], v178, v112 op_sel_hi:[0,0,0] cbsz:2 blgp:2
	v_mfma_scale_f32_16x16x128_f8f6f4 v[142:145], v[128:133], v[68:73], v[142:145], v179, v112 op_sel_hi:[0,0,0] cbsz:2 blgp:2
	v_fma_mix_f32 v158, v134, v100, v85 op_sel_hi:[0,0,1]
	v_exp_f32_e32 v158, v158
	v_fma_mix_f32 v159, v138, v101, v77 op_sel_hi:[0,0,1]
	v_exp_f32_e32 v159, v159
	v_fma_f32 v158, v158, v186, v186
	v_rcp_f32_e32 v158, v158
	v_add_f32_e32 v159, 1.0, v159
	v_rcp_f32_e32 v159, v159
	s_nop 0
	v_fma_mix_f32 v161, v158, v142, v81 op_sel_hi:[0,0,1]
	v_exp_f32_e32 v161, v161
	s_add_u32 s48, s48, s40
	v_add_f32_e32 v161, 1.0, v161
	v_rcp_f32_e32 v161, v161
	s_addc_u32 s49, s49, s41
	v_fma_f32 v162, v161, -2.0, 1.0
	v_sub_f32_e32 v163, v176, v162
	v_fma_f32 v176, v159, v163, v162
	v_fma_f32 v164, |v176|, s17, v113
	v_fma_f32 v165, |v176|, s18, v114
	v_fma_f32 v166, |v176|, s19, v115
	v_lshrrev_b32_e32 v167, 26, v176
	v_min3_u32 v164, v164, v165, v166
	v_bfi_b32 v168, 31, v164, v167
	v_lshrrev_b32_e32 v169, v181, v168
	global_store_short_d16_hi v185, v176, s[48:49]
	v_mul_u32_u24_dpp v170, v168, v180 quad_perm:[1,2,3,3] row_mask:0xf bank_mask:0xf bound_ctrl:1
	v_or_b32_e32 v171, v169, v170
	ds_write_b8 v184, v171 offset:416
	s_barrier
	ds_read_b64 v[122:123], v105 offset:416
	ds_read_b64 v[124:125], v105 offset:424
	ds_read_b64 v[126:127], v105 offset:432
	s_waitcnt lgkmcnt(3)
	s_barrier
	ds_read_b64 v[128:129], v105 offset:512
	ds_read_b64 v[130:131], v105 offset:520
	ds_read_b64 v[132:133], v105 offset:528
	s_waitcnt lgkmcnt(3)
	v_mfma_scale_f32_16x16x128_f8f6f4 v[134:137], v[122:127], v[2:7], 0, v178, v112 op_sel_hi:[0,0,0] cbsz:2 blgp:2
	v_mfma_scale_f32_16x16x128_f8f6f4 v[138:141], v[122:127], v[14:19], 0, v178, v112 op_sel_hi:[0,0,0] cbsz:2 blgp:2
	v_mfma_scale_f32_16x16x128_f8f6f4 v[142:145], v[122:127], v[26:31], v[188:191], v178, v112 op_sel_hi:[0,0,0] cbsz:2 blgp:2
	v_mfma_scale_f32_16x16x128_f8f6f4 v[134:137], v[122:127], v[38:43], v[134:137], v179, v112 op_sel_hi:[0,0,0] cbsz:2 blgp:2
	v_mfma_scale_f32_16x16x128_f8f6f4 v[138:141], v[122:127], v[50:55], v[138:141], v179, v112 op_sel_hi:[0,0,0] cbsz:2 blgp:2
	v_mfma_scale_f32_16x16x128_f8f6f4 v[142:145], v[122:127], v[62:67], v[142:145], v179, v112 op_sel_hi:[0,0,0] cbsz:2 blgp:2
	s_waitcnt lgkmcnt(0)
	v_mfma_scale_f32_16x16x128_f8f6f4 v[134:137], v[128:133], v[8:13], v[134:137], v178, v112 op_sel_hi:[0,0,0] cbsz:2 blgp:2
	v_mfma_scale_f32_16x16x128_f8f6f4 v[134:137], v[128:133], v[44:49], v[134:137], v179, v112 op_sel_hi:[0,0,0] cbsz:2 blgp:2
	v_mfma_scale_f32_16x16x128_f8f6f4 v[138:141], v[128:133], v[20:25], v[138:141], v178, v112 op_sel_hi:[0,0,0] cbsz:2 blgp:2
	v_mfma_scale_f32_16x16x128_f8f6f4 v[138:141], v[128:133], v[56:61], v[138:141], v179, v112 op_sel_hi:[0,0,0] cbsz:2 blgp:2
	v_mfma_scale_f32_16x16x128_f8f6f4 v[142:145], v[128:133], v[32:37], v[142:145], v178, v112 op_sel_hi:[0,0,0] cbsz:2 blgp:2
	v_mfma_scale_f32_16x16x128_f8f6f4 v[142:145], v[128:133], v[68:73], v[142:145], v179, v112 op_sel_hi:[0,0,0] cbsz:2 blgp:2
	v_fma_mix_f32 v158, v134, v100, v85 op_sel:[0,0,1] op_sel_hi:[0,0,1]
	v_exp_f32_e32 v158, v158
	v_fma_mix_f32 v159, v138, v101, v77 op_sel:[0,0,1] op_sel_hi:[0,0,1]
	v_exp_f32_e32 v159, v159
	v_fma_f32 v158, v158, v186, v186
	v_rcp_f32_e32 v158, v158
	v_add_f32_e32 v159, 1.0, v159
	v_rcp_f32_e32 v159, v159
	s_nop 0
	v_fma_mix_f32 v161, v158, v142, v81 op_sel:[0,0,1] op_sel_hi:[0,0,1]
	v_exp_f32_e32 v161, v161
	s_add_u32 s48, s48, s40
	v_add_f32_e32 v161, 1.0, v161
	v_rcp_f32_e32 v161, v161
	s_addc_u32 s49, s49, s41
	v_fma_f32 v162, v161, -2.0, 1.0
	v_sub_f32_e32 v163, v176, v162
	v_fma_f32 v176, v159, v163, v162
	v_fma_f32 v164, |v176|, s17, v113
	v_fma_f32 v165, |v176|, s18, v114
	v_fma_f32 v166, |v176|, s19, v115
	v_lshrrev_b32_e32 v167, 26, v176
	v_min3_u32 v164, v164, v165, v166
	v_bfi_b32 v168, 31, v164, v167
	v_lshrrev_b32_e32 v169, v181, v168
	global_store_short_d16_hi v185, v176, s[48:49]
	v_mul_u32_u24_dpp v170, v168, v180 quad_perm:[1,2,3,3] row_mask:0xf bank_mask:0xf bound_ctrl:1
	v_or_b32_e32 v171, v169, v170
	ds_write_b8 v184, v171
	s_barrier
	ds_read_b64 v[122:123], v105 offset:0
	ds_read_b64 v[124:125], v105 offset:8
	ds_read_b64 v[126:127], v105 offset:16
	s_waitcnt lgkmcnt(3)
	s_barrier
	ds_read_b64 v[128:129], v105 offset:96
	ds_read_b64 v[130:131], v105 offset:104
	ds_read_b64 v[132:133], v105 offset:112
	s_waitcnt vmcnt(8)
	global_load_dwordx4 v[82:85], v[196:197], off
	global_load_dwordx4 v[74:77], v[196:197], off offset:512
	global_load_dwordx4 v[78:81], v[196:197], off offset:1024
	v_lshl_add_u64 v[196:197], v[196:197], 0, s[42:43]
	s_waitcnt lgkmcnt(3)
	v_mfma_scale_f32_16x16x128_f8f6f4 v[134:137], v[122:127], v[2:7], 0, v178, v112 op_sel_hi:[0,0,0] cbsz:2 blgp:2
	v_mfma_scale_f32_16x16x128_f8f6f4 v[138:141], v[122:127], v[14:19], 0, v178, v112 op_sel_hi:[0,0,0] cbsz:2 blgp:2
	v_mfma_scale_f32_16x16x128_f8f6f4 v[142:145], v[122:127], v[26:31], v[188:191], v178, v112 op_sel_hi:[0,0,0] cbsz:2 blgp:2
	v_mfma_scale_f32_16x16x128_f8f6f4 v[134:137], v[122:127], v[38:43], v[134:137], v179, v112 op_sel_hi:[0,0,0] cbsz:2 blgp:2
	v_mfma_scale_f32_16x16x128_f8f6f4 v[138:141], v[122:127], v[50:55], v[138:141], v179, v112 op_sel_hi:[0,0,0] cbsz:2 blgp:2
	v_mfma_scale_f32_16x16x128_f8f6f4 v[142:145], v[122:127], v[62:67], v[142:145], v179, v112 op_sel_hi:[0,0,0] cbsz:2 blgp:2
	s_waitcnt lgkmcnt(0)
	v_mfma_scale_f32_16x16x128_f8f6f4 v[134:137], v[128:133], v[8:13], v[134:137], v178, v112 op_sel_hi:[0,0,0] cbsz:2 blgp:2
	v_mfma_scale_f32_16x16x128_f8f6f4 v[134:137], v[128:133], v[44:49], v[134:137], v179, v112 op_sel_hi:[0,0,0] cbsz:2 blgp:2
	v_mfma_scale_f32_16x16x128_f8f6f4 v[138:141], v[128:133], v[20:25], v[138:141], v178, v112 op_sel_hi:[0,0,0] cbsz:2 blgp:2
	v_mfma_scale_f32_16x16x128_f8f6f4 v[138:141], v[128:133], v[56:61], v[138:141], v179, v112 op_sel_hi:[0,0,0] cbsz:2 blgp:2
	v_mfma_scale_f32_16x16x128_f8f6f4 v[142:145], v[128:133], v[32:37], v[142:145], v178, v112 op_sel_hi:[0,0,0] cbsz:2 blgp:2
	v_mfma_scale_f32_16x16x128_f8f6f4 v[142:145], v[128:133], v[68:73], v[142:145], v179, v112 op_sel_hi:[0,0,0] cbsz:2 blgp:2
	v_fma_mix_f32 v158, v134, v100, v146 op_sel_hi:[0,0,1]
	v_exp_f32_e32 v158, v158
	v_fma_mix_f32 v159, v138, v101, v150 op_sel_hi:[0,0,1]
	v_exp_f32_e32 v159, v159
	v_fma_f32 v158, v158, v186, v186
	v_rcp_f32_e32 v158, v158
	v_add_f32_e32 v159, 1.0, v159
	v_rcp_f32_e32 v159, v159
	s_nop 0
	v_fma_mix_f32 v161, v158, v142, v154 op_sel_hi:[0,0,1]
	v_exp_f32_e32 v161, v161
	s_add_u32 s48, s48, s40
	v_add_f32_e32 v161, 1.0, v161
	v_rcp_f32_e32 v161, v161
	s_addc_u32 s49, s49, s41
	v_fma_f32 v162, v161, -2.0, 1.0
	v_sub_f32_e32 v163, v176, v162
	v_fma_f32 v176, v159, v163, v162
	v_fma_f32 v164, |v176|, s17, v113
	v_fma_f32 v165, |v176|, s18, v114
	v_fma_f32 v166, |v176|, s19, v115
	v_lshrrev_b32_e32 v167, 26, v176
	v_min3_u32 v164, v164, v165, v166
	v_bfi_b32 v168, 31, v164, v167
	v_lshrrev_b32_e32 v169, v181, v168
	global_store_short_d16_hi v185, v176, s[48:49]
	v_mul_u32_u24_dpp v170, v168, v180 quad_perm:[1,2,3,3] row_mask:0xf bank_mask:0xf bound_ctrl:1
	v_or_b32_e32 v171, v169, v170
	ds_write_b8 v184, v171 offset:416
	s_barrier
	ds_read_b64 v[122:123], v105 offset:416
	ds_read_b64 v[124:125], v105 offset:424
	ds_read_b64 v[126:127], v105 offset:432
	s_waitcnt lgkmcnt(3)
	s_barrier
	ds_read_b64 v[128:129], v105 offset:512
	ds_read_b64 v[130:131], v105 offset:520
	ds_read_b64 v[132:133], v105 offset:528
	s_waitcnt lgkmcnt(3)
	v_mfma_scale_f32_16x16x128_f8f6f4 v[134:137], v[122:127], v[2:7], 0, v178, v112 op_sel_hi:[0,0,0] cbsz:2 blgp:2
	v_mfma_scale_f32_16x16x128_f8f6f4 v[138:141], v[122:127], v[14:19], 0, v178, v112 op_sel_hi:[0,0,0] cbsz:2 blgp:2
	v_mfma_scale_f32_16x16x128_f8f6f4 v[142:145], v[122:127], v[26:31], v[188:191], v178, v112 op_sel_hi:[0,0,0] cbsz:2 blgp:2
	v_mfma_scale_f32_16x16x128_f8f6f4 v[134:137], v[122:127], v[38:43], v[134:137], v179, v112 op_sel_hi:[0,0,0] cbsz:2 blgp:2
	v_mfma_scale_f32_16x16x128_f8f6f4 v[138:141], v[122:127], v[50:55], v[138:141], v179, v112 op_sel_hi:[0,0,0] cbsz:2 blgp:2
	v_mfma_scale_f32_16x16x128_f8f6f4 v[142:145], v[122:127], v[62:67], v[142:145], v179, v112 op_sel_hi:[0,0,0] cbsz:2 blgp:2
	s_waitcnt lgkmcnt(0)
	v_mfma_scale_f32_16x16x128_f8f6f4 v[134:137], v[128:133], v[8:13], v[134:137], v178, v112 op_sel_hi:[0,0,0] cbsz:2 blgp:2
	v_mfma_scale_f32_16x16x128_f8f6f4 v[134:137], v[128:133], v[44:49], v[134:137], v179, v112 op_sel_hi:[0,0,0] cbsz:2 blgp:2
	v_mfma_scale_f32_16x16x128_f8f6f4 v[138:141], v[128:133], v[20:25], v[138:141], v178, v112 op_sel_hi:[0,0,0] cbsz:2 blgp:2
	v_mfma_scale_f32_16x16x128_f8f6f4 v[138:141], v[128:133], v[56:61], v[138:141], v179, v112 op_sel_hi:[0,0,0] cbsz:2 blgp:2
	v_mfma_scale_f32_16x16x128_f8f6f4 v[142:145], v[128:133], v[32:37], v[142:145], v178, v112 op_sel_hi:[0,0,0] cbsz:2 blgp:2
	v_mfma_scale_f32_16x16x128_f8f6f4 v[142:145], v[128:133], v[68:73], v[142:145], v179, v112 op_sel_hi:[0,0,0] cbsz:2 blgp:2
	v_fma_mix_f32 v158, v134, v100, v146 op_sel:[0,0,1] op_sel_hi:[0,0,1]
	v_exp_f32_e32 v158, v158
	v_fma_mix_f32 v159, v138, v101, v150 op_sel:[0,0,1] op_sel_hi:[0,0,1]
	v_exp_f32_e32 v159, v159
	v_fma_f32 v158, v158, v186, v186
	v_rcp_f32_e32 v158, v158
	v_add_f32_e32 v159, 1.0, v159
	v_rcp_f32_e32 v159, v159
	s_nop 0
	v_fma_mix_f32 v161, v158, v142, v154 op_sel:[0,0,1] op_sel_hi:[0,0,1]
	v_exp_f32_e32 v161, v161
	s_add_u32 s48, s48, s40
	v_add_f32_e32 v161, 1.0, v161
	v_rcp_f32_e32 v161, v161
	s_addc_u32 s49, s49, s41
	v_fma_f32 v162, v161, -2.0, 1.0
	v_sub_f32_e32 v163, v176, v162
	v_fma_f32 v176, v159, v163, v162
	v_fma_f32 v164, |v176|, s17, v113
	v_fma_f32 v165, |v176|, s18, v114
	v_fma_f32 v166, |v176|, s19, v115
	v_lshrrev_b32_e32 v167, 26, v176
	v_min3_u32 v164, v164, v165, v166
	v_bfi_b32 v168, 31, v164, v167
	v_lshrrev_b32_e32 v169, v181, v168
	global_store_short_d16_hi v185, v176, s[48:49]
	v_mul_u32_u24_dpp v170, v168, v180 quad_perm:[1,2,3,3] row_mask:0xf bank_mask:0xf bound_ctrl:1
	v_or_b32_e32 v171, v169, v170
	ds_write_b8 v184, v171
	s_barrier
	ds_read_b64 v[122:123], v105 offset:0
	ds_read_b64 v[124:125], v105 offset:8
	ds_read_b64 v[126:127], v105 offset:16
	s_waitcnt lgkmcnt(3)
	s_barrier
	ds_read_b64 v[128:129], v105 offset:96
	ds_read_b64 v[130:131], v105 offset:104
	ds_read_b64 v[132:133], v105 offset:112
	s_waitcnt lgkmcnt(3)
	v_mfma_scale_f32_16x16x128_f8f6f4 v[134:137], v[122:127], v[2:7], 0, v178, v112 op_sel_hi:[0,0,0] cbsz:2 blgp:2
	v_mfma_scale_f32_16x16x128_f8f6f4 v[138:141], v[122:127], v[14:19], 0, v178, v112 op_sel_hi:[0,0,0] cbsz:2 blgp:2
	v_mfma_scale_f32_16x16x128_f8f6f4 v[142:145], v[122:127], v[26:31], v[188:191], v178, v112 op_sel_hi:[0,0,0] cbsz:2 blgp:2
	v_mfma_scale_f32_16x16x128_f8f6f4 v[134:137], v[122:127], v[38:43], v[134:137], v179, v112 op_sel_hi:[0,0,0] cbsz:2 blgp:2
	v_mfma_scale_f32_16x16x128_f8f6f4 v[138:141], v[122:127], v[50:55], v[138:141], v179, v112 op_sel_hi:[0,0,0] cbsz:2 blgp:2
	v_mfma_scale_f32_16x16x128_f8f6f4 v[142:145], v[122:127], v[62:67], v[142:145], v179, v112 op_sel_hi:[0,0,0] cbsz:2 blgp:2
	s_waitcnt lgkmcnt(0)
	v_mfma_scale_f32_16x16x128_f8f6f4 v[134:137], v[128:133], v[8:13], v[134:137], v178, v112 op_sel_hi:[0,0,0] cbsz:2 blgp:2
	v_mfma_scale_f32_16x16x128_f8f6f4 v[134:137], v[128:133], v[44:49], v[134:137], v179, v112 op_sel_hi:[0,0,0] cbsz:2 blgp:2
	v_mfma_scale_f32_16x16x128_f8f6f4 v[138:141], v[128:133], v[20:25], v[138:141], v178, v112 op_sel_hi:[0,0,0] cbsz:2 blgp:2
	v_mfma_scale_f32_16x16x128_f8f6f4 v[138:141], v[128:133], v[56:61], v[138:141], v179, v112 op_sel_hi:[0,0,0] cbsz:2 blgp:2
	v_mfma_scale_f32_16x16x128_f8f6f4 v[142:145], v[128:133], v[32:37], v[142:145], v178, v112 op_sel_hi:[0,0,0] cbsz:2 blgp:2
	v_mfma_scale_f32_16x16x128_f8f6f4 v[142:145], v[128:133], v[68:73], v[142:145], v179, v112 op_sel_hi:[0,0,0] cbsz:2 blgp:2
	v_fma_mix_f32 v158, v134, v100, v147 op_sel_hi:[0,0,1]
	v_exp_f32_e32 v158, v158
	v_fma_mix_f32 v159, v138, v101, v151 op_sel_hi:[0,0,1]
	v_exp_f32_e32 v159, v159
	v_fma_f32 v158, v158, v186, v186
	v_rcp_f32_e32 v158, v158
	v_add_f32_e32 v159, 1.0, v159
	v_rcp_f32_e32 v159, v159
	s_nop 0
	v_fma_mix_f32 v161, v158, v142, v155 op_sel_hi:[0,0,1]
	v_exp_f32_e32 v161, v161
	s_add_u32 s48, s48, s40
	v_add_f32_e32 v161, 1.0, v161
	v_rcp_f32_e32 v161, v161
	s_addc_u32 s49, s49, s41
	v_fma_f32 v162, v161, -2.0, 1.0
	v_sub_f32_e32 v163, v176, v162
	v_fma_f32 v176, v159, v163, v162
	v_fma_f32 v164, |v176|, s17, v113
	v_fma_f32 v165, |v176|, s18, v114
	v_fma_f32 v166, |v176|, s19, v115
	v_lshrrev_b32_e32 v167, 26, v176
	v_min3_u32 v164, v164, v165, v166
	v_bfi_b32 v168, 31, v164, v167
	v_lshrrev_b32_e32 v169, v181, v168
	global_store_short_d16_hi v185, v176, s[48:49]
	v_mul_u32_u24_dpp v170, v168, v180 quad_perm:[1,2,3,3] row_mask:0xf bank_mask:0xf bound_ctrl:1
	v_or_b32_e32 v171, v169, v170
	ds_write_b8 v184, v171 offset:416
	s_barrier
	ds_read_b64 v[122:123], v105 offset:416
	ds_read_b64 v[124:125], v105 offset:424
	ds_read_b64 v[126:127], v105 offset:432
	s_waitcnt lgkmcnt(3)
	s_barrier
	ds_read_b64 v[128:129], v105 offset:512
	ds_read_b64 v[130:131], v105 offset:520
	ds_read_b64 v[132:133], v105 offset:528
	s_waitcnt lgkmcnt(3)
	v_mfma_scale_f32_16x16x128_f8f6f4 v[134:137], v[122:127], v[2:7], 0, v178, v112 op_sel_hi:[0,0,0] cbsz:2 blgp:2
	v_mfma_scale_f32_16x16x128_f8f6f4 v[138:141], v[122:127], v[14:19], 0, v178, v112 op_sel_hi:[0,0,0] cbsz:2 blgp:2
	v_mfma_scale_f32_16x16x128_f8f6f4 v[142:145], v[122:127], v[26:31], v[188:191], v178, v112 op_sel_hi:[0,0,0] cbsz:2 blgp:2
	v_mfma_scale_f32_16x16x128_f8f6f4 v[134:137], v[122:127], v[38:43], v[134:137], v179, v112 op_sel_hi:[0,0,0] cbsz:2 blgp:2
	v_mfma_scale_f32_16x16x128_f8f6f4 v[138:141], v[122:127], v[50:55], v[138:141], v179, v112 op_sel_hi:[0,0,0] cbsz:2 blgp:2
	v_mfma_scale_f32_16x16x128_f8f6f4 v[142:145], v[122:127], v[62:67], v[142:145], v179, v112 op_sel_hi:[0,0,0] cbsz:2 blgp:2
	s_waitcnt lgkmcnt(0)
	v_mfma_scale_f32_16x16x128_f8f6f4 v[134:137], v[128:133], v[8:13], v[134:137], v178, v112 op_sel_hi:[0,0,0] cbsz:2 blgp:2
	v_mfma_scale_f32_16x16x128_f8f6f4 v[134:137], v[128:133], v[44:49], v[134:137], v179, v112 op_sel_hi:[0,0,0] cbsz:2 blgp:2
	v_mfma_scale_f32_16x16x128_f8f6f4 v[138:141], v[128:133], v[20:25], v[138:141], v178, v112 op_sel_hi:[0,0,0] cbsz:2 blgp:2
	v_mfma_scale_f32_16x16x128_f8f6f4 v[138:141], v[128:133], v[56:61], v[138:141], v179, v112 op_sel_hi:[0,0,0] cbsz:2 blgp:2
	v_mfma_scale_f32_16x16x128_f8f6f4 v[142:145], v[128:133], v[32:37], v[142:145], v178, v112 op_sel_hi:[0,0,0] cbsz:2 blgp:2
	v_mfma_scale_f32_16x16x128_f8f6f4 v[142:145], v[128:133], v[68:73], v[142:145], v179, v112 op_sel_hi:[0,0,0] cbsz:2 blgp:2
	v_fma_mix_f32 v158, v134, v100, v147 op_sel:[0,0,1] op_sel_hi:[0,0,1]
	v_exp_f32_e32 v158, v158
	v_fma_mix_f32 v159, v138, v101, v151 op_sel:[0,0,1] op_sel_hi:[0,0,1]
	v_exp_f32_e32 v159, v159
	v_fma_f32 v158, v158, v186, v186
	v_rcp_f32_e32 v158, v158
	v_add_f32_e32 v159, 1.0, v159
	v_rcp_f32_e32 v159, v159
	s_nop 0
	v_fma_mix_f32 v161, v158, v142, v155 op_sel:[0,0,1] op_sel_hi:[0,0,1]
	v_exp_f32_e32 v161, v161
	s_add_u32 s48, s48, s40
	v_add_f32_e32 v161, 1.0, v161
	v_rcp_f32_e32 v161, v161
	s_addc_u32 s49, s49, s41
	v_fma_f32 v162, v161, -2.0, 1.0
	v_sub_f32_e32 v163, v176, v162
	v_fma_f32 v176, v159, v163, v162
	v_fma_f32 v164, |v176|, s17, v113
	v_fma_f32 v165, |v176|, s18, v114
	v_fma_f32 v166, |v176|, s19, v115
	v_lshrrev_b32_e32 v167, 26, v176
	v_min3_u32 v164, v164, v165, v166
	v_bfi_b32 v168, 31, v164, v167
	v_lshrrev_b32_e32 v169, v181, v168
	global_store_short_d16_hi v185, v176, s[48:49]
	v_mul_u32_u24_dpp v170, v168, v180 quad_perm:[1,2,3,3] row_mask:0xf bank_mask:0xf bound_ctrl:1
	v_or_b32_e32 v171, v169, v170
	ds_write_b8 v184, v171
	s_barrier
	ds_read_b64 v[122:123], v105 offset:0
	ds_read_b64 v[124:125], v105 offset:8
	ds_read_b64 v[126:127], v105 offset:16
	s_waitcnt lgkmcnt(3)
	s_barrier
	ds_read_b64 v[128:129], v105 offset:96
	ds_read_b64 v[130:131], v105 offset:104
	ds_read_b64 v[132:133], v105 offset:112
	s_waitcnt lgkmcnt(3)
	v_mfma_scale_f32_16x16x128_f8f6f4 v[134:137], v[122:127], v[2:7], 0, v178, v112 op_sel_hi:[0,0,0] cbsz:2 blgp:2
	v_mfma_scale_f32_16x16x128_f8f6f4 v[138:141], v[122:127], v[14:19], 0, v178, v112 op_sel_hi:[0,0,0] cbsz:2 blgp:2
	v_mfma_scale_f32_16x16x128_f8f6f4 v[142:145], v[122:127], v[26:31], v[188:191], v178, v112 op_sel_hi:[0,0,0] cbsz:2 blgp:2
	v_mfma_scale_f32_16x16x128_f8f6f4 v[134:137], v[122:127], v[38:43], v[134:137], v179, v112 op_sel_hi:[0,0,0] cbsz:2 blgp:2
	v_mfma_scale_f32_16x16x128_f8f6f4 v[138:141], v[122:127], v[50:55], v[138:141], v179, v112 op_sel_hi:[0,0,0] cbsz:2 blgp:2
	v_mfma_scale_f32_16x16x128_f8f6f4 v[142:145], v[122:127], v[62:67], v[142:145], v179, v112 op_sel_hi:[0,0,0] cbsz:2 blgp:2
	s_waitcnt lgkmcnt(0)
	v_mfma_scale_f32_16x16x128_f8f6f4 v[134:137], v[128:133], v[8:13], v[134:137], v178, v112 op_sel_hi:[0,0,0] cbsz:2 blgp:2
	v_mfma_scale_f32_16x16x128_f8f6f4 v[134:137], v[128:133], v[44:49], v[134:137], v179, v112 op_sel_hi:[0,0,0] cbsz:2 blgp:2
	v_mfma_scale_f32_16x16x128_f8f6f4 v[138:141], v[128:133], v[20:25], v[138:141], v178, v112 op_sel_hi:[0,0,0] cbsz:2 blgp:2
	v_mfma_scale_f32_16x16x128_f8f6f4 v[138:141], v[128:133], v[56:61], v[138:141], v179, v112 op_sel_hi:[0,0,0] cbsz:2 blgp:2
	v_mfma_scale_f32_16x16x128_f8f6f4 v[142:145], v[128:133], v[32:37], v[142:145], v178, v112 op_sel_hi:[0,0,0] cbsz:2 blgp:2
	v_mfma_scale_f32_16x16x128_f8f6f4 v[142:145], v[128:133], v[68:73], v[142:145], v179, v112 op_sel_hi:[0,0,0] cbsz:2 blgp:2
	v_fma_mix_f32 v158, v134, v100, v148 op_sel_hi:[0,0,1]
	v_exp_f32_e32 v158, v158
	v_fma_mix_f32 v159, v138, v101, v152 op_sel_hi:[0,0,1]
	v_exp_f32_e32 v159, v159
	v_fma_f32 v158, v158, v186, v186
	v_rcp_f32_e32 v158, v158
	v_add_f32_e32 v159, 1.0, v159
	v_rcp_f32_e32 v159, v159
	s_nop 0
	v_fma_mix_f32 v161, v158, v142, v156 op_sel_hi:[0,0,1]
	v_exp_f32_e32 v161, v161
	s_add_u32 s48, s48, s40
	v_add_f32_e32 v161, 1.0, v161
	v_rcp_f32_e32 v161, v161
	s_addc_u32 s49, s49, s41
	v_fma_f32 v162, v161, -2.0, 1.0
	v_sub_f32_e32 v163, v176, v162
	v_fma_f32 v176, v159, v163, v162
	v_fma_f32 v164, |v176|, s17, v113
	v_fma_f32 v165, |v176|, s18, v114
	v_fma_f32 v166, |v176|, s19, v115
	v_lshrrev_b32_e32 v167, 26, v176
	v_min3_u32 v164, v164, v165, v166
	v_bfi_b32 v168, 31, v164, v167
	v_lshrrev_b32_e32 v169, v181, v168
	global_store_short_d16_hi v185, v176, s[48:49]
	v_mul_u32_u24_dpp v170, v168, v180 quad_perm:[1,2,3,3] row_mask:0xf bank_mask:0xf bound_ctrl:1
	v_or_b32_e32 v171, v169, v170
	ds_write_b8 v184, v171 offset:416
	s_barrier
	ds_read_b64 v[122:123], v105 offset:416
	ds_read_b64 v[124:125], v105 offset:424
	ds_read_b64 v[126:127], v105 offset:432
	s_waitcnt lgkmcnt(3)
	s_barrier
	ds_read_b64 v[128:129], v105 offset:512
	ds_read_b64 v[130:131], v105 offset:520
	ds_read_b64 v[132:133], v105 offset:528
	s_waitcnt lgkmcnt(3)
	v_mfma_scale_f32_16x16x128_f8f6f4 v[134:137], v[122:127], v[2:7], 0, v178, v112 op_sel_hi:[0,0,0] cbsz:2 blgp:2
	v_mfma_scale_f32_16x16x128_f8f6f4 v[138:141], v[122:127], v[14:19], 0, v178, v112 op_sel_hi:[0,0,0] cbsz:2 blgp:2
	v_mfma_scale_f32_16x16x128_f8f6f4 v[142:145], v[122:127], v[26:31], v[188:191], v178, v112 op_sel_hi:[0,0,0] cbsz:2 blgp:2
	v_mfma_scale_f32_16x16x128_f8f6f4 v[134:137], v[122:127], v[38:43], v[134:137], v179, v112 op_sel_hi:[0,0,0] cbsz:2 blgp:2
	v_mfma_scale_f32_16x16x128_f8f6f4 v[138:141], v[122:127], v[50:55], v[138:141], v179, v112 op_sel_hi:[0,0,0] cbsz:2 blgp:2
	v_mfma_scale_f32_16x16x128_f8f6f4 v[142:145], v[122:127], v[62:67], v[142:145], v179, v112 op_sel_hi:[0,0,0] cbsz:2 blgp:2
	s_waitcnt lgkmcnt(0)
	v_mfma_scale_f32_16x16x128_f8f6f4 v[134:137], v[128:133], v[8:13], v[134:137], v178, v112 op_sel_hi:[0,0,0] cbsz:2 blgp:2
	v_mfma_scale_f32_16x16x128_f8f6f4 v[134:137], v[128:133], v[44:49], v[134:137], v179, v112 op_sel_hi:[0,0,0] cbsz:2 blgp:2
	v_mfma_scale_f32_16x16x128_f8f6f4 v[138:141], v[128:133], v[20:25], v[138:141], v178, v112 op_sel_hi:[0,0,0] cbsz:2 blgp:2
	v_mfma_scale_f32_16x16x128_f8f6f4 v[138:141], v[128:133], v[56:61], v[138:141], v179, v112 op_sel_hi:[0,0,0] cbsz:2 blgp:2
	v_mfma_scale_f32_16x16x128_f8f6f4 v[142:145], v[128:133], v[32:37], v[142:145], v178, v112 op_sel_hi:[0,0,0] cbsz:2 blgp:2
	v_mfma_scale_f32_16x16x128_f8f6f4 v[142:145], v[128:133], v[68:73], v[142:145], v179, v112 op_sel_hi:[0,0,0] cbsz:2 blgp:2
	v_fma_mix_f32 v158, v134, v100, v148 op_sel:[0,0,1] op_sel_hi:[0,0,1]
	v_exp_f32_e32 v158, v158
	v_fma_mix_f32 v159, v138, v101, v152 op_sel:[0,0,1] op_sel_hi:[0,0,1]
	v_exp_f32_e32 v159, v159
	v_fma_f32 v158, v158, v186, v186
	v_rcp_f32_e32 v158, v158
	v_add_f32_e32 v159, 1.0, v159
	v_rcp_f32_e32 v159, v159
	s_nop 0
	v_fma_mix_f32 v161, v158, v142, v156 op_sel:[0,0,1] op_sel_hi:[0,0,1]
	v_exp_f32_e32 v161, v161
	s_add_u32 s48, s48, s40
	v_add_f32_e32 v161, 1.0, v161
	v_rcp_f32_e32 v161, v161
	s_addc_u32 s49, s49, s41
	v_fma_f32 v162, v161, -2.0, 1.0
	v_sub_f32_e32 v163, v176, v162
	v_fma_f32 v176, v159, v163, v162
	v_fma_f32 v164, |v176|, s17, v113
	v_fma_f32 v165, |v176|, s18, v114
	v_fma_f32 v166, |v176|, s19, v115
	v_lshrrev_b32_e32 v167, 26, v176
	v_min3_u32 v164, v164, v165, v166
	v_bfi_b32 v168, 31, v164, v167
	v_lshrrev_b32_e32 v169, v181, v168
	global_store_short_d16_hi v185, v176, s[48:49]
	v_mul_u32_u24_dpp v170, v168, v180 quad_perm:[1,2,3,3] row_mask:0xf bank_mask:0xf bound_ctrl:1
	v_or_b32_e32 v171, v169, v170
	ds_write_b8 v184, v171
	s_barrier
	ds_read_b64 v[122:123], v105 offset:0
	ds_read_b64 v[124:125], v105 offset:8
	ds_read_b64 v[126:127], v105 offset:16
	s_waitcnt lgkmcnt(3)
	s_barrier
	ds_read_b64 v[128:129], v105 offset:96
	ds_read_b64 v[130:131], v105 offset:104
	ds_read_b64 v[132:133], v105 offset:112
	s_waitcnt lgkmcnt(3)
	v_mfma_scale_f32_16x16x128_f8f6f4 v[134:137], v[122:127], v[2:7], 0, v178, v112 op_sel_hi:[0,0,0] cbsz:2 blgp:2
	v_mfma_scale_f32_16x16x128_f8f6f4 v[138:141], v[122:127], v[14:19], 0, v178, v112 op_sel_hi:[0,0,0] cbsz:2 blgp:2
	v_mfma_scale_f32_16x16x128_f8f6f4 v[142:145], v[122:127], v[26:31], v[188:191], v178, v112 op_sel_hi:[0,0,0] cbsz:2 blgp:2
	v_mfma_scale_f32_16x16x128_f8f6f4 v[134:137], v[122:127], v[38:43], v[134:137], v179, v112 op_sel_hi:[0,0,0] cbsz:2 blgp:2
	v_mfma_scale_f32_16x16x128_f8f6f4 v[138:141], v[122:127], v[50:55], v[138:141], v179, v112 op_sel_hi:[0,0,0] cbsz:2 blgp:2
	v_mfma_scale_f32_16x16x128_f8f6f4 v[142:145], v[122:127], v[62:67], v[142:145], v179, v112 op_sel_hi:[0,0,0] cbsz:2 blgp:2
	s_waitcnt lgkmcnt(0)
	v_mfma_scale_f32_16x16x128_f8f6f4 v[134:137], v[128:133], v[8:13], v[134:137], v178, v112 op_sel_hi:[0,0,0] cbsz:2 blgp:2
	v_mfma_scale_f32_16x16x128_f8f6f4 v[134:137], v[128:133], v[44:49], v[134:137], v179, v112 op_sel_hi:[0,0,0] cbsz:2 blgp:2
	v_mfma_scale_f32_16x16x128_f8f6f4 v[138:141], v[128:133], v[20:25], v[138:141], v178, v112 op_sel_hi:[0,0,0] cbsz:2 blgp:2
	v_mfma_scale_f32_16x16x128_f8f6f4 v[138:141], v[128:133], v[56:61], v[138:141], v179, v112 op_sel_hi:[0,0,0] cbsz:2 blgp:2
	v_mfma_scale_f32_16x16x128_f8f6f4 v[142:145], v[128:133], v[32:37], v[142:145], v178, v112 op_sel_hi:[0,0,0] cbsz:2 blgp:2
	v_mfma_scale_f32_16x16x128_f8f6f4 v[142:145], v[128:133], v[68:73], v[142:145], v179, v112 op_sel_hi:[0,0,0] cbsz:2 blgp:2
	v_fma_mix_f32 v158, v134, v100, v149 op_sel_hi:[0,0,1]
	v_exp_f32_e32 v158, v158
	v_fma_mix_f32 v159, v138, v101, v153 op_sel_hi:[0,0,1]
	v_exp_f32_e32 v159, v159
	v_fma_f32 v158, v158, v186, v186
	v_rcp_f32_e32 v158, v158
	v_add_f32_e32 v159, 1.0, v159
	v_rcp_f32_e32 v159, v159
	s_nop 0
	v_fma_mix_f32 v161, v158, v142, v157 op_sel_hi:[0,0,1]
	v_exp_f32_e32 v161, v161
	s_add_u32 s48, s48, s40
	v_add_f32_e32 v161, 1.0, v161
	v_rcp_f32_e32 v161, v161
	s_addc_u32 s49, s49, s41
	v_fma_f32 v162, v161, -2.0, 1.0
	v_sub_f32_e32 v163, v176, v162
	v_fma_f32 v176, v159, v163, v162
	v_fma_f32 v164, |v176|, s17, v113
	v_fma_f32 v165, |v176|, s18, v114
	v_fma_f32 v166, |v176|, s19, v115
	v_lshrrev_b32_e32 v167, 26, v176
	v_min3_u32 v164, v164, v165, v166
	v_bfi_b32 v168, 31, v164, v167
	v_lshrrev_b32_e32 v169, v181, v168
	global_store_short_d16_hi v185, v176, s[48:49]
	v_mul_u32_u24_dpp v170, v168, v180 quad_perm:[1,2,3,3] row_mask:0xf bank_mask:0xf bound_ctrl:1
	v_or_b32_e32 v171, v169, v170
	ds_write_b8 v184, v171 offset:416
	s_barrier
	ds_read_b64 v[122:123], v105 offset:416
	ds_read_b64 v[124:125], v105 offset:424
	ds_read_b64 v[126:127], v105 offset:432
	s_waitcnt lgkmcnt(3)
	s_barrier
	ds_read_b64 v[128:129], v105 offset:512
	ds_read_b64 v[130:131], v105 offset:520
	ds_read_b64 v[132:133], v105 offset:528
	s_add_i32 s44, s44, 16
	s_waitcnt lgkmcnt(3)
	v_mfma_scale_f32_16x16x128_f8f6f4 v[134:137], v[122:127], v[2:7], 0, v178, v112 op_sel_hi:[0,0,0] cbsz:2 blgp:2
	v_mfma_scale_f32_16x16x128_f8f6f4 v[138:141], v[122:127], v[14:19], 0, v178, v112 op_sel_hi:[0,0,0] cbsz:2 blgp:2
	v_mfma_scale_f32_16x16x128_f8f6f4 v[142:145], v[122:127], v[26:31], v[188:191], v178, v112 op_sel_hi:[0,0,0] cbsz:2 blgp:2
	v_mfma_scale_f32_16x16x128_f8f6f4 v[134:137], v[122:127], v[38:43], v[134:137], v179, v112 op_sel_hi:[0,0,0] cbsz:2 blgp:2
	v_mfma_scale_f32_16x16x128_f8f6f4 v[138:141], v[122:127], v[50:55], v[138:141], v179, v112 op_sel_hi:[0,0,0] cbsz:2 blgp:2
	v_mfma_scale_f32_16x16x128_f8f6f4 v[142:145], v[122:127], v[62:67], v[142:145], v179, v112 op_sel_hi:[0,0,0] cbsz:2 blgp:2
	s_waitcnt lgkmcnt(0)
	v_mfma_scale_f32_16x16x128_f8f6f4 v[134:137], v[128:133], v[8:13], v[134:137], v178, v112 op_sel_hi:[0,0,0] cbsz:2 blgp:2
	v_mfma_scale_f32_16x16x128_f8f6f4 v[134:137], v[128:133], v[44:49], v[134:137], v179, v112 op_sel_hi:[0,0,0] cbsz:2 blgp:2
	v_mfma_scale_f32_16x16x128_f8f6f4 v[138:141], v[128:133], v[20:25], v[138:141], v178, v112 op_sel_hi:[0,0,0] cbsz:2 blgp:2
	v_mfma_scale_f32_16x16x128_f8f6f4 v[138:141], v[128:133], v[56:61], v[138:141], v179, v112 op_sel_hi:[0,0,0] cbsz:2 blgp:2
	v_mfma_scale_f32_16x16x128_f8f6f4 v[142:145], v[128:133], v[32:37], v[142:145], v178, v112 op_sel_hi:[0,0,0] cbsz:2 blgp:2
	v_mfma_scale_f32_16x16x128_f8f6f4 v[142:145], v[128:133], v[68:73], v[142:145], v179, v112 op_sel_hi:[0,0,0] cbsz:2 blgp:2
	v_fma_mix_f32 v158, v134, v100, v149 op_sel:[0,0,1] op_sel_hi:[0,0,1]
	v_exp_f32_e32 v158, v158
	v_fma_mix_f32 v159, v138, v101, v153 op_sel:[0,0,1] op_sel_hi:[0,0,1]
	v_exp_f32_e32 v159, v159
	v_fma_f32 v158, v158, v186, v186
	v_rcp_f32_e32 v158, v158
	v_add_f32_e32 v159, 1.0, v159
	v_rcp_f32_e32 v159, v159
	s_nop 0
	v_fma_mix_f32 v161, v158, v142, v157 op_sel:[0,0,1] op_sel_hi:[0,0,1]
	v_exp_f32_e32 v161, v161
	s_add_u32 s48, s48, s40
	v_add_f32_e32 v161, 1.0, v161
	v_rcp_f32_e32 v161, v161
	s_addc_u32 s49, s49, s41
	v_fma_f32 v162, v161, -2.0, 1.0
	v_sub_f32_e32 v163, v176, v162
	v_fma_f32 v176, v159, v163, v162
	v_fma_f32 v164, |v176|, s17, v113
	v_fma_f32 v165, |v176|, s18, v114
	v_fma_f32 v166, |v176|, s19, v115
	v_lshrrev_b32_e32 v167, 26, v176
	v_min3_u32 v164, v164, v165, v166
	v_bfi_b32 v168, 31, v164, v167
	v_lshrrev_b32_e32 v169, v181, v168
	global_store_short_d16_hi v185, v176, s[48:49]
	v_mul_u32_u24_dpp v170, v168, v180 quad_perm:[1,2,3,3] row_mask:0xf bank_mask:0xf bound_ctrl:1
	v_or_b32_e32 v171, v169, v170
	ds_write_b8 v184, v171
	s_barrier
	ds_read_b64 v[122:123], v105 offset:0
	ds_read_b64 v[124:125], v105 offset:8
	ds_read_b64 v[126:127], v105 offset:16
	s_cmp_lt_i32 s44, s45
	s_waitcnt lgkmcnt(3)
	s_barrier
	s_cbranch_scc1 .Lscan_loop_b_f2
